# k_g + GEMM K-loops: load-segment half runs at prio 2 (s_setprio 2 at end of each MFMA segment)
# speedup vs baseline: 1.0029x; 1.0029x over previous
; #define PG8_STAGE(bufoff, gbase, voff) do { _Pragma("unroll") for (int _i = 0; _i < 2; ++_i) \
;         __builtin_amdgcn_global_load_lds((const unsigned*)((const char*)(gbase) + (voff)[_i]), (PG8_LAS unsigned*)(lds + (bufoff) + ldsw + _i * 8192), 16, 0, 0); } while (0)
; #define PG8_WAIT_V(n) asm volatile("s_waitcnt vmcnt(" #n ")" ::: "memory")
; #define PG8_WAIT_L(n) asm volatile("s_waitcnt lgkmcnt(" #n ")" ::: "memory")
; #define PG8_BAR __builtin_amdgcn_s_barrier()
; #define PG8_SCHED __builtin_amdgcn_sched_barrier(0)
; template <class Epi, class Sched, bool ALIGN_EPI = false, bool SP2 = false, bool F8 = false>
; __device__ __forceinline__ void gemm_phase(PG8_LAS unsigned char* lds, const Gemm g, const Sched& S, const Epi& E, const int tidb  ) {
;     ...
;             if constexpr (SP2) {
;             PG8_LDB(B0, 0, 0); PG8_LDB(B1, 0, 1); PG8_SCHED; PG8_LDA(At, 0, 0); PG8_STAGE(PG8_SA(1, 1), a1 + hstep, voffA);
;             PG8_WAIT_V(8); PG8_WAIT_L(0); PG8_BAR; PG8_MMA(0, 0, At, B0); PG8_MMA(0, 1, At, B1); PG8_BAR; PG8_SCHED;
;             PG8_LDA(At, 0, 1); PG8_STAGE(PG8_SB(0, 0), b2, voffB); PG8_STAGE(PG8_SB(0, 1), b2 + hstep, voffB); PG8_STAGE(PG8_SA(0, 0), a2, voffA);
;             PG8_WAIT_V(8); PG8_WAIT_L(0); PG8_BAR; PG8_MMA(1, 0, At, B0); PG8_MMA(1, 1, At, B1); PG8_BAR; PG8_SCHED;
.LBB0_51:
	s_add_i32 s14, s6, 2
	s_add_u32 s8, s4, 0x80
	s_addc_u32 s7, s5, 0
	s_add_i32 s15, 0, 0x10000
	s_cmp_eq_u32 s97, s6
	s_cselect_b32 s7, s73, s7
	s_cselect_b32 s6, s72, s8
	v_add_u32_e32 v0, s15, v190
	s_cselect_b32 s9, s53, s13
	s_cselect_b32 s8, s52, s12
	s_add_i32 s54, 0, 0x14000
	ds_read_b128 v[18:21], v0
	ds_read_b128 v[22:25], v0 offset:1024
	ds_read_b128 v[26:29], v0 offset:2048
	ds_read_b128 v[30:33], v0 offset:3072
	v_add_u32_e32 v0, s54, v190
	ds_read_b128 v[2:5], v0
	ds_read_b128 v[6:9], v0 offset:1024
	ds_read_b128 v[10:13], v0 offset:2048
	ds_read_b128 v[14:17], v0 offset:3072
	v_lshl_add_u64 v[184:185], s[4:5], 0, v[172:173]
	s_add_i32 m0, s43, 0xc000
	ds_read_b128 v[176:179], v191
	ds_read_b128 v[180:183], v191 offset:1024
	ds_read_b128 v[204:207], v191 offset:2048
	ds_read_b128 v[208:211], v191 offset:3072
	ds_read_b128 v[212:215], v191 offset:4096
	ds_read_b128 v[216:219], v191 offset:5120
	ds_read_b128 v[220:223], v191 offset:6144
	ds_read_b128 v[224:227], v191 offset:7168
	global_load_lds_dwordx4 v[184:185], off
	v_lshl_add_u64 v[184:185], s[4:5], 0, v[174:175]
	s_add_i32 m0, s43, 0xe000
	s_nop 0
	global_load_lds_dwordx4 v[184:185], off
	s_waitcnt vmcnt(8)
	s_waitcnt lgkmcnt(0)
	s_barrier
	s_setprio 1
	s_waitcnt lgkmcnt(0)
	v_mfma_scale_f32_16x16x128_f8f6f4 v[158:161], v[18:25], v[176:183], v[158:161], v246, v247 op_sel_hi:[0,0,0]
	v_mfma_scale_f32_16x16x128_f8f6f4 v[154:157], v[26:33], v[176:183], v[154:157], v246, v247 op_sel_hi:[0,0,0]
	v_mfma_scale_f32_16x16x128_f8f6f4 v[150:153], v[18:25], v[204:211], v[150:153], v246, v247 op_sel_hi:[0,0,0]
	v_mfma_scale_f32_16x16x128_f8f6f4 v[146:149], v[26:33], v[204:211], v[146:149], v246, v247 op_sel_hi:[0,0,0]
	v_mfma_scale_f32_16x16x128_f8f6f4 v[142:145], v[18:25], v[212:219], v[142:145], v246, v247 op_sel_hi:[0,0,0]
	v_mfma_scale_f32_16x16x128_f8f6f4 v[138:141], v[26:33], v[212:219], v[138:141], v246, v247 op_sel_hi:[0,0,0]
	v_mfma_scale_f32_16x16x128_f8f6f4 v[134:137], v[18:25], v[220:227], v[134:137], v246, v247 op_sel_hi:[0,0,0]
	v_mfma_scale_f32_16x16x128_f8f6f4 v[130:133], v[26:33], v[220:227], v[130:133], v246, v247 op_sel_hi:[0,0,0]
	s_setprio 0
	s_setprio 1
	v_mfma_scale_f32_16x16x128_f8f6f4 v[94:97], v[2:9], v[176:183], v[94:97], v246, v247 op_sel_hi:[0,0,0]
	v_mfma_scale_f32_16x16x128_f8f6f4 v[90:93], v[10:17], v[176:183], v[90:93], v246, v247 op_sel_hi:[0,0,0]
	v_mfma_scale_f32_16x16x128_f8f6f4 v[86:89], v[2:9], v[204:211], v[86:89], v246, v247 op_sel_hi:[0,0,0]
	v_mfma_scale_f32_16x16x128_f8f6f4 v[82:85], v[10:17], v[204:211], v[82:85], v246, v247 op_sel_hi:[0,0,0]
	v_mfma_scale_f32_16x16x128_f8f6f4 v[78:81], v[2:9], v[212:219], v[78:81], v246, v247 op_sel_hi:[0,0,0]
	v_mfma_scale_f32_16x16x128_f8f6f4 v[74:77], v[10:17], v[212:219], v[74:77], v246, v247 op_sel_hi:[0,0,0]
	v_mfma_scale_f32_16x16x128_f8f6f4 v[70:73], v[2:9], v[220:227], v[70:73], v246, v247 op_sel_hi:[0,0,0]
	v_mfma_scale_f32_16x16x128_f8f6f4 v[66:69], v[10:17], v[220:227], v[66:69], v246, v247 op_sel_hi:[0,0,0]
	s_setprio 2
	s_barrier
	s_add_i32 s15, s15, s41
	v_lshl_add_u64 v[176:177], s[8:9], 0, v[166:167]
	s_mov_b32 m0, s15
	ds_read_b128 v[204:207], v191 offset:16384
	ds_read_b128 v[208:211], v191 offset:17408
	ds_read_b128 v[212:215], v191 offset:18432
	ds_read_b128 v[216:219], v191 offset:19456
	ds_read_b128 v[220:223], v191 offset:20480
	ds_read_b128 v[224:227], v191 offset:21504
	ds_read_b128 v[228:231], v191 offset:22528
	ds_read_b128 v[232:235], v191 offset:23552
	global_load_lds_dwordx4 v[176:177], off
	s_add_i32 m0, s15, 0x2000
	v_lshl_add_u64 v[178:179], s[8:9], 0, v[170:171]
	s_add_u32 s8, s8, s20
	s_addc_u32 s9, s9, s21
	s_add_i32 s15, s54, s41
	global_load_lds_dwordx4 v[178:179], off
	v_lshl_add_u64 v[180:181], s[8:9], 0, v[166:167]
	s_mov_b32 m0, s15
	v_lshl_add_u64 v[182:183], s[8:9], 0, v[170:171]
	global_load_lds_dwordx4 v[180:181], off
	s_add_i32 m0, s15, 0x2000
	v_lshl_add_u64 v[184:185], s[6:7], 0, v[164:165]
	global_load_lds_dwordx4 v[182:183], off
	s_mov_b32 m0, s43
	v_lshl_add_u64 v[186:187], s[6:7], 0, v[168:169]
	global_load_lds_dwordx4 v[184:185], off
	s_mov_b32 m0, s66
	s_nop 0
	global_load_lds_dwordx4 v[186:187], off
	s_waitcnt vmcnt(8)
	s_waitcnt lgkmcnt(0)
	s_barrier
	s_setprio 1
	s_waitcnt lgkmcnt(0)
	v_mfma_scale_f32_16x16x128_f8f6f4 v[126:129], v[18:25], v[204:211], v[126:129], v246, v247 op_sel_hi:[0,0,0]
	v_mfma_scale_f32_16x16x128_f8f6f4 v[122:125], v[26:33], v[204:211], v[122:125], v246, v247 op_sel_hi:[0,0,0]
	v_mfma_scale_f32_16x16x128_f8f6f4 v[118:121], v[18:25], v[212:219], v[118:121], v246, v247 op_sel_hi:[0,0,0]
	v_mfma_scale_f32_16x16x128_f8f6f4 v[114:117], v[26:33], v[212:219], v[114:117], v246, v247 op_sel_hi:[0,0,0]
	v_mfma_scale_f32_16x16x128_f8f6f4 v[110:113], v[18:25], v[220:227], v[110:113], v246, v247 op_sel_hi:[0,0,0]
	v_mfma_scale_f32_16x16x128_f8f6f4 v[106:109], v[26:33], v[220:227], v[106:109], v246, v247 op_sel_hi:[0,0,0]
	v_mfma_scale_f32_16x16x128_f8f6f4 v[102:105], v[18:25], v[228:235], v[102:105], v246, v247 op_sel_hi:[0,0,0]
	v_mfma_scale_f32_16x16x128_f8f6f4 v[98:101], v[26:33], v[228:235], v[98:101], v246, v247 op_sel_hi:[0,0,0]
	s_setprio 0
	s_setprio 1
	v_mfma_scale_f32_16x16x128_f8f6f4 v[62:65], v[2:9], v[204:211], v[62:65], v246, v247 op_sel_hi:[0,0,0]
	v_mfma_scale_f32_16x16x128_f8f6f4 v[58:61], v[10:17], v[204:211], v[58:61], v246, v247 op_sel_hi:[0,0,0]
	v_mfma_scale_f32_16x16x128_f8f6f4 v[54:57], v[2:9], v[212:219], v[54:57], v246, v247 op_sel_hi:[0,0,0]
	v_mfma_scale_f32_16x16x128_f8f6f4 v[50:53], v[10:17], v[212:219], v[50:53], v246, v247 op_sel_hi:[0,0,0]
	v_mfma_scale_f32_16x16x128_f8f6f4 v[46:49], v[2:9], v[220:227], v[46:49], v246, v247 op_sel_hi:[0,0,0]
	v_mfma_scale_f32_16x16x128_f8f6f4 v[42:45], v[10:17], v[220:227], v[42:45], v246, v247 op_sel_hi:[0,0,0]
	v_mfma_scale_f32_16x16x128_f8f6f4 v[38:41], v[2:9], v[228:235], v[38:41], v246, v247 op_sel_hi:[0,0,0]
	v_mfma_scale_f32_16x16x128_f8f6f4 v[34:37], v[10:17], v[228:235], v[34:37], v246, v247 op_sel_hi:[0,0,0]
	s_setprio 2
	s_barrier
; #define PG8_STAGE(bufoff, gbase, voff) do { _Pragma("unroll") for (int _i = 0; _i < 2; ++_i) \
;         __builtin_amdgcn_global_load_lds((const unsigned*)((const char*)(gbase) + (voff)[_i]), (PG8_LAS unsigned*)(lds + (bufoff) + ldsw + _i * 8192), 16, 0, 0); } while (0)
; #define PG8_WAIT_V(n) asm volatile("s_waitcnt vmcnt(" #n ")" ::: "memory")
; #define PG8_WAIT_L(n) asm volatile("s_waitcnt lgkmcnt(" #n ")" ::: "memory")
; #define PG8_BAR __builtin_amdgcn_s_barrier()
; #define PG8_SCHED __builtin_amdgcn_sched_barrier(0)
; template <class Epi, class Sched, bool ALIGN_EPI = false, bool SP2 = false, bool F8 = false>
; __device__ __forceinline__ void gemm_phase(PG8_LAS unsigned char* lds, const Gemm g, const Sched& S, const Epi& E, const int tidb  ) {
;     ...
;             PG8_LDB(B0, 1, 0); PG8_LDB(B1, 1, 1); PG8_SCHED; PG8_LDA(At, 1, 0); PG8_STAGE(PG8_SA(0, 1), a2 + hstep, voffA);
;             PG8_WAIT_V(8); PG8_WAIT_L(0); PG8_BAR; PG8_MMA(0, 0, At, B0); PG8_MMA(0, 1, At, B1); PG8_BAR; PG8_SCHED;
;             PG8_LDA(At, 1, 1); PG8_STAGE(PG8_SB(1, 0), b3, voffB); PG8_STAGE(PG8_SB(1, 1), b3 + hstep, voffB); PG8_STAGE(PG8_SA(1, 0), a3, voffA);
;             PG8_WAIT_V(8); PG8_WAIT_L(0); PG8_BAR; PG8_MMA(1, 0, At, B0); PG8_MMA(1, 1, At, B1); PG8_BAR; PG8_SCHED;
	s_add_i32 s8, 0, 0x18000
	v_add_u32_e32 v0, s8, v190
	s_add_i32 s9, 0, 0x1c000
	ds_read_b128 v[2:5], v0
	ds_read_b128 v[6:9], v0 offset:1024
	ds_read_b128 v[10:13], v0 offset:2048
	ds_read_b128 v[14:17], v0 offset:3072
	v_add_u32_e32 v0, s9, v190
	ds_read_b128 v[18:21], v0
	ds_read_b128 v[22:25], v0 offset:1024
	ds_read_b128 v[26:29], v0 offset:2048
	ds_read_b128 v[30:33], v0 offset:3072
	s_add_u32 s6, s6, s20
	s_addc_u32 s7, s7, s21
	s_mov_b32 m0, s48
	v_lshl_add_u64 v[192:193], s[6:7], 0, v[164:165]
	ds_read_b128 v[204:207], v191 offset:32768
	ds_read_b128 v[208:211], v191 offset:33792
	ds_read_b128 v[212:215], v191 offset:34816
	ds_read_b128 v[216:219], v191 offset:35840
	ds_read_b128 v[220:223], v191 offset:36864
	ds_read_b128 v[224:227], v191 offset:37888
	ds_read_b128 v[228:231], v191 offset:38912
	ds_read_b128 v[232:235], v191 offset:39936
	global_load_lds_dwordx4 v[192:193], off
	v_lshl_add_u64 v[192:193], s[6:7], 0, v[168:169]
	s_mov_b32 m0, s90
	s_nop 0
	global_load_lds_dwordx4 v[192:193], off
	s_waitcnt vmcnt(8)
	s_waitcnt lgkmcnt(0)
	s_barrier
	s_setprio 1
	s_waitcnt lgkmcnt(0)
	v_mfma_scale_f32_16x16x128_f8f6f4 v[158:161], v[2:9], v[204:211], v[158:161], v246, v247 op_sel_hi:[0,0,0]
	v_mfma_scale_f32_16x16x128_f8f6f4 v[154:157], v[10:17], v[204:211], v[154:157], v246, v247 op_sel_hi:[0,0,0]
	v_mfma_scale_f32_16x16x128_f8f6f4 v[150:153], v[2:9], v[212:219], v[150:153], v246, v247 op_sel_hi:[0,0,0]
	v_mfma_scale_f32_16x16x128_f8f6f4 v[146:149], v[10:17], v[212:219], v[146:149], v246, v247 op_sel_hi:[0,0,0]
	v_mfma_scale_f32_16x16x128_f8f6f4 v[142:145], v[2:9], v[220:227], v[142:145], v246, v247 op_sel_hi:[0,0,0]
	v_mfma_scale_f32_16x16x128_f8f6f4 v[138:141], v[10:17], v[220:227], v[138:141], v246, v247 op_sel_hi:[0,0,0]
	v_mfma_scale_f32_16x16x128_f8f6f4 v[134:137], v[2:9], v[228:235], v[134:137], v246, v247 op_sel_hi:[0,0,0]
	v_mfma_scale_f32_16x16x128_f8f6f4 v[130:133], v[10:17], v[228:235], v[130:133], v246, v247 op_sel_hi:[0,0,0]
	s_setprio 0
	s_setprio 1
	v_mfma_scale_f32_16x16x128_f8f6f4 v[94:97], v[18:25], v[204:211], v[94:97], v246, v247 op_sel_hi:[0,0,0]
	v_mfma_scale_f32_16x16x128_f8f6f4 v[90:93], v[26:33], v[204:211], v[90:93], v246, v247 op_sel_hi:[0,0,0]
	v_mfma_scale_f32_16x16x128_f8f6f4 v[86:89], v[18:25], v[212:219], v[86:89], v246, v247 op_sel_hi:[0,0,0]
	v_mfma_scale_f32_16x16x128_f8f6f4 v[82:85], v[26:33], v[212:219], v[82:85], v246, v247 op_sel_hi:[0,0,0]
	v_mfma_scale_f32_16x16x128_f8f6f4 v[78:81], v[18:25], v[220:227], v[78:81], v246, v247 op_sel_hi:[0,0,0]
	v_mfma_scale_f32_16x16x128_f8f6f4 v[74:77], v[26:33], v[220:227], v[74:77], v246, v247 op_sel_hi:[0,0,0]
	v_mfma_scale_f32_16x16x128_f8f6f4 v[70:73], v[18:25], v[228:235], v[70:73], v246, v247 op_sel_hi:[0,0,0]
	v_mfma_scale_f32_16x16x128_f8f6f4 v[66:69], v[26:33], v[228:235], v[66:69], v246, v247 op_sel_hi:[0,0,0]
	s_setprio 2
	s_barrier
	s_add_i32 s6, s8, s41
	v_lshl_add_u64 v[176:177], v[176:177], 0, s[92:93]
	s_mov_b32 m0, s6
	ds_read_b128 v[204:207], v191 offset:49152
	ds_read_b128 v[208:211], v191 offset:50176
	ds_read_b128 v[212:215], v191 offset:51200
	ds_read_b128 v[216:219], v191 offset:52224
	ds_read_b128 v[220:223], v191 offset:53248
	ds_read_b128 v[224:227], v191 offset:54272
	ds_read_b128 v[228:231], v191 offset:55296
	ds_read_b128 v[232:235], v191 offset:56320
	global_load_lds_dwordx4 v[176:177], off
	v_lshl_add_u64 v[176:177], v[178:179], 0, s[92:93]
	s_add_i32 m0, s6, 0x2000
	s_add_i32 s6, s9, s41
	global_load_lds_dwordx4 v[176:177], off
	v_lshl_add_u64 v[176:177], v[180:181], 0, s[92:93]
	s_mov_b32 m0, s6
	s_nop 0
	global_load_lds_dwordx4 v[176:177], off
	v_lshl_add_u64 v[176:177], v[182:183], 0, s[92:93]
	s_add_i32 m0, s6, 0x2000
	s_nop 0
	global_load_lds_dwordx4 v[176:177], off
	v_lshl_add_u64 v[176:177], v[184:185], 0, s[92:93]
	s_mov_b32 m0, s91
	s_nop 0
	global_load_lds_dwordx4 v[176:177], off
	v_lshl_add_u64 v[176:177], v[186:187], 0, s[92:93]
	s_mov_b32 m0, s51
	s_nop 0
	global_load_lds_dwordx4 v[176:177], off
	s_waitcnt vmcnt(8)
	s_waitcnt lgkmcnt(0)
	s_barrier
	s_setprio 1
	s_waitcnt lgkmcnt(0)
	v_mfma_scale_f32_16x16x128_f8f6f4 v[126:129], v[2:9], v[204:211], v[126:129], v246, v247 op_sel_hi:[0,0,0]
	v_mfma_scale_f32_16x16x128_f8f6f4 v[122:125], v[10:17], v[204:211], v[122:125], v246, v247 op_sel_hi:[0,0,0]
	v_mfma_scale_f32_16x16x128_f8f6f4 v[118:121], v[2:9], v[212:219], v[118:121], v246, v247 op_sel_hi:[0,0,0]
	v_mfma_scale_f32_16x16x128_f8f6f4 v[114:117], v[10:17], v[212:219], v[114:117], v246, v247 op_sel_hi:[0,0,0]
	v_mfma_scale_f32_16x16x128_f8f6f4 v[110:113], v[2:9], v[220:227], v[110:113], v246, v247 op_sel_hi:[0,0,0]
	v_mfma_scale_f32_16x16x128_f8f6f4 v[106:109], v[10:17], v[220:227], v[106:109], v246, v247 op_sel_hi:[0,0,0]
	v_mfma_scale_f32_16x16x128_f8f6f4 v[102:105], v[2:9], v[228:235], v[102:105], v246, v247 op_sel_hi:[0,0,0]
	v_mfma_scale_f32_16x16x128_f8f6f4 v[98:101], v[10:17], v[228:235], v[98:101], v246, v247 op_sel_hi:[0,0,0]
	s_setprio 0
	s_setprio 1
	v_mfma_scale_f32_16x16x128_f8f6f4 v[62:65], v[18:25], v[204:211], v[62:65], v246, v247 op_sel_hi:[0,0,0]
	v_mfma_scale_f32_16x16x128_f8f6f4 v[58:61], v[26:33], v[204:211], v[58:61], v246, v247 op_sel_hi:[0,0,0]
	v_mfma_scale_f32_16x16x128_f8f6f4 v[54:57], v[18:25], v[212:219], v[54:57], v246, v247 op_sel_hi:[0,0,0]
	v_mfma_scale_f32_16x16x128_f8f6f4 v[50:53], v[26:33], v[212:219], v[50:53], v246, v247 op_sel_hi:[0,0,0]
	v_mfma_scale_f32_16x16x128_f8f6f4 v[46:49], v[18:25], v[220:227], v[46:49], v246, v247 op_sel_hi:[0,0,0]
	v_mfma_scale_f32_16x16x128_f8f6f4 v[42:45], v[26:33], v[220:227], v[42:45], v246, v247 op_sel_hi:[0,0,0]
	v_mfma_scale_f32_16x16x128_f8f6f4 v[38:41], v[18:25], v[228:235], v[38:41], v246, v247 op_sel_hi:[0,0,0]
	v_mfma_scale_f32_16x16x128_f8f6f4 v[34:37], v[26:33], v[228:235], v[34:37], v246, v247 op_sel_hi:[0,0,0]
	s_setprio 2
	s_barrier
	s_add_u32 s4, s4, 0x100
	s_addc_u32 s5, s5, 0
	s_add_u32 s12, s12, 0x100
	s_addc_u32 s13, s13, 0
	s_cmp_ge_i32 s14, s84
	s_mov_b32 s6, s14
	s_cbranch_scc0 .LBB0_51

; #define PG8_STAGE(bufoff, gbase, voff) do { _Pragma("unroll") for (int _i = 0; _i < 2; ++_i) \
;         __builtin_amdgcn_global_load_lds((const unsigned*)((const char*)(gbase) + (voff)[_i]), (PG8_LAS unsigned*)(lds + (bufoff) + ldsw + _i * 8192), 16, 0, 0); } while (0)
; #define PG8_WAIT_V(n) asm volatile("s_waitcnt vmcnt(" #n ")" ::: "memory")
; #define PG8_WAIT_L(n) asm volatile("s_waitcnt lgkmcnt(" #n ")" ::: "memory")
; #define PG8_BAR __builtin_amdgcn_s_barrier()
; #define PG8_SCHED __builtin_amdgcn_sched_barrier(0)
; template <class Epi, class Sched, bool ALIGN_EPI = false, bool SP2 = false, bool F8 = false>
; __device__ __forceinline__ void gemm_phase(PG8_LAS unsigned char* lds, const Gemm g, const Sched& S, const Epi& E, const int tidb  ) {
;     ...
;             if constexpr (SP2) {
;             PG8_LDB(B0, 0, 0); PG8_LDB(B1, 0, 1); PG8_SCHED; PG8_LDA(At, 0, 0); PG8_STAGE(PG8_SA(1, 1), a1 + hstep, voffA);
;             PG8_WAIT_V(8); PG8_WAIT_L(0); PG8_BAR; PG8_MMA(0, 0, At, B0); PG8_MMA(0, 1, At, B1); PG8_BAR; PG8_SCHED;
;             PG8_LDA(At, 0, 1); PG8_STAGE(PG8_SB(0, 0), b2, voffB); PG8_STAGE(PG8_SB(0, 1), b2 + hstep, voffB); PG8_STAGE(PG8_SA(0, 0), a2, voffA);
;             PG8_WAIT_V(8); PG8_WAIT_L(0); PG8_BAR; PG8_MMA(1, 0, At, B0); PG8_MMA(1, 1, At, B1); PG8_BAR; PG8_SCHED;
.LBB0_393:
	s_add_i32 s63, s28, 2
	s_add_u32 s65, s4, 0x80
	s_addc_u32 s29, s5, 0
	s_add_i32 s68, 0, 0x10000
	s_cmp_eq_u32 s55, s28
	s_cselect_b32 s29, s25, s29
	s_cselect_b32 s28, s24, s65
	v_add_u32_e32 v0, s68, v152
	s_cselect_b32 s67, s27, s31
	s_cselect_b32 s66, s26, s30
	s_add_i32 s65, 0, 0x14000
	ds_read_b128 v[158:161], v0
	s_waitcnt vmcnt(0)
	ds_read_b128 v[164:167], v0 offset:1024
	ds_read_b128 v[168:171], v0 offset:2048
	ds_read_b128 v[172:175], v0 offset:3072
	v_add_u32_e32 v0, s65, v152
	ds_read_b128 v[176:179], v0
	ds_read_b128 v[180:183], v0 offset:1024
	ds_read_b128 v[184:187], v0 offset:2048
	ds_read_b128 v[188:191], v0 offset:3072
	v_lshl_add_u64 v[148:149], s[4:5], 0, v[144:145]
	s_add_i32 m0, s46, 0xc000
	ds_read_b128 v[192:195], v156
	ds_read_b128 v[204:207], v156 offset:1024
	ds_read_b128 v[208:211], v156 offset:2048
	ds_read_b128 v[212:215], v156 offset:3072
	ds_read_b128 v[216:219], v156 offset:4096
	ds_read_b128 v[220:223], v156 offset:5120
	ds_read_b128 v[224:227], v156 offset:6144
	ds_read_b128 v[228:231], v156 offset:7168
	global_load_lds_dwordx4 v[148:149], off
	v_lshl_add_u64 v[148:149], s[4:5], 0, v[146:147]
	s_add_i32 m0, s46, 0xe000
	s_nop 0
	global_load_lds_dwordx4 v[148:149], off
	s_waitcnt vmcnt(8)
	s_waitcnt lgkmcnt(0)
	s_barrier
	s_setprio 1
	s_waitcnt lgkmcnt(0)
	v_mfma_f32_16x16x32_bf16 v[122:125], v[158:161], v[192:195], v[122:125]
	v_mfma_f32_16x16x32_bf16 v[126:129], v[168:171], v[192:195], v[126:129]
	v_mfma_f32_16x16x32_bf16 v[118:121], v[158:161], v[208:211], v[118:121]
	v_mfma_f32_16x16x32_bf16 v[114:117], v[168:171], v[208:211], v[114:117]
	v_mfma_f32_16x16x32_bf16 v[110:113], v[158:161], v[216:219], v[110:113]
	v_mfma_f32_16x16x32_bf16 v[106:109], v[168:171], v[216:219], v[106:109]
	v_mfma_f32_16x16x32_bf16 v[102:105], v[158:161], v[224:227], v[102:105]
	v_mfma_f32_16x16x32_bf16 v[98:101], v[168:171], v[224:227], v[98:101]
	v_mfma_f32_16x16x32_bf16 v[122:125], v[164:167], v[204:207], v[122:125]
	v_mfma_f32_16x16x32_bf16 v[126:129], v[172:175], v[204:207], v[126:129]
	v_mfma_f32_16x16x32_bf16 v[118:121], v[164:167], v[212:215], v[118:121]
	v_mfma_f32_16x16x32_bf16 v[114:117], v[172:175], v[212:215], v[114:117]
	v_mfma_f32_16x16x32_bf16 v[110:113], v[164:167], v[220:223], v[110:113]
	v_mfma_f32_16x16x32_bf16 v[106:109], v[172:175], v[220:223], v[106:109]
	v_mfma_f32_16x16x32_bf16 v[102:105], v[164:167], v[228:231], v[102:105]
	v_mfma_f32_16x16x32_bf16 v[98:101], v[172:175], v[228:231], v[98:101]
	s_setprio 0
	s_setprio 1
	v_mfma_f32_16x16x32_bf16 v[62:65], v[176:179], v[192:195], v[62:65]
	v_mfma_f32_16x16x32_bf16 v[58:61], v[184:187], v[192:195], v[58:61]
	v_mfma_f32_16x16x32_bf16 v[54:57], v[176:179], v[208:211], v[54:57]
	v_mfma_f32_16x16x32_bf16 v[50:53], v[184:187], v[208:211], v[50:53]
	v_mfma_f32_16x16x32_bf16 v[46:49], v[176:179], v[216:219], v[46:49]
	v_mfma_f32_16x16x32_bf16 v[42:45], v[184:187], v[216:219], v[42:45]
	v_mfma_f32_16x16x32_bf16 v[38:41], v[176:179], v[224:227], v[38:41]
	v_mfma_f32_16x16x32_bf16 v[34:37], v[184:187], v[224:227], v[34:37]
	v_mfma_f32_16x16x32_bf16 v[62:65], v[180:183], v[204:207], v[62:65]
	v_mfma_f32_16x16x32_bf16 v[58:61], v[188:191], v[204:207], v[58:61]
	v_mfma_f32_16x16x32_bf16 v[54:57], v[180:183], v[212:215], v[54:57]
	v_mfma_f32_16x16x32_bf16 v[50:53], v[188:191], v[212:215], v[50:53]
	v_mfma_f32_16x16x32_bf16 v[46:49], v[180:183], v[220:223], v[46:49]
	v_mfma_f32_16x16x32_bf16 v[42:45], v[188:191], v[220:223], v[42:45]
	v_mfma_f32_16x16x32_bf16 v[38:41], v[180:183], v[228:231], v[38:41]
	v_mfma_f32_16x16x32_bf16 v[34:37], v[188:191], v[228:231], v[34:37]
	s_setprio 2
	s_barrier
	s_add_i32 s68, s68, s45
	v_lshl_add_u64 v[148:149], s[66:67], 0, v[132:133]
	s_mov_b32 m0, s68
	ds_read_b128 v[192:195], v156 offset:16384
	ds_read_b128 v[204:207], v156 offset:17408
	ds_read_b128 v[208:211], v156 offset:18432
	ds_read_b128 v[212:215], v156 offset:19456
	ds_read_b128 v[216:219], v156 offset:20480
	ds_read_b128 v[220:223], v156 offset:21504
	ds_read_b128 v[224:227], v156 offset:22528
	ds_read_b128 v[228:231], v156 offset:23552
	global_load_lds_dwordx4 v[148:149], off
	s_add_i32 m0, s68, 0x2000
	v_lshl_add_u64 v[196:197], s[66:67], 0, v[136:137]
	s_add_u32 s66, s66, s10
	s_addc_u32 s67, s67, s11
	s_add_i32 s65, s65, s45
	global_load_lds_dwordx4 v[196:197], off
	v_lshl_add_u64 v[200:201], s[66:67], 0, v[132:133]
	s_mov_b32 m0, s65
	v_lshl_add_u64 v[232:233], s[66:67], 0, v[136:137]
	global_load_lds_dwordx4 v[200:201], off
	s_add_i32 m0, s65, 0x2000
	v_lshl_add_u64 v[234:235], s[28:29], 0, v[130:131]
	global_load_lds_dwordx4 v[232:233], off
	s_mov_b32 m0, s46
	v_lshl_add_u64 v[236:237], s[28:29], 0, v[134:135]
	global_load_lds_dwordx4 v[234:235], off
	s_mov_b32 m0, s47
	s_nop 0
	global_load_lds_dwordx4 v[236:237], off
	s_waitcnt vmcnt(8)
	s_waitcnt lgkmcnt(0)
	s_barrier
; #define PG8_STAGE(bufoff, gbase, voff) do { _Pragma("unroll") for (int _i = 0; _i < 2; ++_i) \
;         __builtin_amdgcn_global_load_lds((const unsigned*)((const char*)(gbase) + (voff)[_i]), (PG8_LAS unsigned*)(lds + (bufoff) + ldsw + _i * 8192), 16, 0, 0); } while (0)
; #define PG8_WAIT_V(n) asm volatile("s_waitcnt vmcnt(" #n ")" ::: "memory")
; #define PG8_WAIT_L(n) asm volatile("s_waitcnt lgkmcnt(" #n ")" ::: "memory")
; #define PG8_BAR __builtin_amdgcn_s_barrier()
; #define PG8_SCHED __builtin_amdgcn_sched_barrier(0)
; template <class Epi, class Sched, bool ALIGN_EPI = false, bool SP2 = false, bool F8 = false>
; __device__ __forceinline__ void gemm_phase(PG8_LAS unsigned char* lds, const Gemm g, const Sched& S, const Epi& E, const int tidb  ) {
;     ...
;             PG8_WAIT_V(8); PG8_WAIT_L(0); PG8_BAR; PG8_MMA(1, 0, At, B0); PG8_MMA(1, 1, At, B1); PG8_BAR; PG8_SCHED;
;             PG8_LDB(B0, 1, 0); PG8_LDB(B1, 1, 1); PG8_SCHED; PG8_LDA(At, 1, 0); PG8_STAGE(PG8_SA(0, 1), a2 + hstep, voffA);
;             PG8_WAIT_V(8); PG8_WAIT_L(0); PG8_BAR; PG8_MMA(0, 0, At, B0); PG8_MMA(0, 1, At, B1); PG8_BAR; PG8_SCHED;
;             PG8_LDA(At, 1, 1); PG8_STAGE(PG8_SB(1, 0), b3, voffB); PG8_STAGE(PG8_SB(1, 1), b3 + hstep, voffB); PG8_STAGE(PG8_SA(1, 0), a3, voffA);
	s_setprio 1
	s_waitcnt lgkmcnt(0)
	v_mfma_f32_16x16x32_bf16 v[94:97], v[158:161], v[192:195], v[94:97]
	v_mfma_f32_16x16x32_bf16 v[90:93], v[168:171], v[192:195], v[90:93]
	v_mfma_f32_16x16x32_bf16 v[86:89], v[158:161], v[208:211], v[86:89]
	v_mfma_f32_16x16x32_bf16 v[82:85], v[168:171], v[208:211], v[82:85]
	v_mfma_f32_16x16x32_bf16 v[78:81], v[158:161], v[216:219], v[78:81]
	v_mfma_f32_16x16x32_bf16 v[74:77], v[168:171], v[216:219], v[74:77]
	v_mfma_f32_16x16x32_bf16 v[70:73], v[158:161], v[224:227], v[70:73]
	v_mfma_f32_16x16x32_bf16 v[66:69], v[168:171], v[224:227], v[66:69]
	v_mfma_f32_16x16x32_bf16 v[94:97], v[164:167], v[204:207], v[94:97]
	v_mfma_f32_16x16x32_bf16 v[90:93], v[172:175], v[204:207], v[90:93]
	v_mfma_f32_16x16x32_bf16 v[86:89], v[164:167], v[212:215], v[86:89]
	v_mfma_f32_16x16x32_bf16 v[82:85], v[172:175], v[212:215], v[82:85]
	v_mfma_f32_16x16x32_bf16 v[78:81], v[164:167], v[220:223], v[78:81]
	v_mfma_f32_16x16x32_bf16 v[74:77], v[172:175], v[220:223], v[74:77]
	v_mfma_f32_16x16x32_bf16 v[70:73], v[164:167], v[228:231], v[70:73]
	v_mfma_f32_16x16x32_bf16 v[66:69], v[172:175], v[228:231], v[66:69]
	s_setprio 0
	s_setprio 1
	v_mfma_f32_16x16x32_bf16 v[30:33], v[176:179], v[192:195], v[30:33]
	v_mfma_f32_16x16x32_bf16 v[26:29], v[184:187], v[192:195], v[26:29]
	v_mfma_f32_16x16x32_bf16 v[22:25], v[176:179], v[208:211], v[22:25]
	v_mfma_f32_16x16x32_bf16 v[18:21], v[184:187], v[208:211], v[18:21]
	v_mfma_f32_16x16x32_bf16 v[14:17], v[176:179], v[216:219], v[14:17]
	v_mfma_f32_16x16x32_bf16 v[10:13], v[184:187], v[216:219], v[10:13]
	v_mfma_f32_16x16x32_bf16 v[6:9], v[176:179], v[224:227], v[6:9]
	v_mfma_f32_16x16x32_bf16 v[2:5], v[184:187], v[224:227], v[2:5]
	v_mfma_f32_16x16x32_bf16 v[30:33], v[180:183], v[204:207], v[30:33]
	v_mfma_f32_16x16x32_bf16 v[26:29], v[188:191], v[204:207], v[26:29]
	v_mfma_f32_16x16x32_bf16 v[22:25], v[180:183], v[212:215], v[22:25]
	v_mfma_f32_16x16x32_bf16 v[18:21], v[188:191], v[212:215], v[18:21]
	v_mfma_f32_16x16x32_bf16 v[14:17], v[180:183], v[220:223], v[14:17]
	v_mfma_f32_16x16x32_bf16 v[10:13], v[188:191], v[220:223], v[10:13]
	v_mfma_f32_16x16x32_bf16 v[6:9], v[180:183], v[228:231], v[6:9]
	v_mfma_f32_16x16x32_bf16 v[2:5], v[188:191], v[228:231], v[2:5]
	s_setprio 2
	s_barrier
	s_add_i32 s65, 0, 0x18000
	v_add_u32_e32 v0, s65, v152
	s_add_i32 s66, 0, 0x1c000
	ds_read_b128 v[158:161], v0
	ds_read_b128 v[164:167], v0 offset:1024
	ds_read_b128 v[168:171], v0 offset:2048
	ds_read_b128 v[172:175], v0 offset:3072
	v_add_u32_e32 v0, s66, v152
	ds_read_b128 v[176:179], v0
	ds_read_b128 v[180:183], v0 offset:1024
	ds_read_b128 v[184:187], v0 offset:2048
	ds_read_b128 v[188:191], v0 offset:3072
	s_add_u32 s28, s28, s10
	s_addc_u32 s29, s29, s11
	s_mov_b32 m0, s48
	v_lshl_add_u64 v[238:239], s[28:29], 0, v[130:131]
	ds_read_b128 v[192:195], v156 offset:32768
	ds_read_b128 v[204:207], v156 offset:33792
	ds_read_b128 v[208:211], v156 offset:34816
	ds_read_b128 v[212:215], v156 offset:35840
	ds_read_b128 v[216:219], v156 offset:36864
	ds_read_b128 v[220:223], v156 offset:37888
	ds_read_b128 v[224:227], v156 offset:38912
	ds_read_b128 v[228:231], v156 offset:39936
	global_load_lds_dwordx4 v[238:239], off
	v_lshl_add_u64 v[238:239], s[28:29], 0, v[134:135]
	s_mov_b32 m0, s49
	s_nop 0
	global_load_lds_dwordx4 v[238:239], off
	s_waitcnt vmcnt(8)
	s_waitcnt lgkmcnt(0)
	s_barrier
	s_setprio 1
	s_waitcnt lgkmcnt(0)
	v_mfma_f32_16x16x32_bf16 v[122:125], v[158:161], v[192:195], v[122:125]
	v_mfma_f32_16x16x32_bf16 v[126:129], v[168:171], v[192:195], v[126:129]
	v_mfma_f32_16x16x32_bf16 v[118:121], v[158:161], v[208:211], v[118:121]
	v_mfma_f32_16x16x32_bf16 v[114:117], v[168:171], v[208:211], v[114:117]
	v_mfma_f32_16x16x32_bf16 v[110:113], v[158:161], v[216:219], v[110:113]
	v_mfma_f32_16x16x32_bf16 v[106:109], v[168:171], v[216:219], v[106:109]
	v_mfma_f32_16x16x32_bf16 v[102:105], v[158:161], v[224:227], v[102:105]
	v_mfma_f32_16x16x32_bf16 v[98:101], v[168:171], v[224:227], v[98:101]
	v_mfma_f32_16x16x32_bf16 v[122:125], v[164:167], v[204:207], v[122:125]
	v_mfma_f32_16x16x32_bf16 v[126:129], v[172:175], v[204:207], v[126:129]
	v_mfma_f32_16x16x32_bf16 v[118:121], v[164:167], v[212:215], v[118:121]
	v_mfma_f32_16x16x32_bf16 v[114:117], v[172:175], v[212:215], v[114:117]
	v_mfma_f32_16x16x32_bf16 v[110:113], v[164:167], v[220:223], v[110:113]
	v_mfma_f32_16x16x32_bf16 v[106:109], v[172:175], v[220:223], v[106:109]
	v_mfma_f32_16x16x32_bf16 v[102:105], v[164:167], v[228:231], v[102:105]
	v_mfma_f32_16x16x32_bf16 v[98:101], v[172:175], v[228:231], v[98:101]
	s_setprio 0
	s_setprio 1
	v_mfma_f32_16x16x32_bf16 v[62:65], v[176:179], v[192:195], v[62:65]
	v_mfma_f32_16x16x32_bf16 v[58:61], v[184:187], v[192:195], v[58:61]
	v_mfma_f32_16x16x32_bf16 v[54:57], v[176:179], v[208:211], v[54:57]
	v_mfma_f32_16x16x32_bf16 v[50:53], v[184:187], v[208:211], v[50:53]
	v_mfma_f32_16x16x32_bf16 v[46:49], v[176:179], v[216:219], v[46:49]
	v_mfma_f32_16x16x32_bf16 v[42:45], v[184:187], v[216:219], v[42:45]
	v_mfma_f32_16x16x32_bf16 v[38:41], v[176:179], v[224:227], v[38:41]
	v_mfma_f32_16x16x32_bf16 v[34:37], v[184:187], v[224:227], v[34:37]
	v_mfma_f32_16x16x32_bf16 v[62:65], v[180:183], v[204:207], v[62:65]
	v_mfma_f32_16x16x32_bf16 v[58:61], v[188:191], v[204:207], v[58:61]
	v_mfma_f32_16x16x32_bf16 v[54:57], v[180:183], v[212:215], v[54:57]
	v_mfma_f32_16x16x32_bf16 v[50:53], v[188:191], v[212:215], v[50:53]
	v_mfma_f32_16x16x32_bf16 v[46:49], v[180:183], v[220:223], v[46:49]
	v_mfma_f32_16x16x32_bf16 v[42:45], v[188:191], v[220:223], v[42:45]
	v_mfma_f32_16x16x32_bf16 v[38:41], v[180:183], v[228:231], v[38:41]
	v_mfma_f32_16x16x32_bf16 v[34:37], v[188:191], v[228:231], v[34:37]
	s_setprio 2
	s_barrier
; #define PG8_STAGE(bufoff, gbase, voff) do { _Pragma("unroll") for (int _i = 0; _i < 2; ++_i) \
;         __builtin_amdgcn_global_load_lds((const unsigned*)((const char*)(gbase) + (voff)[_i]), (PG8_LAS unsigned*)(lds + (bufoff) + ldsw + _i * 8192), 16, 0, 0); } while (0)
; #define PG8_WAIT_V(n) asm volatile("s_waitcnt vmcnt(" #n ")" ::: "memory")
; #define PG8_WAIT_L(n) asm volatile("s_waitcnt lgkmcnt(" #n ")" ::: "memory")
; #define PG8_BAR __builtin_amdgcn_s_barrier()
; #define PG8_SCHED __builtin_amdgcn_sched_barrier(0)
; template <class Epi, class Sched, bool ALIGN_EPI = false, bool SP2 = false, bool F8 = false>
; __device__ __forceinline__ void gemm_phase(PG8_LAS unsigned char* lds, const Gemm g, const Sched& S, const Epi& E, const int tidb  ) {
;     ...
;             PG8_LDA(At, 1, 1); PG8_STAGE(PG8_SB(1, 0), b3, voffB); PG8_STAGE(PG8_SB(1, 1), b3 + hstep, voffB); PG8_STAGE(PG8_SA(1, 0), a3, voffA);
;             PG8_WAIT_V(8); PG8_WAIT_L(0); PG8_BAR; PG8_MMA(1, 0, At, B0); PG8_MMA(1, 1, At, B1); PG8_BAR; PG8_SCHED;
	s_add_i32 s28, s65, s45
	v_lshl_add_u64 v[148:149], v[148:149], 0, s[92:93]
	s_mov_b32 m0, s28
	ds_read_b128 v[192:195], v156 offset:49152
	ds_read_b128 v[204:207], v156 offset:50176
	ds_read_b128 v[208:211], v156 offset:51200
	ds_read_b128 v[212:215], v156 offset:52224
	ds_read_b128 v[216:219], v156 offset:53248
	ds_read_b128 v[220:223], v156 offset:54272
	ds_read_b128 v[224:227], v156 offset:55296
	ds_read_b128 v[228:231], v156 offset:56320
	global_load_lds_dwordx4 v[148:149], off
	v_lshl_add_u64 v[148:149], v[196:197], 0, s[92:93]
	s_add_i32 m0, s28, 0x2000
	s_add_i32 s28, s66, s45
	global_load_lds_dwordx4 v[148:149], off
	v_lshl_add_u64 v[148:149], v[200:201], 0, s[92:93]
	s_mov_b32 m0, s28
	s_nop 0
	global_load_lds_dwordx4 v[148:149], off
	v_lshl_add_u64 v[148:149], v[232:233], 0, s[92:93]
	s_add_i32 m0, s28, 0x2000
	s_nop 0
	global_load_lds_dwordx4 v[148:149], off
	v_lshl_add_u64 v[148:149], v[234:235], 0, s[92:93]
	s_mov_b32 m0, s50
	s_nop 0
	global_load_lds_dwordx4 v[148:149], off
	v_lshl_add_u64 v[148:149], v[236:237], 0, s[92:93]
	s_mov_b32 m0, s51
	s_nop 0
	global_load_lds_dwordx4 v[148:149], off
	s_waitcnt vmcnt(8)
	s_waitcnt lgkmcnt(0)
	s_barrier
	s_setprio 1
	s_waitcnt lgkmcnt(0)
	v_mfma_f32_16x16x32_bf16 v[94:97], v[158:161], v[192:195], v[94:97]
	v_mfma_f32_16x16x32_bf16 v[90:93], v[168:171], v[192:195], v[90:93]
	v_mfma_f32_16x16x32_bf16 v[86:89], v[158:161], v[208:211], v[86:89]
	v_mfma_f32_16x16x32_bf16 v[82:85], v[168:171], v[208:211], v[82:85]
	v_mfma_f32_16x16x32_bf16 v[78:81], v[158:161], v[216:219], v[78:81]
	v_mfma_f32_16x16x32_bf16 v[74:77], v[168:171], v[216:219], v[74:77]
	v_mfma_f32_16x16x32_bf16 v[70:73], v[158:161], v[224:227], v[70:73]
	v_mfma_f32_16x16x32_bf16 v[66:69], v[168:171], v[224:227], v[66:69]
	v_mfma_f32_16x16x32_bf16 v[94:97], v[164:167], v[204:207], v[94:97]
	v_mfma_f32_16x16x32_bf16 v[90:93], v[172:175], v[204:207], v[90:93]
	v_mfma_f32_16x16x32_bf16 v[86:89], v[164:167], v[212:215], v[86:89]
	v_mfma_f32_16x16x32_bf16 v[82:85], v[172:175], v[212:215], v[82:85]
	v_mfma_f32_16x16x32_bf16 v[78:81], v[164:167], v[220:223], v[78:81]
	v_mfma_f32_16x16x32_bf16 v[74:77], v[172:175], v[220:223], v[74:77]
	v_mfma_f32_16x16x32_bf16 v[70:73], v[164:167], v[228:231], v[70:73]
	v_mfma_f32_16x16x32_bf16 v[66:69], v[172:175], v[228:231], v[66:69]
	s_setprio 0
	s_setprio 1
	v_mfma_f32_16x16x32_bf16 v[30:33], v[176:179], v[192:195], v[30:33]
	v_mfma_f32_16x16x32_bf16 v[26:29], v[184:187], v[192:195], v[26:29]
	v_mfma_f32_16x16x32_bf16 v[22:25], v[176:179], v[208:211], v[22:25]
	v_mfma_f32_16x16x32_bf16 v[18:21], v[184:187], v[208:211], v[18:21]
	v_mfma_f32_16x16x32_bf16 v[14:17], v[176:179], v[216:219], v[14:17]
	v_mfma_f32_16x16x32_bf16 v[10:13], v[184:187], v[216:219], v[10:13]
	v_mfma_f32_16x16x32_bf16 v[6:9], v[176:179], v[224:227], v[6:9]
	v_mfma_f32_16x16x32_bf16 v[2:5], v[184:187], v[224:227], v[2:5]
	v_mfma_f32_16x16x32_bf16 v[30:33], v[180:183], v[204:207], v[30:33]
	v_mfma_f32_16x16x32_bf16 v[26:29], v[188:191], v[204:207], v[26:29]
	v_mfma_f32_16x16x32_bf16 v[22:25], v[180:183], v[212:215], v[22:25]
	v_mfma_f32_16x16x32_bf16 v[18:21], v[188:191], v[212:215], v[18:21]
	v_mfma_f32_16x16x32_bf16 v[14:17], v[180:183], v[220:223], v[14:17]
	v_mfma_f32_16x16x32_bf16 v[10:13], v[188:191], v[220:223], v[10:13]
	v_mfma_f32_16x16x32_bf16 v[6:9], v[180:183], v[228:231], v[6:9]
	v_mfma_f32_16x16x32_bf16 v[2:5], v[188:191], v[228:231], v[2:5]
	s_setprio 2
	s_barrier
	s_add_u32 s4, s4, 0x100
	s_addc_u32 s5, s5, 0
	s_add_u32 s30, s30, 0x100
	s_addc_u32 s31, s31, 0
	s_cmp_ge_i32 s63, s52
	s_mov_b32 s28, s63
	s_cbranch_scc0 .LBB0_393
	s_movk_i32 s67, 0x300

; #define PG8_STAGE(bufoff, gbase, voff) do { _Pragma("unroll") for (int _i = 0; _i < 2; ++_i) \
;         __builtin_amdgcn_global_load_lds((const unsigned*)((const char*)(gbase) + (voff)[_i]), (PG8_LAS unsigned*)(lds + (bufoff) + ldsw + _i * 8192), 16, 0, 0); } while (0)
; #define PG8_WAIT_V(n) asm volatile("s_waitcnt vmcnt(" #n ")" ::: "memory")
; #define PG8_WAIT_L(n) asm volatile("s_waitcnt lgkmcnt(" #n ")" ::: "memory")
; #define PG8_BAR __builtin_amdgcn_s_barrier()
; #define PG8_SCHED __builtin_amdgcn_sched_barrier(0)
; template <class Epi, class Sched, bool ALIGN_EPI = false, bool SP2 = false, bool F8 = false>
; __device__ __forceinline__ void gemm_phase(PG8_LAS unsigned char* lds, const Gemm g, const Sched& S, const Epi& E, const int tidb  ) {
;     ...
;             if constexpr (SP2) {
;             PG8_LDB(B0, 0, 0); PG8_LDB(B1, 0, 1); PG8_SCHED; PG8_LDA(At, 0, 0); PG8_STAGE(PG8_SA(1, 1), a1 + hstep, voffA);
;             PG8_WAIT_V(8); PG8_WAIT_L(0); PG8_BAR; PG8_MMA(0, 0, At, B0); PG8_MMA(0, 1, At, B1); PG8_BAR; PG8_SCHED;
;             PG8_LDA(At, 0, 1); PG8_STAGE(PG8_SB(0, 0), b2, voffB); PG8_STAGE(PG8_SB(0, 1), b2 + hstep, voffB); PG8_STAGE(PG8_SA(0, 0), a2, voffA);
;             PG8_WAIT_V(8); PG8_WAIT_L(0); PG8_BAR; PG8_MMA(1, 0, At, B0); PG8_MMA(1, 1, At, B1); PG8_BAR; PG8_SCHED;
.LBB0_465:
	s_add_i32 s61, s6, 2
	s_add_u32 s62, s4, 0x80
	s_addc_u32 s7, s5, 0
	s_add_i32 s65, 0, 0x10000
	s_cmp_eq_u32 s54, s6
	s_cselect_b32 s7, s25, s7
	s_cselect_b32 s6, s24, s62
	v_add_u32_e32 v0, s65, v159
	s_cselect_b32 s63, s27, s29
	s_cselect_b32 s62, s26, s28
	s_add_i32 s66, 0, 0x14000
	ds_read_b128 v[142:145], v0
	ds_read_b128 v[146:149], v0 offset:1024
	ds_read_b128 v[154:157], v0 offset:2048
	s_waitcnt vmcnt(0)
	ds_read_b128 v[164:167], v0 offset:3072
	v_add_u32_e32 v0, s66, v159
	ds_read_b128 v[168:171], v0
	ds_read_b128 v[172:175], v0 offset:1024
	ds_read_b128 v[176:179], v0 offset:2048
	ds_read_b128 v[180:183], v0 offset:3072
	v_lshl_add_u64 v[150:151], s[4:5], 0, v[138:139]
	s_add_i32 m0, s45, 0xc000
	ds_read_b128 v[184:187], v160
	ds_read_b128 v[188:191], v160 offset:1024
	ds_read_b128 v[192:195], v160 offset:2048
	ds_read_b128 v[204:207], v160 offset:3072
	ds_read_b128 v[208:211], v160 offset:4096
	ds_read_b128 v[212:215], v160 offset:5120
	ds_read_b128 v[216:219], v160 offset:6144
	ds_read_b128 v[220:223], v160 offset:7168
	global_load_lds_dwordx4 v[150:151], off
	v_lshl_add_u64 v[150:151], s[4:5], 0, v[140:141]
	s_add_i32 m0, s45, 0xe000
	s_nop 0
	global_load_lds_dwordx4 v[150:151], off
	s_waitcnt vmcnt(8)
	s_waitcnt lgkmcnt(0)
	s_barrier
	s_setprio 1
	s_waitcnt lgkmcnt(0)
	v_mfma_f32_16x16x32_bf16 v[126:129], v[142:145], v[184:187], v[126:129]
	v_mfma_f32_16x16x32_bf16 v[122:125], v[154:157], v[184:187], v[122:125]
	v_mfma_f32_16x16x32_bf16 v[118:121], v[142:145], v[192:195], v[118:121]
	v_mfma_f32_16x16x32_bf16 v[114:117], v[154:157], v[192:195], v[114:117]
	v_mfma_f32_16x16x32_bf16 v[110:113], v[142:145], v[208:211], v[110:113]
	v_mfma_f32_16x16x32_bf16 v[106:109], v[154:157], v[208:211], v[106:109]
	v_mfma_f32_16x16x32_bf16 v[102:105], v[142:145], v[216:219], v[102:105]
	v_mfma_f32_16x16x32_bf16 v[98:101], v[154:157], v[216:219], v[98:101]
	v_mfma_f32_16x16x32_bf16 v[126:129], v[146:149], v[188:191], v[126:129]
	v_mfma_f32_16x16x32_bf16 v[122:125], v[164:167], v[188:191], v[122:125]
	v_mfma_f32_16x16x32_bf16 v[118:121], v[146:149], v[204:207], v[118:121]
	v_mfma_f32_16x16x32_bf16 v[114:117], v[164:167], v[204:207], v[114:117]
	v_mfma_f32_16x16x32_bf16 v[110:113], v[146:149], v[212:215], v[110:113]
	v_mfma_f32_16x16x32_bf16 v[106:109], v[164:167], v[212:215], v[106:109]
	v_mfma_f32_16x16x32_bf16 v[102:105], v[146:149], v[220:223], v[102:105]
	v_mfma_f32_16x16x32_bf16 v[98:101], v[164:167], v[220:223], v[98:101]
	s_setprio 0
	s_setprio 1
	v_mfma_f32_16x16x32_bf16 v[62:65], v[168:171], v[184:187], v[62:65]
	v_mfma_f32_16x16x32_bf16 v[58:61], v[176:179], v[184:187], v[58:61]
	v_mfma_f32_16x16x32_bf16 v[54:57], v[168:171], v[192:195], v[54:57]
	v_mfma_f32_16x16x32_bf16 v[50:53], v[176:179], v[192:195], v[50:53]
	v_mfma_f32_16x16x32_bf16 v[46:49], v[168:171], v[208:211], v[46:49]
	v_mfma_f32_16x16x32_bf16 v[42:45], v[176:179], v[208:211], v[42:45]
	v_mfma_f32_16x16x32_bf16 v[38:41], v[168:171], v[216:219], v[38:41]
	v_mfma_f32_16x16x32_bf16 v[34:37], v[176:179], v[216:219], v[34:37]
	v_mfma_f32_16x16x32_bf16 v[62:65], v[172:175], v[188:191], v[62:65]
	v_mfma_f32_16x16x32_bf16 v[58:61], v[180:183], v[188:191], v[58:61]
	v_mfma_f32_16x16x32_bf16 v[54:57], v[172:175], v[204:207], v[54:57]
	v_mfma_f32_16x16x32_bf16 v[50:53], v[180:183], v[204:207], v[50:53]
	v_mfma_f32_16x16x32_bf16 v[46:49], v[172:175], v[212:215], v[46:49]
	v_mfma_f32_16x16x32_bf16 v[42:45], v[180:183], v[212:215], v[42:45]
	v_mfma_f32_16x16x32_bf16 v[38:41], v[172:175], v[220:223], v[38:41]
	v_mfma_f32_16x16x32_bf16 v[34:37], v[180:183], v[220:223], v[34:37]
	s_setprio 2
	s_barrier
	s_add_i32 s65, s65, s43
	v_lshl_add_u64 v[150:151], s[62:63], 0, v[132:133]
	s_mov_b32 m0, s65
	ds_read_b128 v[184:187], v160 offset:16384
	ds_read_b128 v[188:191], v160 offset:17408
	ds_read_b128 v[192:195], v160 offset:18432
	ds_read_b128 v[204:207], v160 offset:19456
	ds_read_b128 v[208:211], v160 offset:20480
	ds_read_b128 v[212:215], v160 offset:21504
	ds_read_b128 v[216:219], v160 offset:22528
	ds_read_b128 v[220:223], v160 offset:23552
	global_load_lds_dwordx4 v[150:151], off
	s_add_i32 m0, s65, 0x2000
	v_lshl_add_u64 v[196:197], s[62:63], 0, v[136:137]
	s_add_u32 s62, s62, s8
	s_addc_u32 s63, s63, s9
	s_add_i32 s65, s66, s43
	global_load_lds_dwordx4 v[196:197], off
	v_lshl_add_u64 v[200:201], s[62:63], 0, v[132:133]
	s_mov_b32 m0, s65
	v_lshl_add_u64 v[224:225], s[62:63], 0, v[136:137]
	global_load_lds_dwordx4 v[200:201], off
	s_add_i32 m0, s65, 0x2000
	v_lshl_add_u64 v[226:227], s[6:7], 0, v[130:131]
	global_load_lds_dwordx4 v[224:225], off
	s_mov_b32 m0, s45
	v_lshl_add_u64 v[228:229], s[6:7], 0, v[134:135]
	global_load_lds_dwordx4 v[226:227], off
	s_mov_b32 m0, s46
	s_nop 0
	global_load_lds_dwordx4 v[228:229], off
	s_waitcnt vmcnt(8)
	s_waitcnt lgkmcnt(0)
	s_barrier
; #define PG8_STAGE(bufoff, gbase, voff) do { _Pragma("unroll") for (int _i = 0; _i < 2; ++_i) \
;         __builtin_amdgcn_global_load_lds((const unsigned*)((const char*)(gbase) + (voff)[_i]), (PG8_LAS unsigned*)(lds + (bufoff) + ldsw + _i * 8192), 16, 0, 0); } while (0)
; #define PG8_WAIT_V(n) asm volatile("s_waitcnt vmcnt(" #n ")" ::: "memory")
; #define PG8_WAIT_L(n) asm volatile("s_waitcnt lgkmcnt(" #n ")" ::: "memory")
; #define PG8_BAR __builtin_amdgcn_s_barrier()
; #define PG8_SCHED __builtin_amdgcn_sched_barrier(0)
; template <class Epi, class Sched, bool ALIGN_EPI = false, bool SP2 = false, bool F8 = false>
; __device__ __forceinline__ void gemm_phase(PG8_LAS unsigned char* lds, const Gemm g, const Sched& S, const Epi& E, const int tidb  ) {
;     ...
;             PG8_WAIT_V(8); PG8_WAIT_L(0); PG8_BAR; PG8_MMA(1, 0, At, B0); PG8_MMA(1, 1, At, B1); PG8_BAR; PG8_SCHED;
;             PG8_LDB(B0, 1, 0); PG8_LDB(B1, 1, 1); PG8_SCHED; PG8_LDA(At, 1, 0); PG8_STAGE(PG8_SA(0, 1), a2 + hstep, voffA);
;             PG8_WAIT_V(8); PG8_WAIT_L(0); PG8_BAR; PG8_MMA(0, 0, At, B0); PG8_MMA(0, 1, At, B1); PG8_BAR; PG8_SCHED;
;             PG8_LDA(At, 1, 1); PG8_STAGE(PG8_SB(1, 0), b3, voffB); PG8_STAGE(PG8_SB(1, 1), b3 + hstep, voffB); PG8_STAGE(PG8_SA(1, 0), a3, voffA);
;             PG8_WAIT_V(8); PG8_WAIT_L(0); PG8_BAR; PG8_MMA(1, 0, At, B0); PG8_MMA(1, 1, At, B1); PG8_BAR; PG8_SCHED;
	s_setprio 1
	s_waitcnt lgkmcnt(0)
	v_mfma_f32_16x16x32_bf16 v[94:97], v[142:145], v[184:187], v[94:97]
	v_mfma_f32_16x16x32_bf16 v[90:93], v[154:157], v[184:187], v[90:93]
	v_mfma_f32_16x16x32_bf16 v[86:89], v[142:145], v[192:195], v[86:89]
	v_mfma_f32_16x16x32_bf16 v[82:85], v[154:157], v[192:195], v[82:85]
	v_mfma_f32_16x16x32_bf16 v[78:81], v[142:145], v[208:211], v[78:81]
	v_mfma_f32_16x16x32_bf16 v[74:77], v[154:157], v[208:211], v[74:77]
	v_mfma_f32_16x16x32_bf16 v[70:73], v[142:145], v[216:219], v[70:73]
	v_mfma_f32_16x16x32_bf16 v[66:69], v[154:157], v[216:219], v[66:69]
	v_mfma_f32_16x16x32_bf16 v[94:97], v[146:149], v[188:191], v[94:97]
	v_mfma_f32_16x16x32_bf16 v[90:93], v[164:167], v[188:191], v[90:93]
	v_mfma_f32_16x16x32_bf16 v[86:89], v[146:149], v[204:207], v[86:89]
	v_mfma_f32_16x16x32_bf16 v[82:85], v[164:167], v[204:207], v[82:85]
	v_mfma_f32_16x16x32_bf16 v[78:81], v[146:149], v[212:215], v[78:81]
	v_mfma_f32_16x16x32_bf16 v[74:77], v[164:167], v[212:215], v[74:77]
	v_mfma_f32_16x16x32_bf16 v[70:73], v[146:149], v[220:223], v[70:73]
	v_mfma_f32_16x16x32_bf16 v[66:69], v[164:167], v[220:223], v[66:69]
	s_setprio 0
	s_setprio 1
	v_mfma_f32_16x16x32_bf16 v[30:33], v[168:171], v[184:187], v[30:33]
	v_mfma_f32_16x16x32_bf16 v[26:29], v[176:179], v[184:187], v[26:29]
	v_mfma_f32_16x16x32_bf16 v[22:25], v[168:171], v[192:195], v[22:25]
	v_mfma_f32_16x16x32_bf16 v[18:21], v[176:179], v[192:195], v[18:21]
	v_mfma_f32_16x16x32_bf16 v[14:17], v[168:171], v[208:211], v[14:17]
	v_mfma_f32_16x16x32_bf16 v[10:13], v[176:179], v[208:211], v[10:13]
	v_mfma_f32_16x16x32_bf16 v[6:9], v[168:171], v[216:219], v[6:9]
	v_mfma_f32_16x16x32_bf16 v[2:5], v[176:179], v[216:219], v[2:5]
	v_mfma_f32_16x16x32_bf16 v[30:33], v[172:175], v[188:191], v[30:33]
	v_mfma_f32_16x16x32_bf16 v[26:29], v[180:183], v[188:191], v[26:29]
	v_mfma_f32_16x16x32_bf16 v[22:25], v[172:175], v[204:207], v[22:25]
	v_mfma_f32_16x16x32_bf16 v[18:21], v[180:183], v[204:207], v[18:21]
	v_mfma_f32_16x16x32_bf16 v[14:17], v[172:175], v[212:215], v[14:17]
	v_mfma_f32_16x16x32_bf16 v[10:13], v[180:183], v[212:215], v[10:13]
	v_mfma_f32_16x16x32_bf16 v[6:9], v[172:175], v[220:223], v[6:9]
	v_mfma_f32_16x16x32_bf16 v[2:5], v[180:183], v[220:223], v[2:5]
	s_setprio 2
	s_barrier
	s_add_i32 s62, 0, 0x18000
	v_add_u32_e32 v0, s62, v159
	s_add_i32 s63, 0, 0x1c000
	ds_read_b128 v[142:145], v0
	ds_read_b128 v[146:149], v0 offset:1024
	ds_read_b128 v[154:157], v0 offset:2048
	ds_read_b128 v[164:167], v0 offset:3072
	v_add_u32_e32 v0, s63, v159
	ds_read_b128 v[168:171], v0
	ds_read_b128 v[172:175], v0 offset:1024
	ds_read_b128 v[176:179], v0 offset:2048
	ds_read_b128 v[180:183], v0 offset:3072
	s_add_u32 s6, s6, s8
	s_addc_u32 s7, s7, s9
	s_mov_b32 m0, s47
	v_lshl_add_u64 v[230:231], s[6:7], 0, v[130:131]
	ds_read_b128 v[184:187], v160 offset:32768
	ds_read_b128 v[188:191], v160 offset:33792
	ds_read_b128 v[192:195], v160 offset:34816
	ds_read_b128 v[204:207], v160 offset:35840
	ds_read_b128 v[208:211], v160 offset:36864
	ds_read_b128 v[212:215], v160 offset:37888
	ds_read_b128 v[216:219], v160 offset:38912
	ds_read_b128 v[220:223], v160 offset:39936
	global_load_lds_dwordx4 v[230:231], off
	v_lshl_add_u64 v[230:231], s[6:7], 0, v[134:135]
	s_mov_b32 m0, s48
	s_nop 0
	global_load_lds_dwordx4 v[230:231], off
	s_waitcnt vmcnt(8)
	s_waitcnt lgkmcnt(0)
	s_barrier
	s_setprio 1
	s_waitcnt lgkmcnt(0)
	v_mfma_f32_16x16x32_bf16 v[126:129], v[142:145], v[184:187], v[126:129]
	v_mfma_f32_16x16x32_bf16 v[122:125], v[154:157], v[184:187], v[122:125]
	v_mfma_f32_16x16x32_bf16 v[118:121], v[142:145], v[192:195], v[118:121]
	v_mfma_f32_16x16x32_bf16 v[114:117], v[154:157], v[192:195], v[114:117]
	v_mfma_f32_16x16x32_bf16 v[110:113], v[142:145], v[208:211], v[110:113]
	v_mfma_f32_16x16x32_bf16 v[106:109], v[154:157], v[208:211], v[106:109]
	v_mfma_f32_16x16x32_bf16 v[102:105], v[142:145], v[216:219], v[102:105]
	v_mfma_f32_16x16x32_bf16 v[98:101], v[154:157], v[216:219], v[98:101]
	v_mfma_f32_16x16x32_bf16 v[126:129], v[146:149], v[188:191], v[126:129]
	v_mfma_f32_16x16x32_bf16 v[122:125], v[164:167], v[188:191], v[122:125]
	v_mfma_f32_16x16x32_bf16 v[118:121], v[146:149], v[204:207], v[118:121]
	v_mfma_f32_16x16x32_bf16 v[114:117], v[164:167], v[204:207], v[114:117]
	v_mfma_f32_16x16x32_bf16 v[110:113], v[146:149], v[212:215], v[110:113]
	v_mfma_f32_16x16x32_bf16 v[106:109], v[164:167], v[212:215], v[106:109]
	v_mfma_f32_16x16x32_bf16 v[102:105], v[146:149], v[220:223], v[102:105]
	v_mfma_f32_16x16x32_bf16 v[98:101], v[164:167], v[220:223], v[98:101]
	s_setprio 0
	s_setprio 1
	v_mfma_f32_16x16x32_bf16 v[62:65], v[168:171], v[184:187], v[62:65]
	v_mfma_f32_16x16x32_bf16 v[58:61], v[176:179], v[184:187], v[58:61]
	v_mfma_f32_16x16x32_bf16 v[54:57], v[168:171], v[192:195], v[54:57]
	v_mfma_f32_16x16x32_bf16 v[50:53], v[176:179], v[192:195], v[50:53]
	v_mfma_f32_16x16x32_bf16 v[46:49], v[168:171], v[208:211], v[46:49]
	v_mfma_f32_16x16x32_bf16 v[42:45], v[176:179], v[208:211], v[42:45]
	v_mfma_f32_16x16x32_bf16 v[38:41], v[168:171], v[216:219], v[38:41]
	v_mfma_f32_16x16x32_bf16 v[34:37], v[176:179], v[216:219], v[34:37]
	v_mfma_f32_16x16x32_bf16 v[62:65], v[172:175], v[188:191], v[62:65]
	v_mfma_f32_16x16x32_bf16 v[58:61], v[180:183], v[188:191], v[58:61]
	v_mfma_f32_16x16x32_bf16 v[54:57], v[172:175], v[204:207], v[54:57]
	v_mfma_f32_16x16x32_bf16 v[50:53], v[180:183], v[204:207], v[50:53]
	v_mfma_f32_16x16x32_bf16 v[46:49], v[172:175], v[212:215], v[46:49]
	v_mfma_f32_16x16x32_bf16 v[42:45], v[180:183], v[212:215], v[42:45]
	v_mfma_f32_16x16x32_bf16 v[38:41], v[172:175], v[220:223], v[38:41]
	v_mfma_f32_16x16x32_bf16 v[34:37], v[180:183], v[220:223], v[34:37]
	s_setprio 2
	s_barrier
; #define PG8_STAGE(bufoff, gbase, voff) do { _Pragma("unroll") for (int _i = 0; _i < 2; ++_i) \
;         __builtin_amdgcn_global_load_lds((const unsigned*)((const char*)(gbase) + (voff)[_i]), (PG8_LAS unsigned*)(lds + (bufoff) + ldsw + _i * 8192), 16, 0, 0); } while (0)
; #define PG8_WAIT_V(n) asm volatile("s_waitcnt vmcnt(" #n ")" ::: "memory")
; #define PG8_WAIT_L(n) asm volatile("s_waitcnt lgkmcnt(" #n ")" ::: "memory")
; #define PG8_BAR __builtin_amdgcn_s_barrier()
; #define PG8_SCHED __builtin_amdgcn_sched_barrier(0)
; template <class Epi, class Sched, bool ALIGN_EPI = false, bool SP2 = false, bool F8 = false>
; __device__ __forceinline__ void gemm_phase(PG8_LAS unsigned char* lds, const Gemm g, const Sched& S, const Epi& E, const int tidb  ) {
;     ...
;             const char* a1 = cA + (size_t)(t + 1) * kstep;
;             const char* a2 = last ? nA : cA + (size_t)(t + 2) * kstep; const char* b2 = last ? nB : cB + (size_t)(t + 2) * kstep;
;             const char* a3 = a2 + kstep; const char* b3 = b2 + kstep;
;             if (last && has_next) S.a_ready(nxt);
;             if constexpr (SP2) {
;             PG8_LDB(B0, 0, 0); PG8_LDB(B1, 0, 1); PG8_SCHED; PG8_LDA(At, 0, 0); PG8_STAGE(PG8_SA(1, 1), a1 + hstep, voffA);
;             PG8_WAIT_V(8); PG8_WAIT_L(0); PG8_BAR; PG8_MMA(0, 0, At, B0); PG8_MMA(0, 1, At, B1); PG8_BAR; PG8_SCHED;
;             PG8_LDA(At, 0, 1); PG8_STAGE(PG8_SB(0, 0), b2, voffB); PG8_STAGE(PG8_SB(0, 1), b2 + hstep, voffB); PG8_STAGE(PG8_SA(0, 0), a2, voffA);
;             PG8_WAIT_V(8); PG8_WAIT_L(0); PG8_BAR; PG8_MMA(1, 0, At, B0); PG8_MMA(1, 1, At, B1); PG8_BAR; PG8_SCHED;
;             PG8_LDB(B0, 1, 0); PG8_LDB(B1, 1, 1); PG8_SCHED; PG8_LDA(At, 1, 0); PG8_STAGE(PG8_SA(0, 1), a2 + hstep, voffA);
;             PG8_WAIT_V(8); PG8_WAIT_L(0); PG8_BAR; PG8_MMA(0, 0, At, B0); PG8_MMA(0, 1, At, B1); PG8_BAR; PG8_SCHED;
;             PG8_LDA(At, 1, 1); PG8_STAGE(PG8_SB(1, 0), b3, voffB); PG8_STAGE(PG8_SB(1, 1), b3 + hstep, voffB); PG8_STAGE(PG8_SA(1, 0), a3, voffA);
;             PG8_WAIT_V(8); PG8_WAIT_L(0); PG8_BAR; PG8_MMA(1, 0, At, B0); PG8_MMA(1, 1, At, B1); PG8_BAR; PG8_SCHED;
	s_add_i32 s6, s62, s43
	v_lshl_add_u64 v[150:151], v[150:151], 0, s[92:93]
	s_mov_b32 m0, s6
	ds_read_b128 v[184:187], v160 offset:49152
	ds_read_b128 v[188:191], v160 offset:50176
	ds_read_b128 v[192:195], v160 offset:51200
	ds_read_b128 v[204:207], v160 offset:52224
	ds_read_b128 v[208:211], v160 offset:53248
	ds_read_b128 v[212:215], v160 offset:54272
	ds_read_b128 v[216:219], v160 offset:55296
	ds_read_b128 v[220:223], v160 offset:56320
	global_load_lds_dwordx4 v[150:151], off
	v_lshl_add_u64 v[150:151], v[196:197], 0, s[92:93]
	s_add_i32 m0, s6, 0x2000
	s_add_i32 s6, s63, s43
	global_load_lds_dwordx4 v[150:151], off
	v_lshl_add_u64 v[150:151], v[200:201], 0, s[92:93]
	s_mov_b32 m0, s6
	s_nop 0
	global_load_lds_dwordx4 v[150:151], off
	v_lshl_add_u64 v[150:151], v[224:225], 0, s[92:93]
	s_add_i32 m0, s6, 0x2000
	s_nop 0
	global_load_lds_dwordx4 v[150:151], off
	v_lshl_add_u64 v[150:151], v[226:227], 0, s[92:93]
	s_mov_b32 m0, s49
	s_nop 0
	global_load_lds_dwordx4 v[150:151], off
	v_lshl_add_u64 v[150:151], v[228:229], 0, s[92:93]
	s_mov_b32 m0, s50
	s_nop 0
	global_load_lds_dwordx4 v[150:151], off
	s_waitcnt vmcnt(8)
	s_waitcnt lgkmcnt(0)
	s_barrier
	s_setprio 1
	s_waitcnt lgkmcnt(0)
	v_mfma_f32_16x16x32_bf16 v[94:97], v[142:145], v[184:187], v[94:97]
	v_mfma_f32_16x16x32_bf16 v[90:93], v[154:157], v[184:187], v[90:93]
	v_mfma_f32_16x16x32_bf16 v[86:89], v[142:145], v[192:195], v[86:89]
	v_mfma_f32_16x16x32_bf16 v[82:85], v[154:157], v[192:195], v[82:85]
	v_mfma_f32_16x16x32_bf16 v[78:81], v[142:145], v[208:211], v[78:81]
	v_mfma_f32_16x16x32_bf16 v[74:77], v[154:157], v[208:211], v[74:77]
	v_mfma_f32_16x16x32_bf16 v[70:73], v[142:145], v[216:219], v[70:73]
	v_mfma_f32_16x16x32_bf16 v[66:69], v[154:157], v[216:219], v[66:69]
	v_mfma_f32_16x16x32_bf16 v[94:97], v[146:149], v[188:191], v[94:97]
	v_mfma_f32_16x16x32_bf16 v[90:93], v[164:167], v[188:191], v[90:93]
	v_mfma_f32_16x16x32_bf16 v[86:89], v[146:149], v[204:207], v[86:89]
	v_mfma_f32_16x16x32_bf16 v[82:85], v[164:167], v[204:207], v[82:85]
	v_mfma_f32_16x16x32_bf16 v[78:81], v[146:149], v[212:215], v[78:81]
	v_mfma_f32_16x16x32_bf16 v[74:77], v[164:167], v[212:215], v[74:77]
	v_mfma_f32_16x16x32_bf16 v[70:73], v[146:149], v[220:223], v[70:73]
	v_mfma_f32_16x16x32_bf16 v[66:69], v[164:167], v[220:223], v[66:69]
	s_setprio 0
	s_setprio 1
	v_mfma_f32_16x16x32_bf16 v[30:33], v[168:171], v[184:187], v[30:33]
	v_mfma_f32_16x16x32_bf16 v[26:29], v[176:179], v[184:187], v[26:29]
	v_mfma_f32_16x16x32_bf16 v[22:25], v[168:171], v[192:195], v[22:25]
	v_mfma_f32_16x16x32_bf16 v[18:21], v[176:179], v[192:195], v[18:21]
	v_mfma_f32_16x16x32_bf16 v[14:17], v[168:171], v[208:211], v[14:17]
	v_mfma_f32_16x16x32_bf16 v[10:13], v[176:179], v[208:211], v[10:13]
	v_mfma_f32_16x16x32_bf16 v[6:9], v[168:171], v[216:219], v[6:9]
	v_mfma_f32_16x16x32_bf16 v[2:5], v[176:179], v[216:219], v[2:5]
	v_mfma_f32_16x16x32_bf16 v[30:33], v[172:175], v[188:191], v[30:33]
	v_mfma_f32_16x16x32_bf16 v[26:29], v[180:183], v[188:191], v[26:29]
	v_mfma_f32_16x16x32_bf16 v[22:25], v[172:175], v[204:207], v[22:25]
	v_mfma_f32_16x16x32_bf16 v[18:21], v[180:183], v[204:207], v[18:21]
	v_mfma_f32_16x16x32_bf16 v[14:17], v[172:175], v[212:215], v[14:17]
	v_mfma_f32_16x16x32_bf16 v[10:13], v[180:183], v[212:215], v[10:13]
	v_mfma_f32_16x16x32_bf16 v[6:9], v[172:175], v[220:223], v[6:9]
	v_mfma_f32_16x16x32_bf16 v[2:5], v[180:183], v[220:223], v[2:5]
	s_setprio 2
	s_barrier
	s_add_u32 s4, s4, 0x100
	s_addc_u32 s5, s5, 0
	s_add_u32 s28, s28, 0x100
	s_addc_u32 s29, s29, 0
	s_cmp_ge_i32 s61, s51
	s_mov_b32 s6, s61
	s_cbranch_scc0 .LBB0_465

; #define PG8_STAGE(bufoff, gbase, voff) do { _Pragma("unroll") for (int _i = 0; _i < 2; ++_i) \
;         __builtin_amdgcn_global_load_lds((const unsigned*)((const char*)(gbase) + (voff)[_i]), (PG8_LAS unsigned*)(lds + (bufoff) + ldsw + _i * 8192), 16, 0, 0); } while (0)
; #define PG8_WAIT_V(n) asm volatile("s_waitcnt vmcnt(" #n ")" ::: "memory")
; #define PG8_WAIT_L(n) asm volatile("s_waitcnt lgkmcnt(" #n ")" ::: "memory")
; #define PG8_BAR __builtin_amdgcn_s_barrier()
; #define PG8_SCHED __builtin_amdgcn_sched_barrier(0)
; template <class Epi, class Sched, bool ALIGN_EPI = false, bool SP2 = false, bool F8 = false>
; __device__ __forceinline__ void gemm_phase(PG8_LAS unsigned char* lds, const Gemm g, const Sched& S, const Epi& E, const int tidb  ) {
;     ...
;             const bool last = (t == nt - 2);
;             if constexpr (Epi::PREFETCH) { if (t == 0) E.prefetch(cur, wid, lane); }
;             const char* a1 = cA + (size_t)(t + 1) * kstep;
;             const char* a2 = last ? nA : cA + (size_t)(t + 2) * kstep; const char* b2 = last ? nB : cB + (size_t)(t + 2) * kstep;
;             const char* a3 = a2 + kstep; const char* b3 = b2 + kstep;
;             if (last && has_next) S.a_ready(nxt);
;             if constexpr (SP2) {
;             PG8_LDB(B0, 0, 0); PG8_LDB(B1, 0, 1); PG8_SCHED; PG8_LDA(At, 0, 0); PG8_STAGE(PG8_SA(1, 1), a1 + hstep, voffA);
;             PG8_WAIT_V(8); PG8_WAIT_L(0); PG8_BAR; PG8_MMA(0, 0, At, B0); PG8_MMA(0, 1, At, B1); PG8_BAR; PG8_SCHED;
;             PG8_LDA(At, 0, 1); PG8_STAGE(PG8_SB(0, 0), b2, voffB); PG8_STAGE(PG8_SB(0, 1), b2 + hstep, voffB); PG8_STAGE(PG8_SA(0, 0), a2, voffA);
;             PG8_WAIT_V(8); PG8_WAIT_L(0); PG8_BAR; PG8_MMA(1, 0, At, B0); PG8_MMA(1, 1, At, B1); PG8_BAR; PG8_SCHED;
.LBB0_943:
	s_add_i32 s60, s26, 2
	s_add_u32 s61, s24, 0x80
	s_addc_u32 s27, s25, 0
	s_add_i32 s65, 0, 0x10000
	s_cmp_eq_u32 s45, s26
	s_cselect_b32 s27, s7, s27
	s_cselect_b32 s26, s6, s61
	s_cselect_b32 s63, s23, s59
	s_cselect_b32 s62, s22, s58
	s_add_i32 s61, 0, 0x14000
	v_add_u32_e32 v142, s65, v196
	v_add_u32_e32 v158, s61, v196
	ds_read_b128 v[130:133], v142
	ds_read_b128 v[134:137], v142 offset:1024
	ds_read_b128 v[138:141], v142 offset:2048
	ds_read_b128 v[142:145], v142 offset:3072
	ds_read_b128 v[146:149], v158
	ds_read_b128 v[150:153], v158 offset:1024
	ds_read_b128 v[154:157], v158 offset:2048
	ds_read_b128 v[158:161], v158 offset:3072
	v_lshl_add_u64 v[198:199], s[24:25], 0, v[210:211]
	s_add_i32 m0, s1, 0xc000
	ds_read_b128 v[164:167], v200
	ds_read_b128 v[168:171], v200 offset:1024
	ds_read_b128 v[172:175], v200 offset:2048
	ds_read_b128 v[176:179], v200 offset:3072
	ds_read_b128 v[180:183], v200 offset:4096
	ds_read_b128 v[184:187], v200 offset:5120
	ds_read_b128 v[188:191], v200 offset:6144
	ds_read_b128 v[192:195], v200 offset:7168
	global_load_lds_dwordx4 v[198:199], off
	v_lshl_add_u64 v[198:199], s[24:25], 0, v[212:213]
	s_add_i32 m0, s1, 0xe000
	s_nop 0
	global_load_lds_dwordx4 v[198:199], off
	s_waitcnt vmcnt(8)
	s_waitcnt lgkmcnt(0)
	s_barrier
	s_setprio 1
	s_waitcnt lgkmcnt(0)
	v_mfma_f32_16x16x32_bf16 v[126:129], v[130:133], v[164:167], v[126:129]
	v_mfma_f32_16x16x32_bf16 v[122:125], v[138:141], v[164:167], v[122:125]
	v_mfma_f32_16x16x32_bf16 v[110:113], v[130:133], v[172:175], v[110:113]
	v_mfma_f32_16x16x32_bf16 v[106:109], v[138:141], v[172:175], v[106:109]
	v_mfma_f32_16x16x32_bf16 v[94:97], v[130:133], v[180:183], v[94:97]
	v_mfma_f32_16x16x32_bf16 v[90:93], v[138:141], v[180:183], v[90:93]
	v_mfma_f32_16x16x32_bf16 v[78:81], v[130:133], v[188:191], v[78:81]
	v_mfma_f32_16x16x32_bf16 v[74:77], v[138:141], v[188:191], v[74:77]
	v_mfma_f32_16x16x32_bf16 v[126:129], v[134:137], v[168:171], v[126:129]
	v_mfma_f32_16x16x32_bf16 v[122:125], v[142:145], v[168:171], v[122:125]
	v_mfma_f32_16x16x32_bf16 v[110:113], v[134:137], v[176:179], v[110:113]
	v_mfma_f32_16x16x32_bf16 v[106:109], v[142:145], v[176:179], v[106:109]
	v_mfma_f32_16x16x32_bf16 v[94:97], v[134:137], v[184:187], v[94:97]
	v_mfma_f32_16x16x32_bf16 v[90:93], v[142:145], v[184:187], v[90:93]
	v_mfma_f32_16x16x32_bf16 v[78:81], v[134:137], v[192:195], v[78:81]
	v_mfma_f32_16x16x32_bf16 v[74:77], v[142:145], v[192:195], v[74:77]
	s_setprio 0
	s_setprio 1
	v_mfma_f32_16x16x32_bf16 v[118:121], v[146:149], v[164:167], v[118:121]
	v_mfma_f32_16x16x32_bf16 v[114:117], v[154:157], v[164:167], v[114:117]
	v_mfma_f32_16x16x32_bf16 v[102:105], v[146:149], v[172:175], v[102:105]
	v_mfma_f32_16x16x32_bf16 v[98:101], v[154:157], v[172:175], v[98:101]
	v_mfma_f32_16x16x32_bf16 v[86:89], v[146:149], v[180:183], v[86:89]
	v_mfma_f32_16x16x32_bf16 v[82:85], v[154:157], v[180:183], v[82:85]
	v_mfma_f32_16x16x32_bf16 v[70:73], v[146:149], v[188:191], v[70:73]
	v_mfma_f32_16x16x32_bf16 v[66:69], v[154:157], v[188:191], v[66:69]
	v_mfma_f32_16x16x32_bf16 v[118:121], v[150:153], v[168:171], v[118:121]
	v_mfma_f32_16x16x32_bf16 v[114:117], v[158:161], v[168:171], v[114:117]
	v_mfma_f32_16x16x32_bf16 v[102:105], v[150:153], v[176:179], v[102:105]
	v_mfma_f32_16x16x32_bf16 v[98:101], v[158:161], v[176:179], v[98:101]
	v_mfma_f32_16x16x32_bf16 v[86:89], v[150:153], v[184:187], v[86:89]
	v_mfma_f32_16x16x32_bf16 v[82:85], v[158:161], v[184:187], v[82:85]
	v_mfma_f32_16x16x32_bf16 v[70:73], v[150:153], v[192:195], v[70:73]
	v_mfma_f32_16x16x32_bf16 v[66:69], v[158:161], v[192:195], v[66:69]
	s_setprio 2
	s_barrier
	s_add_i32 s65, s65, s0
	v_lshl_add_u64 v[198:199], s[62:63], 0, v[0:1]
	s_mov_b32 m0, s65
	ds_read_b128 v[164:167], v200 offset:16384
	ds_read_b128 v[168:171], v200 offset:17408
	ds_read_b128 v[172:175], v200 offset:18432
	ds_read_b128 v[176:179], v200 offset:19456
	ds_read_b128 v[180:183], v200 offset:20480
	ds_read_b128 v[184:187], v200 offset:21504
	ds_read_b128 v[188:191], v200 offset:22528
	ds_read_b128 v[192:195], v200 offset:23552
	global_load_lds_dwordx4 v[198:199], off
	s_add_i32 m0, s65, 0x2000
	v_lshl_add_u64 v[214:215], s[62:63], 0, v[208:209]
	s_add_u32 s62, s62, s10
	s_addc_u32 s63, s63, s11
	s_add_i32 s61, s61, s0
	global_load_lds_dwordx4 v[214:215], off
	v_lshl_add_u64 v[216:217], s[62:63], 0, v[0:1]
	s_mov_b32 m0, s61
	v_lshl_add_u64 v[218:219], s[62:63], 0, v[208:209]
	global_load_lds_dwordx4 v[216:217], off
	s_add_i32 m0, s61, 0x2000
	v_lshl_add_u64 v[220:221], s[26:27], 0, v[204:205]
	global_load_lds_dwordx4 v[218:219], off
	s_mov_b32 m0, s1
	v_lshl_add_u64 v[222:223], s[26:27], 0, v[206:207]
	global_load_lds_dwordx4 v[220:221], off
	s_mov_b32 m0, s28
	s_nop 0
	global_load_lds_dwordx4 v[222:223], off
	s_waitcnt vmcnt(8)
	s_waitcnt lgkmcnt(0)
	s_barrier
; #define PG8_STAGE(bufoff, gbase, voff) do { _Pragma("unroll") for (int _i = 0; _i < 2; ++_i) \
;         __builtin_amdgcn_global_load_lds((const unsigned*)((const char*)(gbase) + (voff)[_i]), (PG8_LAS unsigned*)(lds + (bufoff) + ldsw + _i * 8192), 16, 0, 0); } while (0)
; #define PG8_WAIT_V(n) asm volatile("s_waitcnt vmcnt(" #n ")" ::: "memory")
; #define PG8_WAIT_L(n) asm volatile("s_waitcnt lgkmcnt(" #n ")" ::: "memory")
; #define PG8_BAR __builtin_amdgcn_s_barrier()
; #define PG8_SCHED __builtin_amdgcn_sched_barrier(0)
; template <class Epi, class Sched, bool ALIGN_EPI = false, bool SP2 = false, bool F8 = false>
; __device__ __forceinline__ void gemm_phase(PG8_LAS unsigned char* lds, const Gemm g, const Sched& S, const Epi& E, const int tidb  ) {
;     ...
;             PG8_WAIT_V(8); PG8_WAIT_L(0); PG8_BAR; PG8_MMA(1, 0, At, B0); PG8_MMA(1, 1, At, B1); PG8_BAR; PG8_SCHED;
;             PG8_LDB(B0, 1, 0); PG8_LDB(B1, 1, 1); PG8_SCHED; PG8_LDA(At, 1, 0); PG8_STAGE(PG8_SA(0, 1), a2 + hstep, voffA);
;             PG8_WAIT_V(8); PG8_WAIT_L(0); PG8_BAR; PG8_MMA(0, 0, At, B0); PG8_MMA(0, 1, At, B1); PG8_BAR; PG8_SCHED;
	s_setprio 1
	s_waitcnt lgkmcnt(0)
	v_mfma_f32_16x16x32_bf16 v[62:65], v[130:133], v[164:167], v[62:65]
	v_mfma_f32_16x16x32_bf16 v[58:61], v[138:141], v[164:167], v[58:61]
	v_mfma_f32_16x16x32_bf16 v[46:49], v[130:133], v[172:175], v[46:49]
	v_mfma_f32_16x16x32_bf16 v[42:45], v[138:141], v[172:175], v[42:45]
	v_mfma_f32_16x16x32_bf16 v[30:33], v[130:133], v[180:183], v[30:33]
	v_mfma_f32_16x16x32_bf16 v[26:29], v[138:141], v[180:183], v[26:29]
	v_mfma_f32_16x16x32_bf16 v[14:17], v[130:133], v[188:191], v[14:17]
	v_mfma_f32_16x16x32_bf16 v[10:13], v[138:141], v[188:191], v[10:13]
	v_mfma_f32_16x16x32_bf16 v[62:65], v[134:137], v[168:171], v[62:65]
	v_mfma_f32_16x16x32_bf16 v[58:61], v[142:145], v[168:171], v[58:61]
	v_mfma_f32_16x16x32_bf16 v[46:49], v[134:137], v[176:179], v[46:49]
	v_mfma_f32_16x16x32_bf16 v[42:45], v[142:145], v[176:179], v[42:45]
	v_mfma_f32_16x16x32_bf16 v[30:33], v[134:137], v[184:187], v[30:33]
	v_mfma_f32_16x16x32_bf16 v[26:29], v[142:145], v[184:187], v[26:29]
	v_mfma_f32_16x16x32_bf16 v[14:17], v[134:137], v[192:195], v[14:17]
	v_mfma_f32_16x16x32_bf16 v[10:13], v[142:145], v[192:195], v[10:13]
	s_setprio 0
	s_setprio 1
	v_mfma_f32_16x16x32_bf16 v[54:57], v[146:149], v[164:167], v[54:57]
	v_mfma_f32_16x16x32_bf16 v[50:53], v[154:157], v[164:167], v[50:53]
	v_mfma_f32_16x16x32_bf16 v[38:41], v[146:149], v[172:175], v[38:41]
	v_mfma_f32_16x16x32_bf16 v[34:37], v[154:157], v[172:175], v[34:37]
	v_mfma_f32_16x16x32_bf16 v[22:25], v[146:149], v[180:183], v[22:25]
	v_mfma_f32_16x16x32_bf16 v[18:21], v[154:157], v[180:183], v[18:21]
	v_mfma_f32_16x16x32_bf16 v[6:9], v[146:149], v[188:191], v[6:9]
	v_mfma_f32_16x16x32_bf16 v[2:5], v[154:157], v[188:191], v[2:5]
	v_mfma_f32_16x16x32_bf16 v[54:57], v[150:153], v[168:171], v[54:57]
	v_mfma_f32_16x16x32_bf16 v[50:53], v[158:161], v[168:171], v[50:53]
	v_mfma_f32_16x16x32_bf16 v[38:41], v[150:153], v[176:179], v[38:41]
	v_mfma_f32_16x16x32_bf16 v[34:37], v[158:161], v[176:179], v[34:37]
	v_mfma_f32_16x16x32_bf16 v[22:25], v[150:153], v[184:187], v[22:25]
	v_mfma_f32_16x16x32_bf16 v[18:21], v[158:161], v[184:187], v[18:21]
	v_mfma_f32_16x16x32_bf16 v[6:9], v[150:153], v[192:195], v[6:9]
	v_mfma_f32_16x16x32_bf16 v[2:5], v[158:161], v[192:195], v[2:5]
	s_setprio 2
	s_barrier
	s_add_i32 s61, 0, 0x18000
	s_add_i32 s62, 0, 0x1c000
	v_add_u32_e32 v142, s61, v196
	v_add_u32_e32 v158, s62, v196
	ds_read_b128 v[130:133], v142
	ds_read_b128 v[134:137], v142 offset:1024
	ds_read_b128 v[138:141], v142 offset:2048
	ds_read_b128 v[142:145], v142 offset:3072
	ds_read_b128 v[146:149], v158
	ds_read_b128 v[150:153], v158 offset:1024
	ds_read_b128 v[154:157], v158 offset:2048
	ds_read_b128 v[158:161], v158 offset:3072
	s_add_u32 s26, s26, s10
	s_addc_u32 s27, s27, s11
	s_mov_b32 m0, s29
	v_lshl_add_u64 v[224:225], s[26:27], 0, v[204:205]
	ds_read_b128 v[164:167], v200 offset:32768
	ds_read_b128 v[168:171], v200 offset:33792
	ds_read_b128 v[172:175], v200 offset:34816
	ds_read_b128 v[176:179], v200 offset:35840
	ds_read_b128 v[180:183], v200 offset:36864
	ds_read_b128 v[184:187], v200 offset:37888
	ds_read_b128 v[188:191], v200 offset:38912
	ds_read_b128 v[192:195], v200 offset:39936
	global_load_lds_dwordx4 v[224:225], off
	v_lshl_add_u64 v[224:225], s[26:27], 0, v[206:207]
	s_mov_b32 m0, s36
	s_nop 0
	global_load_lds_dwordx4 v[224:225], off
	s_waitcnt vmcnt(8)
	s_waitcnt lgkmcnt(0)
	s_barrier
	s_setprio 1
	s_waitcnt lgkmcnt(0)
	v_mfma_f32_16x16x32_bf16 v[126:129], v[130:133], v[164:167], v[126:129]
	v_mfma_f32_16x16x32_bf16 v[122:125], v[138:141], v[164:167], v[122:125]
	v_mfma_f32_16x16x32_bf16 v[110:113], v[130:133], v[172:175], v[110:113]
	v_mfma_f32_16x16x32_bf16 v[106:109], v[138:141], v[172:175], v[106:109]
	v_mfma_f32_16x16x32_bf16 v[94:97], v[130:133], v[180:183], v[94:97]
	v_mfma_f32_16x16x32_bf16 v[90:93], v[138:141], v[180:183], v[90:93]
	v_mfma_f32_16x16x32_bf16 v[78:81], v[130:133], v[188:191], v[78:81]
	v_mfma_f32_16x16x32_bf16 v[74:77], v[138:141], v[188:191], v[74:77]
	v_mfma_f32_16x16x32_bf16 v[126:129], v[134:137], v[168:171], v[126:129]
	v_mfma_f32_16x16x32_bf16 v[122:125], v[142:145], v[168:171], v[122:125]
	v_mfma_f32_16x16x32_bf16 v[110:113], v[134:137], v[176:179], v[110:113]
	v_mfma_f32_16x16x32_bf16 v[106:109], v[142:145], v[176:179], v[106:109]
	v_mfma_f32_16x16x32_bf16 v[94:97], v[134:137], v[184:187], v[94:97]
	v_mfma_f32_16x16x32_bf16 v[90:93], v[142:145], v[184:187], v[90:93]
	v_mfma_f32_16x16x32_bf16 v[78:81], v[134:137], v[192:195], v[78:81]
	v_mfma_f32_16x16x32_bf16 v[74:77], v[142:145], v[192:195], v[74:77]
	s_setprio 0
	s_setprio 1
	v_mfma_f32_16x16x32_bf16 v[118:121], v[146:149], v[164:167], v[118:121]
	v_mfma_f32_16x16x32_bf16 v[114:117], v[154:157], v[164:167], v[114:117]
	v_mfma_f32_16x16x32_bf16 v[102:105], v[146:149], v[172:175], v[102:105]
	v_mfma_f32_16x16x32_bf16 v[98:101], v[154:157], v[172:175], v[98:101]
	v_mfma_f32_16x16x32_bf16 v[86:89], v[146:149], v[180:183], v[86:89]
	v_mfma_f32_16x16x32_bf16 v[82:85], v[154:157], v[180:183], v[82:85]
	v_mfma_f32_16x16x32_bf16 v[70:73], v[146:149], v[188:191], v[70:73]
	v_mfma_f32_16x16x32_bf16 v[66:69], v[154:157], v[188:191], v[66:69]
	v_mfma_f32_16x16x32_bf16 v[118:121], v[150:153], v[168:171], v[118:121]
	v_mfma_f32_16x16x32_bf16 v[114:117], v[158:161], v[168:171], v[114:117]
	v_mfma_f32_16x16x32_bf16 v[102:105], v[150:153], v[176:179], v[102:105]
	v_mfma_f32_16x16x32_bf16 v[98:101], v[158:161], v[176:179], v[98:101]
	v_mfma_f32_16x16x32_bf16 v[86:89], v[150:153], v[184:187], v[86:89]
	v_mfma_f32_16x16x32_bf16 v[82:85], v[158:161], v[184:187], v[82:85]
	v_mfma_f32_16x16x32_bf16 v[70:73], v[150:153], v[192:195], v[70:73]
	v_mfma_f32_16x16x32_bf16 v[66:69], v[158:161], v[192:195], v[66:69]
	s_setprio 2
	s_barrier
; #define PG8_STAGE(bufoff, gbase, voff) do { _Pragma("unroll") for (int _i = 0; _i < 2; ++_i) \
;         __builtin_amdgcn_global_load_lds((const unsigned*)((const char*)(gbase) + (voff)[_i]), (PG8_LAS unsigned*)(lds + (bufoff) + ldsw + _i * 8192), 16, 0, 0); } while (0)
; #define PG8_WAIT_V(n) asm volatile("s_waitcnt vmcnt(" #n ")" ::: "memory")
; #define PG8_WAIT_L(n) asm volatile("s_waitcnt lgkmcnt(" #n ")" ::: "memory")
; #define PG8_BAR __builtin_amdgcn_s_barrier()
; #define PG8_SCHED __builtin_amdgcn_sched_barrier(0)
; template <class Epi, class Sched, bool ALIGN_EPI = false, bool SP2 = false, bool F8 = false>
; __device__ __forceinline__ void gemm_phase(PG8_LAS unsigned char* lds, const Gemm g, const Sched& S, const Epi& E, const int tidb  ) {
;     ...
;             PG8_LDA(At, 1, 1); PG8_STAGE(PG8_SB(1, 0), b3, voffB); PG8_STAGE(PG8_SB(1, 1), b3 + hstep, voffB); PG8_STAGE(PG8_SA(1, 0), a3, voffA);
;             PG8_WAIT_V(8); PG8_WAIT_L(0); PG8_BAR; PG8_MMA(1, 0, At, B0); PG8_MMA(1, 1, At, B1); PG8_BAR; PG8_SCHED;
	s_add_i32 s26, s61, s0
	v_lshl_add_u64 v[198:199], v[198:199], 0, s[92:93]
	s_mov_b32 m0, s26
	ds_read_b128 v[164:167], v200 offset:49152
	ds_read_b128 v[168:171], v200 offset:50176
	ds_read_b128 v[172:175], v200 offset:51200
	ds_read_b128 v[176:179], v200 offset:52224
	ds_read_b128 v[180:183], v200 offset:53248
	ds_read_b128 v[184:187], v200 offset:54272
	ds_read_b128 v[188:191], v200 offset:55296
	ds_read_b128 v[192:195], v200 offset:56320
	global_load_lds_dwordx4 v[198:199], off
	v_lshl_add_u64 v[198:199], v[214:215], 0, s[92:93]
	s_add_i32 m0, s26, 0x2000
	s_add_i32 s26, s62, s0
	global_load_lds_dwordx4 v[198:199], off
	v_lshl_add_u64 v[198:199], v[216:217], 0, s[92:93]
	s_mov_b32 m0, s26
	s_nop 0
	global_load_lds_dwordx4 v[198:199], off
	v_lshl_add_u64 v[198:199], v[218:219], 0, s[92:93]
	s_add_i32 m0, s26, 0x2000
	s_nop 0
	global_load_lds_dwordx4 v[198:199], off
	v_lshl_add_u64 v[198:199], v[220:221], 0, s[92:93]
	s_mov_b32 m0, s37
	s_nop 0
	global_load_lds_dwordx4 v[198:199], off
	v_lshl_add_u64 v[198:199], v[222:223], 0, s[92:93]
	s_mov_b32 m0, s41
	s_nop 0
	global_load_lds_dwordx4 v[198:199], off
	s_waitcnt vmcnt(8)
	s_waitcnt lgkmcnt(0)
	s_barrier
	s_setprio 1
	s_waitcnt lgkmcnt(0)
	v_mfma_f32_16x16x32_bf16 v[62:65], v[130:133], v[164:167], v[62:65]
	v_mfma_f32_16x16x32_bf16 v[58:61], v[138:141], v[164:167], v[58:61]
	v_mfma_f32_16x16x32_bf16 v[46:49], v[130:133], v[172:175], v[46:49]
	v_mfma_f32_16x16x32_bf16 v[42:45], v[138:141], v[172:175], v[42:45]
	v_mfma_f32_16x16x32_bf16 v[30:33], v[130:133], v[180:183], v[30:33]
	v_mfma_f32_16x16x32_bf16 v[26:29], v[138:141], v[180:183], v[26:29]
	v_mfma_f32_16x16x32_bf16 v[14:17], v[130:133], v[188:191], v[14:17]
	v_mfma_f32_16x16x32_bf16 v[10:13], v[138:141], v[188:191], v[10:13]
	v_mfma_f32_16x16x32_bf16 v[62:65], v[134:137], v[168:171], v[62:65]
	v_mfma_f32_16x16x32_bf16 v[58:61], v[142:145], v[168:171], v[58:61]
	v_mfma_f32_16x16x32_bf16 v[46:49], v[134:137], v[176:179], v[46:49]
	v_mfma_f32_16x16x32_bf16 v[42:45], v[142:145], v[176:179], v[42:45]
	v_mfma_f32_16x16x32_bf16 v[30:33], v[134:137], v[184:187], v[30:33]
	v_mfma_f32_16x16x32_bf16 v[26:29], v[142:145], v[184:187], v[26:29]
	v_mfma_f32_16x16x32_bf16 v[14:17], v[134:137], v[192:195], v[14:17]
	v_mfma_f32_16x16x32_bf16 v[10:13], v[142:145], v[192:195], v[10:13]
	s_setprio 0
	s_setprio 1
	v_mfma_f32_16x16x32_bf16 v[54:57], v[146:149], v[164:167], v[54:57]
	v_mfma_f32_16x16x32_bf16 v[50:53], v[154:157], v[164:167], v[50:53]
	v_mfma_f32_16x16x32_bf16 v[38:41], v[146:149], v[172:175], v[38:41]
	v_mfma_f32_16x16x32_bf16 v[34:37], v[154:157], v[172:175], v[34:37]
	v_mfma_f32_16x16x32_bf16 v[22:25], v[146:149], v[180:183], v[22:25]
	v_mfma_f32_16x16x32_bf16 v[18:21], v[154:157], v[180:183], v[18:21]
	v_mfma_f32_16x16x32_bf16 v[6:9], v[146:149], v[188:191], v[6:9]
	v_mfma_f32_16x16x32_bf16 v[2:5], v[154:157], v[188:191], v[2:5]
	v_mfma_f32_16x16x32_bf16 v[54:57], v[150:153], v[168:171], v[54:57]
	v_mfma_f32_16x16x32_bf16 v[50:53], v[158:161], v[168:171], v[50:53]
	v_mfma_f32_16x16x32_bf16 v[38:41], v[150:153], v[176:179], v[38:41]
	v_mfma_f32_16x16x32_bf16 v[34:37], v[158:161], v[176:179], v[34:37]
	v_mfma_f32_16x16x32_bf16 v[22:25], v[150:153], v[184:187], v[22:25]
	v_mfma_f32_16x16x32_bf16 v[18:21], v[158:161], v[184:187], v[18:21]
	v_mfma_f32_16x16x32_bf16 v[6:9], v[150:153], v[192:195], v[6:9]
	v_mfma_f32_16x16x32_bf16 v[2:5], v[158:161], v[192:195], v[2:5]
	s_setprio 2
	s_barrier
	s_add_u32 s24, s24, 0x100
	s_addc_u32 s25, s25, 0
	s_add_u32 s58, s58, 0x100
	s_addc_u32 s59, s59, 0
	s_cmp_ge_i32 s60, s43
	s_mov_b32 s26, s60
	s_cbranch_scc0 .LBB0_943

; #define PG8_STAGE(bufoff, gbase, voff) do { _Pragma("unroll") for (int _i = 0; _i < 2; ++_i) \
;         __builtin_amdgcn_global_load_lds((const unsigned*)((const char*)(gbase) + (voff)[_i]), (PG8_LAS unsigned*)(lds + (bufoff) + ldsw + _i * 8192), 16, 0, 0); } while (0)
; #define PG8_WAIT_V(n) asm volatile("s_waitcnt vmcnt(" #n ")" ::: "memory")
; #define PG8_WAIT_L(n) asm volatile("s_waitcnt lgkmcnt(" #n ")" ::: "memory")
; #define PG8_BAR __builtin_amdgcn_s_barrier()
; #define PG8_SCHED __builtin_amdgcn_sched_barrier(0)
; template <class Epi, class Sched, bool ALIGN_EPI = false, bool SP2 = false, bool F8 = false>
; __device__ __forceinline__ void gemm_phase(PG8_LAS unsigned char* lds, const Gemm g, const Sched& S, const Epi& E, const int tidb  ) {
;     ...
;             const bool last = (t == nt - 2);
;             if constexpr (Epi::PREFETCH) { if (t == 0) E.prefetch(cur, wid, lane); }
;             const char* a1 = cA + (size_t)(t + 1) * kstep;
;             const char* a2 = last ? nA : cA + (size_t)(t + 2) * kstep; const char* b2 = last ? nB : cB + (size_t)(t + 2) * kstep;
;             const char* a3 = a2 + kstep; const char* b3 = b2 + kstep;
;             if (last && has_next) S.a_ready(nxt);
;             if constexpr (SP2) {
;             PG8_LDB(B0, 0, 0); PG8_LDB(B1, 0, 1); PG8_SCHED; PG8_LDA(At, 0, 0); PG8_STAGE(PG8_SA(1, 1), a1 + hstep, voffA);
;             PG8_WAIT_V(8); PG8_WAIT_L(0); PG8_BAR; PG8_MMA(0, 0, At, B0); PG8_MMA(0, 1, At, B1); PG8_BAR; PG8_SCHED;
;             PG8_LDA(At, 0, 1); PG8_STAGE(PG8_SB(0, 0), b2, voffB); PG8_STAGE(PG8_SB(0, 1), b2 + hstep, voffB); PG8_STAGE(PG8_SA(0, 0), a2, voffA);
;             PG8_WAIT_V(8); PG8_WAIT_L(0); PG8_BAR; PG8_MMA(1, 0, At, B0); PG8_MMA(1, 1, At, B1); PG8_BAR; PG8_SCHED;
.LBB0_993:
	s_add_i32 s62, s26, 2
	s_add_u32 s28, s24, 0x80
	s_addc_u32 s27, s25, 0
	s_add_i32 s63, 0, 0x10000
	s_cmp_eq_u32 s47, s26
	s_cselect_b32 s27, s7, s27
	s_cselect_b32 s26, s6, s28
	s_cselect_b32 s29, s23, s61
	s_cselect_b32 s28, s22, s60
	s_add_i32 s65, 0, 0x14000
	v_add_u32_e32 v2, s63, v200
	v_add_u32_e32 v14, s65, v200
	ds_read_b128 v[18:21], v2
	ds_read_b128 v[22:25], v2 offset:1024
	ds_read_b128 v[26:29], v2 offset:2048
	ds_read_b128 v[30:33], v2 offset:3072
	ds_read_b128 v[2:5], v14
	ds_read_b128 v[6:9], v14 offset:1024
	ds_read_b128 v[10:13], v14 offset:2048
	ds_read_b128 v[14:17], v14 offset:3072
	v_lshl_add_u64 v[198:199], s[24:25], 0, v[210:211]
	s_add_i32 m0, s1, 0xc000
	ds_read_b128 v[164:167], v196
	ds_read_b128 v[168:171], v196 offset:1024
	ds_read_b128 v[172:175], v196 offset:2048
	ds_read_b128 v[176:179], v196 offset:3072
	ds_read_b128 v[180:183], v196 offset:4096
	ds_read_b128 v[184:187], v196 offset:5120
	ds_read_b128 v[188:191], v196 offset:6144
	ds_read_b128 v[192:195], v196 offset:7168
	global_load_lds_dwordx4 v[198:199], off
	v_lshl_add_u64 v[198:199], s[24:25], 0, v[212:213]
	s_add_i32 m0, s1, 0xe000
	s_nop 0
	global_load_lds_dwordx4 v[198:199], off
	s_waitcnt vmcnt(8)
	s_waitcnt lgkmcnt(0)
	s_barrier
	s_setprio 1
	s_waitcnt lgkmcnt(0)
	v_mfma_scale_f32_16x16x128_f8f6f4 v[158:161], v[18:25], v[164:171], v[158:161], v246, v247 op_sel_hi:[0,0,0]
	v_mfma_scale_f32_16x16x128_f8f6f4 v[154:157], v[26:33], v[164:171], v[154:157], v246, v247 op_sel_hi:[0,0,0]
	v_mfma_scale_f32_16x16x128_f8f6f4 v[142:145], v[18:25], v[172:179], v[142:145], v246, v247 op_sel_hi:[0,0,0]
	v_mfma_scale_f32_16x16x128_f8f6f4 v[138:141], v[26:33], v[172:179], v[138:141], v246, v247 op_sel_hi:[0,0,0]
	v_mfma_scale_f32_16x16x128_f8f6f4 v[126:129], v[18:25], v[180:187], v[126:129], v246, v247 op_sel_hi:[0,0,0]
	v_mfma_scale_f32_16x16x128_f8f6f4 v[122:125], v[26:33], v[180:187], v[122:125], v246, v247 op_sel_hi:[0,0,0]
	v_mfma_scale_f32_16x16x128_f8f6f4 v[110:113], v[18:25], v[188:195], v[110:113], v246, v247 op_sel_hi:[0,0,0]
	v_mfma_scale_f32_16x16x128_f8f6f4 v[106:109], v[26:33], v[188:195], v[106:109], v246, v247 op_sel_hi:[0,0,0]
	s_setprio 0
	s_setprio 1
	v_mfma_scale_f32_16x16x128_f8f6f4 v[150:153], v[2:9], v[164:171], v[150:153], v246, v247 op_sel_hi:[0,0,0]
	v_mfma_scale_f32_16x16x128_f8f6f4 v[146:149], v[10:17], v[164:171], v[146:149], v246, v247 op_sel_hi:[0,0,0]
	v_mfma_scale_f32_16x16x128_f8f6f4 v[134:137], v[2:9], v[172:179], v[134:137], v246, v247 op_sel_hi:[0,0,0]
	v_mfma_scale_f32_16x16x128_f8f6f4 v[130:133], v[10:17], v[172:179], v[130:133], v246, v247 op_sel_hi:[0,0,0]
	v_mfma_scale_f32_16x16x128_f8f6f4 v[118:121], v[2:9], v[180:187], v[118:121], v246, v247 op_sel_hi:[0,0,0]
	v_mfma_scale_f32_16x16x128_f8f6f4 v[114:117], v[10:17], v[180:187], v[114:117], v246, v247 op_sel_hi:[0,0,0]
	v_mfma_scale_f32_16x16x128_f8f6f4 v[102:105], v[2:9], v[188:195], v[102:105], v246, v247 op_sel_hi:[0,0,0]
	v_mfma_scale_f32_16x16x128_f8f6f4 v[98:101], v[10:17], v[188:195], v[98:101], v246, v247 op_sel_hi:[0,0,0]
	s_setprio 2
	s_barrier
	s_add_i32 s63, s63, s0
	v_lshl_add_u64 v[164:165], s[28:29], 0, v[0:1]
	s_mov_b32 m0, s63
	ds_read_b128 v[176:179], v196 offset:16384
	ds_read_b128 v[180:183], v196 offset:17408
	ds_read_b128 v[184:187], v196 offset:18432
	ds_read_b128 v[188:191], v196 offset:19456
	ds_read_b128 v[214:217], v196 offset:20480
	ds_read_b128 v[218:221], v196 offset:21504
	ds_read_b128 v[222:225], v196 offset:22528
	ds_read_b128 v[226:229], v196 offset:23552
	global_load_lds_dwordx4 v[164:165], off
	s_add_i32 m0, s63, 0x2000
	v_lshl_add_u64 v[166:167], s[28:29], 0, v[208:209]
	s_add_u32 s28, s28, s10
	s_addc_u32 s29, s29, s11
	s_add_i32 s63, s65, s0
	global_load_lds_dwordx4 v[166:167], off
	v_lshl_add_u64 v[168:169], s[28:29], 0, v[0:1]
	s_mov_b32 m0, s63
	v_lshl_add_u64 v[170:171], s[28:29], 0, v[208:209]
	global_load_lds_dwordx4 v[168:169], off
	s_add_i32 m0, s63, 0x2000
	v_lshl_add_u64 v[172:173], s[26:27], 0, v[204:205]
	global_load_lds_dwordx4 v[170:171], off
	s_mov_b32 m0, s1
	v_lshl_add_u64 v[174:175], s[26:27], 0, v[206:207]
	global_load_lds_dwordx4 v[172:173], off
	s_mov_b32 m0, s36
	s_nop 0
	global_load_lds_dwordx4 v[174:175], off
	s_waitcnt vmcnt(8)
	s_waitcnt lgkmcnt(0)
	s_barrier
	s_setprio 1
	s_waitcnt lgkmcnt(0)
	v_mfma_scale_f32_16x16x128_f8f6f4 v[94:97], v[18:25], v[176:183], v[94:97], v246, v247 op_sel_hi:[0,0,0]
	v_mfma_scale_f32_16x16x128_f8f6f4 v[90:93], v[26:33], v[176:183], v[90:93], v246, v247 op_sel_hi:[0,0,0]
	v_mfma_scale_f32_16x16x128_f8f6f4 v[78:81], v[18:25], v[184:191], v[78:81], v246, v247 op_sel_hi:[0,0,0]
	v_mfma_scale_f32_16x16x128_f8f6f4 v[74:77], v[26:33], v[184:191], v[74:77], v246, v247 op_sel_hi:[0,0,0]
	v_mfma_scale_f32_16x16x128_f8f6f4 v[62:65], v[18:25], v[214:221], v[62:65], v246, v247 op_sel_hi:[0,0,0]
	v_mfma_scale_f32_16x16x128_f8f6f4 v[58:61], v[26:33], v[214:221], v[58:61], v246, v247 op_sel_hi:[0,0,0]
	v_mfma_scale_f32_16x16x128_f8f6f4 v[46:49], v[18:25], v[222:229], v[46:49], v246, v247 op_sel_hi:[0,0,0]
	v_mfma_scale_f32_16x16x128_f8f6f4 v[42:45], v[26:33], v[222:229], v[42:45], v246, v247 op_sel_hi:[0,0,0]
	s_setprio 0
	s_setprio 1
	v_mfma_scale_f32_16x16x128_f8f6f4 v[86:89], v[2:9], v[176:183], v[86:89], v246, v247 op_sel_hi:[0,0,0]
	v_mfma_scale_f32_16x16x128_f8f6f4 v[82:85], v[10:17], v[176:183], v[82:85], v246, v247 op_sel_hi:[0,0,0]
	v_mfma_scale_f32_16x16x128_f8f6f4 v[70:73], v[2:9], v[184:191], v[70:73], v246, v247 op_sel_hi:[0,0,0]
	v_mfma_scale_f32_16x16x128_f8f6f4 v[66:69], v[10:17], v[184:191], v[66:69], v246, v247 op_sel_hi:[0,0,0]
	v_mfma_scale_f32_16x16x128_f8f6f4 v[54:57], v[2:9], v[214:221], v[54:57], v246, v247 op_sel_hi:[0,0,0]
	v_mfma_scale_f32_16x16x128_f8f6f4 v[50:53], v[10:17], v[214:221], v[50:53], v246, v247 op_sel_hi:[0,0,0]
	v_mfma_scale_f32_16x16x128_f8f6f4 v[38:41], v[2:9], v[222:229], v[38:41], v246, v247 op_sel_hi:[0,0,0]
	v_mfma_scale_f32_16x16x128_f8f6f4 v[34:37], v[10:17], v[222:229], v[34:37], v246, v247 op_sel_hi:[0,0,0]
	s_setprio 2
	s_barrier
; #define PG8_STAGE(bufoff, gbase, voff) do { _Pragma("unroll") for (int _i = 0; _i < 2; ++_i) \
;         __builtin_amdgcn_global_load_lds((const unsigned*)((const char*)(gbase) + (voff)[_i]), (PG8_LAS unsigned*)(lds + (bufoff) + ldsw + _i * 8192), 16, 0, 0); } while (0)
; #define PG8_WAIT_V(n) asm volatile("s_waitcnt vmcnt(" #n ")" ::: "memory")
; #define PG8_WAIT_L(n) asm volatile("s_waitcnt lgkmcnt(" #n ")" ::: "memory")
; #define PG8_BAR __builtin_amdgcn_s_barrier()
; #define PG8_SCHED __builtin_amdgcn_sched_barrier(0)
; template <class Epi, class Sched, bool ALIGN_EPI = false, bool SP2 = false, bool F8 = false>
; __device__ __forceinline__ void gemm_phase(PG8_LAS unsigned char* lds, const Gemm g, const Sched& S, const Epi& E, const int tidb  ) {
;     ...
;             PG8_LDB(B0, 1, 0); PG8_LDB(B1, 1, 1); PG8_SCHED; PG8_LDA(At, 1, 0); PG8_STAGE(PG8_SA(0, 1), a2 + hstep, voffA);
;             PG8_WAIT_V(8); PG8_WAIT_L(0); PG8_BAR; PG8_MMA(0, 0, At, B0); PG8_MMA(0, 1, At, B1); PG8_BAR; PG8_SCHED;
;             PG8_LDA(At, 1, 1); PG8_STAGE(PG8_SB(1, 0), b3, voffB); PG8_STAGE(PG8_SB(1, 1), b3 + hstep, voffB); PG8_STAGE(PG8_SA(1, 0), a3, voffA);
;             PG8_WAIT_V(8); PG8_WAIT_L(0); PG8_BAR; PG8_MMA(1, 0, At, B0); PG8_MMA(1, 1, At, B1); PG8_BAR; PG8_SCHED;
	s_add_i32 s28, 0, 0x18000
	s_add_i32 s29, 0, 0x1c000
	v_add_u32_e32 v14, s28, v200
	v_add_u32_e32 v30, s29, v200
	ds_read_b128 v[2:5], v14
	ds_read_b128 v[6:9], v14 offset:1024
	ds_read_b128 v[10:13], v14 offset:2048
	ds_read_b128 v[14:17], v14 offset:3072
	ds_read_b128 v[18:21], v30
	ds_read_b128 v[22:25], v30 offset:1024
	ds_read_b128 v[26:29], v30 offset:2048
	ds_read_b128 v[30:33], v30 offset:3072
	s_add_u32 s26, s26, s10
	s_addc_u32 s27, s27, s11
	s_mov_b32 m0, s37
	v_lshl_add_u64 v[192:193], s[26:27], 0, v[204:205]
	ds_read_b128 v[176:179], v196 offset:32768
	ds_read_b128 v[180:183], v196 offset:33792
	ds_read_b128 v[184:187], v196 offset:34816
	ds_read_b128 v[188:191], v196 offset:35840
	ds_read_b128 v[214:217], v196 offset:36864
	ds_read_b128 v[218:221], v196 offset:37888
	ds_read_b128 v[222:225], v196 offset:38912
	ds_read_b128 v[226:229], v196 offset:39936
	global_load_lds_dwordx4 v[192:193], off
	v_lshl_add_u64 v[192:193], s[26:27], 0, v[206:207]
	s_mov_b32 m0, s41
	s_nop 0
	global_load_lds_dwordx4 v[192:193], off
	s_waitcnt vmcnt(8)
	s_waitcnt lgkmcnt(0)
	s_barrier
	s_setprio 1
	s_waitcnt lgkmcnt(0)
	v_mfma_scale_f32_16x16x128_f8f6f4 v[158:161], v[2:9], v[176:183], v[158:161], v246, v247 op_sel_hi:[0,0,0]
	v_mfma_scale_f32_16x16x128_f8f6f4 v[154:157], v[10:17], v[176:183], v[154:157], v246, v247 op_sel_hi:[0,0,0]
	v_mfma_scale_f32_16x16x128_f8f6f4 v[142:145], v[2:9], v[184:191], v[142:145], v246, v247 op_sel_hi:[0,0,0]
	v_mfma_scale_f32_16x16x128_f8f6f4 v[138:141], v[10:17], v[184:191], v[138:141], v246, v247 op_sel_hi:[0,0,0]
	v_mfma_scale_f32_16x16x128_f8f6f4 v[126:129], v[2:9], v[214:221], v[126:129], v246, v247 op_sel_hi:[0,0,0]
	v_mfma_scale_f32_16x16x128_f8f6f4 v[122:125], v[10:17], v[214:221], v[122:125], v246, v247 op_sel_hi:[0,0,0]
	v_mfma_scale_f32_16x16x128_f8f6f4 v[110:113], v[2:9], v[222:229], v[110:113], v246, v247 op_sel_hi:[0,0,0]
	v_mfma_scale_f32_16x16x128_f8f6f4 v[106:109], v[10:17], v[222:229], v[106:109], v246, v247 op_sel_hi:[0,0,0]
	s_setprio 0
	s_setprio 1
	v_mfma_scale_f32_16x16x128_f8f6f4 v[150:153], v[18:25], v[176:183], v[150:153], v246, v247 op_sel_hi:[0,0,0]
	v_mfma_scale_f32_16x16x128_f8f6f4 v[146:149], v[26:33], v[176:183], v[146:149], v246, v247 op_sel_hi:[0,0,0]
	v_mfma_scale_f32_16x16x128_f8f6f4 v[134:137], v[18:25], v[184:191], v[134:137], v246, v247 op_sel_hi:[0,0,0]
	v_mfma_scale_f32_16x16x128_f8f6f4 v[130:133], v[26:33], v[184:191], v[130:133], v246, v247 op_sel_hi:[0,0,0]
	v_mfma_scale_f32_16x16x128_f8f6f4 v[118:121], v[18:25], v[214:221], v[118:121], v246, v247 op_sel_hi:[0,0,0]
	v_mfma_scale_f32_16x16x128_f8f6f4 v[114:117], v[26:33], v[214:221], v[114:117], v246, v247 op_sel_hi:[0,0,0]
	v_mfma_scale_f32_16x16x128_f8f6f4 v[102:105], v[18:25], v[222:229], v[102:105], v246, v247 op_sel_hi:[0,0,0]
	v_mfma_scale_f32_16x16x128_f8f6f4 v[98:101], v[26:33], v[222:229], v[98:101], v246, v247 op_sel_hi:[0,0,0]
	s_setprio 2
	s_barrier
	s_add_i32 s26, s28, s0
	v_lshl_add_u64 v[164:165], v[164:165], 0, s[92:93]
	s_mov_b32 m0, s26
	ds_read_b128 v[176:179], v196 offset:49152
	ds_read_b128 v[180:183], v196 offset:50176
	ds_read_b128 v[184:187], v196 offset:51200
	ds_read_b128 v[188:191], v196 offset:52224
	ds_read_b128 v[214:217], v196 offset:53248
	ds_read_b128 v[218:221], v196 offset:54272
	ds_read_b128 v[222:225], v196 offset:55296
	ds_read_b128 v[226:229], v196 offset:56320
	global_load_lds_dwordx4 v[164:165], off
	v_lshl_add_u64 v[164:165], v[166:167], 0, s[92:93]
	s_add_i32 m0, s26, 0x2000
	s_add_i32 s26, s29, s0
	global_load_lds_dwordx4 v[164:165], off
	v_lshl_add_u64 v[164:165], v[168:169], 0, s[92:93]
	s_mov_b32 m0, s26
	s_nop 0
	global_load_lds_dwordx4 v[164:165], off
	v_lshl_add_u64 v[164:165], v[170:171], 0, s[92:93]
	s_add_i32 m0, s26, 0x2000
	s_nop 0
	global_load_lds_dwordx4 v[164:165], off
	v_lshl_add_u64 v[164:165], v[172:173], 0, s[92:93]
	s_mov_b32 m0, s43
	s_nop 0
	global_load_lds_dwordx4 v[164:165], off
	v_lshl_add_u64 v[164:165], v[174:175], 0, s[92:93]
	s_mov_b32 m0, s45
	s_nop 0
	global_load_lds_dwordx4 v[164:165], off
	s_waitcnt vmcnt(8)
	s_waitcnt lgkmcnt(0)
	s_barrier
	s_setprio 1
	s_waitcnt lgkmcnt(0)
	v_mfma_scale_f32_16x16x128_f8f6f4 v[94:97], v[2:9], v[176:183], v[94:97], v246, v247 op_sel_hi:[0,0,0]
	v_mfma_scale_f32_16x16x128_f8f6f4 v[90:93], v[10:17], v[176:183], v[90:93], v246, v247 op_sel_hi:[0,0,0]
	v_mfma_scale_f32_16x16x128_f8f6f4 v[78:81], v[2:9], v[184:191], v[78:81], v246, v247 op_sel_hi:[0,0,0]
	v_mfma_scale_f32_16x16x128_f8f6f4 v[74:77], v[10:17], v[184:191], v[74:77], v246, v247 op_sel_hi:[0,0,0]
	v_mfma_scale_f32_16x16x128_f8f6f4 v[62:65], v[2:9], v[214:221], v[62:65], v246, v247 op_sel_hi:[0,0,0]
	v_mfma_scale_f32_16x16x128_f8f6f4 v[58:61], v[10:17], v[214:221], v[58:61], v246, v247 op_sel_hi:[0,0,0]
	v_mfma_scale_f32_16x16x128_f8f6f4 v[46:49], v[2:9], v[222:229], v[46:49], v246, v247 op_sel_hi:[0,0,0]
	v_mfma_scale_f32_16x16x128_f8f6f4 v[42:45], v[10:17], v[222:229], v[42:45], v246, v247 op_sel_hi:[0,0,0]
	s_setprio 0
	s_setprio 1
	v_mfma_scale_f32_16x16x128_f8f6f4 v[86:89], v[18:25], v[176:183], v[86:89], v246, v247 op_sel_hi:[0,0,0]
	v_mfma_scale_f32_16x16x128_f8f6f4 v[82:85], v[26:33], v[176:183], v[82:85], v246, v247 op_sel_hi:[0,0,0]
	v_mfma_scale_f32_16x16x128_f8f6f4 v[70:73], v[18:25], v[184:191], v[70:73], v246, v247 op_sel_hi:[0,0,0]
	v_mfma_scale_f32_16x16x128_f8f6f4 v[66:69], v[26:33], v[184:191], v[66:69], v246, v247 op_sel_hi:[0,0,0]
	v_mfma_scale_f32_16x16x128_f8f6f4 v[54:57], v[18:25], v[214:221], v[54:57], v246, v247 op_sel_hi:[0,0,0]
	v_mfma_scale_f32_16x16x128_f8f6f4 v[50:53], v[26:33], v[214:221], v[50:53], v246, v247 op_sel_hi:[0,0,0]
	v_mfma_scale_f32_16x16x128_f8f6f4 v[38:41], v[18:25], v[222:229], v[38:41], v246, v247 op_sel_hi:[0,0,0]
	v_mfma_scale_f32_16x16x128_f8f6f4 v[34:37], v[26:33], v[222:229], v[34:37], v246, v247 op_sel_hi:[0,0,0]
	s_setprio 2
	s_barrier
	s_add_u32 s24, s24, 0x100
	s_addc_u32 s25, s25, 0
	s_add_u32 s60, s60, 0x100
	s_addc_u32 s61, s61, 0
	s_cmp_ge_i32 s62, s46
	s_mov_b32 s26, s62
	s_cbranch_scc0 .LBB0_993

; #define PG8_STAGE(bufoff, gbase, voff) do { _Pragma("unroll") for (int _i = 0; _i < 2; ++_i) \
;         __builtin_amdgcn_global_load_lds((const unsigned*)((const char*)(gbase) + (voff)[_i]), (PG8_LAS unsigned*)(lds + (bufoff) + ldsw + _i * 8192), 16, 0, 0); } while (0)
; #define PG8_WAIT_V(n) asm volatile("s_waitcnt vmcnt(" #n ")" ::: "memory")
; #define PG8_WAIT_L(n) asm volatile("s_waitcnt lgkmcnt(" #n ")" ::: "memory")
; #define PG8_BAR __builtin_amdgcn_s_barrier()
; #define PG8_SCHED __builtin_amdgcn_sched_barrier(0)
; template <class Epi, class Sched, bool ALIGN_EPI = false, bool SP2 = false, bool F8 = false>
; __device__ __forceinline__ void gemm_phase(PG8_LAS unsigned char* lds, const Gemm g, const Sched& S, const Epi& E, const int tidb  ) {
;     ...
;             const bool last = (t == nt - 2);
;             if constexpr (Epi::PREFETCH) { if (t == 0) E.prefetch(cur, wid, lane); }
;             const char* a1 = cA + (size_t)(t + 1) * kstep;
;             const char* a2 = last ? nA : cA + (size_t)(t + 2) * kstep; const char* b2 = last ? nB : cB + (size_t)(t + 2) * kstep;
;             const char* a3 = a2 + kstep; const char* b3 = b2 + kstep;
;             if (last && has_next) S.a_ready(nxt);
;             if constexpr (SP2) {
;             PG8_LDB(B0, 0, 0); PG8_LDB(B1, 0, 1); PG8_SCHED; PG8_LDA(At, 0, 0); PG8_STAGE(PG8_SA(1, 1), a1 + hstep, voffA);
;             PG8_WAIT_V(8); PG8_WAIT_L(0); PG8_BAR; PG8_MMA(0, 0, At, B0); PG8_MMA(0, 1, At, B1); PG8_BAR; PG8_SCHED;
;             PG8_LDA(At, 0, 1); PG8_STAGE(PG8_SB(0, 0), b2, voffB); PG8_STAGE(PG8_SB(0, 1), b2 + hstep, voffB); PG8_STAGE(PG8_SA(0, 0), a2, voffA);
;             PG8_WAIT_V(8); PG8_WAIT_L(0); PG8_BAR; PG8_MMA(1, 0, At, B0); PG8_MMA(1, 1, At, B1); PG8_BAR; PG8_SCHED;
.LBB0_1042:
	s_add_i32 s62, s26, 2
	s_add_u32 s28, s24, 0x80
	s_addc_u32 s27, s25, 0
	s_add_i32 s63, 0, 0x10000
	s_cmp_eq_u32 s47, s26
	s_cselect_b32 s27, s7, s27
	s_cselect_b32 s26, s6, s28
	s_cselect_b32 s29, s9, s61
	s_cselect_b32 s28, s8, s60
	s_add_i32 s65, 0, 0x14000
	v_add_u32_e32 v2, s63, v192
	v_add_u32_e32 v14, s65, v192
	ds_read_b128 v[18:21], v2
	ds_read_b128 v[22:25], v2 offset:1024
	ds_read_b128 v[26:29], v2 offset:2048
	ds_read_b128 v[30:33], v2 offset:3072
	ds_read_b128 v[2:5], v14
	ds_read_b128 v[6:9], v14 offset:1024
	ds_read_b128 v[10:13], v14 offset:2048
	ds_read_b128 v[14:17], v14 offset:3072
	v_lshl_add_u64 v[190:191], s[24:25], 0, v[170:171]
	s_add_i32 m0, s1, 0xc000
	ds_read_b128 v[174:177], v194
	ds_read_b128 v[178:181], v194 offset:1024
	ds_read_b128 v[182:185], v194 offset:2048
	ds_read_b128 v[186:189], v194 offset:3072
	ds_read_b128 v[204:207], v194 offset:4096
	ds_read_b128 v[208:211], v194 offset:5120
	ds_read_b128 v[212:215], v194 offset:6144
	ds_read_b128 v[216:219], v194 offset:7168
	global_load_lds_dwordx4 v[190:191], off
	v_lshl_add_u64 v[190:191], s[24:25], 0, v[172:173]
	s_add_i32 m0, s1, 0xe000
	s_nop 0
	global_load_lds_dwordx4 v[190:191], off
	s_waitcnt vmcnt(8)
	s_waitcnt lgkmcnt(0)
	s_barrier
	s_setprio 1
	s_waitcnt lgkmcnt(0)
	v_mfma_scale_f32_16x16x128_f8f6f4 v[158:161], v[18:25], v[174:181], v[158:161], v246, v247 op_sel_hi:[0,0,0]
	v_mfma_scale_f32_16x16x128_f8f6f4 v[154:157], v[26:33], v[174:181], v[154:157], v246, v247 op_sel_hi:[0,0,0]
	v_mfma_scale_f32_16x16x128_f8f6f4 v[142:145], v[18:25], v[182:189], v[142:145], v246, v247 op_sel_hi:[0,0,0]
	v_mfma_scale_f32_16x16x128_f8f6f4 v[138:141], v[26:33], v[182:189], v[138:141], v246, v247 op_sel_hi:[0,0,0]
	v_mfma_scale_f32_16x16x128_f8f6f4 v[126:129], v[18:25], v[204:211], v[126:129], v246, v247 op_sel_hi:[0,0,0]
	v_mfma_scale_f32_16x16x128_f8f6f4 v[122:125], v[26:33], v[204:211], v[122:125], v246, v247 op_sel_hi:[0,0,0]
	v_mfma_scale_f32_16x16x128_f8f6f4 v[110:113], v[18:25], v[212:219], v[110:113], v246, v247 op_sel_hi:[0,0,0]
	v_mfma_scale_f32_16x16x128_f8f6f4 v[106:109], v[26:33], v[212:219], v[106:109], v246, v247 op_sel_hi:[0,0,0]
	s_setprio 0
	s_setprio 1
	v_mfma_scale_f32_16x16x128_f8f6f4 v[150:153], v[2:9], v[174:181], v[150:153], v246, v247 op_sel_hi:[0,0,0]
	v_mfma_scale_f32_16x16x128_f8f6f4 v[146:149], v[10:17], v[174:181], v[146:149], v246, v247 op_sel_hi:[0,0,0]
	v_mfma_scale_f32_16x16x128_f8f6f4 v[134:137], v[2:9], v[182:189], v[134:137], v246, v247 op_sel_hi:[0,0,0]
	v_mfma_scale_f32_16x16x128_f8f6f4 v[130:133], v[10:17], v[182:189], v[130:133], v246, v247 op_sel_hi:[0,0,0]
	v_mfma_scale_f32_16x16x128_f8f6f4 v[118:121], v[2:9], v[204:211], v[118:121], v246, v247 op_sel_hi:[0,0,0]
	v_mfma_scale_f32_16x16x128_f8f6f4 v[114:117], v[10:17], v[204:211], v[114:117], v246, v247 op_sel_hi:[0,0,0]
	v_mfma_scale_f32_16x16x128_f8f6f4 v[102:105], v[2:9], v[212:219], v[102:105], v246, v247 op_sel_hi:[0,0,0]
	v_mfma_scale_f32_16x16x128_f8f6f4 v[98:101], v[10:17], v[212:219], v[98:101], v246, v247 op_sel_hi:[0,0,0]
	s_setprio 2
	s_barrier
	s_add_i32 s63, s63, s0
	v_lshl_add_u64 v[174:175], s[28:29], 0, v[0:1]
	s_mov_b32 m0, s63
	ds_read_b128 v[204:207], v194 offset:16384
	ds_read_b128 v[208:211], v194 offset:17408
	ds_read_b128 v[212:215], v194 offset:18432
	ds_read_b128 v[216:219], v194 offset:19456
	ds_read_b128 v[220:223], v194 offset:20480
	ds_read_b128 v[224:227], v194 offset:21504
	ds_read_b128 v[228:231], v194 offset:22528
	ds_read_b128 v[232:235], v194 offset:23552
	global_load_lds_dwordx4 v[174:175], off
	s_add_i32 m0, s63, 0x2000
	v_lshl_add_u64 v[176:177], s[28:29], 0, v[168:169]
	s_add_u32 s28, s28, s10
	s_addc_u32 s29, s29, s11
	s_add_i32 s63, s65, s0
	global_load_lds_dwordx4 v[176:177], off
	v_lshl_add_u64 v[178:179], s[28:29], 0, v[0:1]
	s_mov_b32 m0, s63
	v_lshl_add_u64 v[180:181], s[28:29], 0, v[168:169]
	global_load_lds_dwordx4 v[178:179], off
	s_add_i32 m0, s63, 0x2000
	v_lshl_add_u64 v[182:183], s[26:27], 0, v[164:165]
	global_load_lds_dwordx4 v[180:181], off
	s_mov_b32 m0, s1
	v_lshl_add_u64 v[184:185], s[26:27], 0, v[166:167]
	global_load_lds_dwordx4 v[182:183], off
	s_mov_b32 m0, s36
	s_nop 0
	global_load_lds_dwordx4 v[184:185], off
	s_waitcnt vmcnt(8)
	s_waitcnt lgkmcnt(0)
	s_barrier
	s_setprio 1
	s_waitcnt lgkmcnt(0)
	v_mfma_scale_f32_16x16x128_f8f6f4 v[94:97], v[18:25], v[204:211], v[94:97], v246, v247 op_sel_hi:[0,0,0]
	v_mfma_scale_f32_16x16x128_f8f6f4 v[90:93], v[26:33], v[204:211], v[90:93], v246, v247 op_sel_hi:[0,0,0]
	v_mfma_scale_f32_16x16x128_f8f6f4 v[78:81], v[18:25], v[212:219], v[78:81], v246, v247 op_sel_hi:[0,0,0]
	v_mfma_scale_f32_16x16x128_f8f6f4 v[74:77], v[26:33], v[212:219], v[74:77], v246, v247 op_sel_hi:[0,0,0]
	v_mfma_scale_f32_16x16x128_f8f6f4 v[62:65], v[18:25], v[220:227], v[62:65], v246, v247 op_sel_hi:[0,0,0]
	v_mfma_scale_f32_16x16x128_f8f6f4 v[58:61], v[26:33], v[220:227], v[58:61], v246, v247 op_sel_hi:[0,0,0]
	v_mfma_scale_f32_16x16x128_f8f6f4 v[46:49], v[18:25], v[228:235], v[46:49], v246, v247 op_sel_hi:[0,0,0]
	v_mfma_scale_f32_16x16x128_f8f6f4 v[42:45], v[26:33], v[228:235], v[42:45], v246, v247 op_sel_hi:[0,0,0]
	s_setprio 0
	s_setprio 1
	v_mfma_scale_f32_16x16x128_f8f6f4 v[86:89], v[2:9], v[204:211], v[86:89], v246, v247 op_sel_hi:[0,0,0]
	v_mfma_scale_f32_16x16x128_f8f6f4 v[82:85], v[10:17], v[204:211], v[82:85], v246, v247 op_sel_hi:[0,0,0]
	v_mfma_scale_f32_16x16x128_f8f6f4 v[70:73], v[2:9], v[212:219], v[70:73], v246, v247 op_sel_hi:[0,0,0]
	v_mfma_scale_f32_16x16x128_f8f6f4 v[66:69], v[10:17], v[212:219], v[66:69], v246, v247 op_sel_hi:[0,0,0]
	v_mfma_scale_f32_16x16x128_f8f6f4 v[54:57], v[2:9], v[220:227], v[54:57], v246, v247 op_sel_hi:[0,0,0]
	v_mfma_scale_f32_16x16x128_f8f6f4 v[50:53], v[10:17], v[220:227], v[50:53], v246, v247 op_sel_hi:[0,0,0]
	v_mfma_scale_f32_16x16x128_f8f6f4 v[38:41], v[2:9], v[228:235], v[38:41], v246, v247 op_sel_hi:[0,0,0]
	v_mfma_scale_f32_16x16x128_f8f6f4 v[34:37], v[10:17], v[228:235], v[34:37], v246, v247 op_sel_hi:[0,0,0]
	s_setprio 2
	s_barrier
; #define PG8_STAGE(bufoff, gbase, voff) do { _Pragma("unroll") for (int _i = 0; _i < 2; ++_i) \
;         __builtin_amdgcn_global_load_lds((const unsigned*)((const char*)(gbase) + (voff)[_i]), (PG8_LAS unsigned*)(lds + (bufoff) + ldsw + _i * 8192), 16, 0, 0); } while (0)
; #define PG8_WAIT_V(n) asm volatile("s_waitcnt vmcnt(" #n ")" ::: "memory")
; #define PG8_WAIT_L(n) asm volatile("s_waitcnt lgkmcnt(" #n ")" ::: "memory")
; #define PG8_BAR __builtin_amdgcn_s_barrier()
; #define PG8_SCHED __builtin_amdgcn_sched_barrier(0)
; template <class Epi, class Sched, bool ALIGN_EPI = false, bool SP2 = false, bool F8 = false>
; __device__ __forceinline__ void gemm_phase(PG8_LAS unsigned char* lds, const Gemm g, const Sched& S, const Epi& E, const int tidb  ) {
;     ...
;             PG8_LDB(B0, 1, 0); PG8_LDB(B1, 1, 1); PG8_SCHED; PG8_LDA(At, 1, 0); PG8_STAGE(PG8_SA(0, 1), a2 + hstep, voffA);
;             PG8_WAIT_V(8); PG8_WAIT_L(0); PG8_BAR; PG8_MMA(0, 0, At, B0); PG8_MMA(0, 1, At, B1); PG8_BAR; PG8_SCHED;
;             PG8_LDA(At, 1, 1); PG8_STAGE(PG8_SB(1, 0), b3, voffB); PG8_STAGE(PG8_SB(1, 1), b3 + hstep, voffB); PG8_STAGE(PG8_SA(1, 0), a3, voffA);
;             PG8_WAIT_V(8); PG8_WAIT_L(0); PG8_BAR; PG8_MMA(1, 0, At, B0); PG8_MMA(1, 1, At, B1); PG8_BAR; PG8_SCHED;
	s_add_i32 s28, 0, 0x18000
	s_add_i32 s29, 0, 0x1c000
	v_add_u32_e32 v14, s28, v192
	v_add_u32_e32 v30, s29, v192
	ds_read_b128 v[2:5], v14
	ds_read_b128 v[6:9], v14 offset:1024
	ds_read_b128 v[10:13], v14 offset:2048
	ds_read_b128 v[14:17], v14 offset:3072
	ds_read_b128 v[18:21], v30
	ds_read_b128 v[22:25], v30 offset:1024
	ds_read_b128 v[26:29], v30 offset:2048
	ds_read_b128 v[30:33], v30 offset:3072
	s_add_u32 s26, s26, s10
	s_addc_u32 s27, s27, s11
	s_mov_b32 m0, s37
	v_lshl_add_u64 v[186:187], s[26:27], 0, v[164:165]
	ds_read_b128 v[204:207], v194 offset:32768
	ds_read_b128 v[208:211], v194 offset:33792
	ds_read_b128 v[212:215], v194 offset:34816
	ds_read_b128 v[216:219], v194 offset:35840
	ds_read_b128 v[220:223], v194 offset:36864
	ds_read_b128 v[224:227], v194 offset:37888
	ds_read_b128 v[228:231], v194 offset:38912
	ds_read_b128 v[232:235], v194 offset:39936
	global_load_lds_dwordx4 v[186:187], off
	v_lshl_add_u64 v[186:187], s[26:27], 0, v[166:167]
	s_mov_b32 m0, s41
	s_nop 0
	global_load_lds_dwordx4 v[186:187], off
	s_waitcnt vmcnt(8)
	s_waitcnt lgkmcnt(0)
	s_barrier
	s_setprio 1
	s_waitcnt lgkmcnt(0)
	v_mfma_scale_f32_16x16x128_f8f6f4 v[158:161], v[2:9], v[204:211], v[158:161], v246, v247 op_sel_hi:[0,0,0]
	v_mfma_scale_f32_16x16x128_f8f6f4 v[154:157], v[10:17], v[204:211], v[154:157], v246, v247 op_sel_hi:[0,0,0]
	v_mfma_scale_f32_16x16x128_f8f6f4 v[142:145], v[2:9], v[212:219], v[142:145], v246, v247 op_sel_hi:[0,0,0]
	v_mfma_scale_f32_16x16x128_f8f6f4 v[138:141], v[10:17], v[212:219], v[138:141], v246, v247 op_sel_hi:[0,0,0]
	v_mfma_scale_f32_16x16x128_f8f6f4 v[126:129], v[2:9], v[220:227], v[126:129], v246, v247 op_sel_hi:[0,0,0]
	v_mfma_scale_f32_16x16x128_f8f6f4 v[122:125], v[10:17], v[220:227], v[122:125], v246, v247 op_sel_hi:[0,0,0]
	v_mfma_scale_f32_16x16x128_f8f6f4 v[110:113], v[2:9], v[228:235], v[110:113], v246, v247 op_sel_hi:[0,0,0]
	v_mfma_scale_f32_16x16x128_f8f6f4 v[106:109], v[10:17], v[228:235], v[106:109], v246, v247 op_sel_hi:[0,0,0]
	s_setprio 0
	s_setprio 1
	v_mfma_scale_f32_16x16x128_f8f6f4 v[150:153], v[18:25], v[204:211], v[150:153], v246, v247 op_sel_hi:[0,0,0]
	v_mfma_scale_f32_16x16x128_f8f6f4 v[146:149], v[26:33], v[204:211], v[146:149], v246, v247 op_sel_hi:[0,0,0]
	v_mfma_scale_f32_16x16x128_f8f6f4 v[134:137], v[18:25], v[212:219], v[134:137], v246, v247 op_sel_hi:[0,0,0]
	v_mfma_scale_f32_16x16x128_f8f6f4 v[130:133], v[26:33], v[212:219], v[130:133], v246, v247 op_sel_hi:[0,0,0]
	v_mfma_scale_f32_16x16x128_f8f6f4 v[118:121], v[18:25], v[220:227], v[118:121], v246, v247 op_sel_hi:[0,0,0]
	v_mfma_scale_f32_16x16x128_f8f6f4 v[114:117], v[26:33], v[220:227], v[114:117], v246, v247 op_sel_hi:[0,0,0]
	v_mfma_scale_f32_16x16x128_f8f6f4 v[102:105], v[18:25], v[228:235], v[102:105], v246, v247 op_sel_hi:[0,0,0]
	v_mfma_scale_f32_16x16x128_f8f6f4 v[98:101], v[26:33], v[228:235], v[98:101], v246, v247 op_sel_hi:[0,0,0]
	s_setprio 2
	s_barrier
	s_add_i32 s26, s28, s0
	v_lshl_add_u64 v[174:175], v[174:175], 0, s[92:93]
	s_mov_b32 m0, s26
	ds_read_b128 v[204:207], v194 offset:49152
	ds_read_b128 v[208:211], v194 offset:50176
	ds_read_b128 v[212:215], v194 offset:51200
	ds_read_b128 v[216:219], v194 offset:52224
	ds_read_b128 v[220:223], v194 offset:53248
	ds_read_b128 v[224:227], v194 offset:54272
	ds_read_b128 v[228:231], v194 offset:55296
	ds_read_b128 v[232:235], v194 offset:56320
	global_load_lds_dwordx4 v[174:175], off
	v_lshl_add_u64 v[174:175], v[176:177], 0, s[92:93]
	s_add_i32 m0, s26, 0x2000
	s_add_i32 s26, s29, s0
	global_load_lds_dwordx4 v[174:175], off
	v_lshl_add_u64 v[174:175], v[178:179], 0, s[92:93]
	s_mov_b32 m0, s26
	s_nop 0
	global_load_lds_dwordx4 v[174:175], off
	v_lshl_add_u64 v[174:175], v[180:181], 0, s[92:93]
	s_add_i32 m0, s26, 0x2000
	s_nop 0
	global_load_lds_dwordx4 v[174:175], off
	v_lshl_add_u64 v[174:175], v[182:183], 0, s[92:93]
	s_mov_b32 m0, s43
	s_nop 0
	global_load_lds_dwordx4 v[174:175], off
	v_lshl_add_u64 v[174:175], v[184:185], 0, s[92:93]
	s_mov_b32 m0, s45
	s_nop 0
	global_load_lds_dwordx4 v[174:175], off
	s_waitcnt vmcnt(8)
	s_waitcnt lgkmcnt(0)
	s_barrier
	s_setprio 1
	s_waitcnt lgkmcnt(0)
	v_mfma_scale_f32_16x16x128_f8f6f4 v[94:97], v[2:9], v[204:211], v[94:97], v246, v247 op_sel_hi:[0,0,0]
	v_mfma_scale_f32_16x16x128_f8f6f4 v[90:93], v[10:17], v[204:211], v[90:93], v246, v247 op_sel_hi:[0,0,0]
	v_mfma_scale_f32_16x16x128_f8f6f4 v[78:81], v[2:9], v[212:219], v[78:81], v246, v247 op_sel_hi:[0,0,0]
	v_mfma_scale_f32_16x16x128_f8f6f4 v[74:77], v[10:17], v[212:219], v[74:77], v246, v247 op_sel_hi:[0,0,0]
	v_mfma_scale_f32_16x16x128_f8f6f4 v[62:65], v[2:9], v[220:227], v[62:65], v246, v247 op_sel_hi:[0,0,0]
	v_mfma_scale_f32_16x16x128_f8f6f4 v[58:61], v[10:17], v[220:227], v[58:61], v246, v247 op_sel_hi:[0,0,0]
	v_mfma_scale_f32_16x16x128_f8f6f4 v[46:49], v[2:9], v[228:235], v[46:49], v246, v247 op_sel_hi:[0,0,0]
	v_mfma_scale_f32_16x16x128_f8f6f4 v[42:45], v[10:17], v[228:235], v[42:45], v246, v247 op_sel_hi:[0,0,0]
	s_setprio 0
	s_setprio 1
	v_mfma_scale_f32_16x16x128_f8f6f4 v[86:89], v[18:25], v[204:211], v[86:89], v246, v247 op_sel_hi:[0,0,0]
	v_mfma_scale_f32_16x16x128_f8f6f4 v[82:85], v[26:33], v[204:211], v[82:85], v246, v247 op_sel_hi:[0,0,0]
	v_mfma_scale_f32_16x16x128_f8f6f4 v[70:73], v[18:25], v[212:219], v[70:73], v246, v247 op_sel_hi:[0,0,0]
	v_mfma_scale_f32_16x16x128_f8f6f4 v[66:69], v[26:33], v[212:219], v[66:69], v246, v247 op_sel_hi:[0,0,0]
	v_mfma_scale_f32_16x16x128_f8f6f4 v[54:57], v[18:25], v[220:227], v[54:57], v246, v247 op_sel_hi:[0,0,0]
	v_mfma_scale_f32_16x16x128_f8f6f4 v[50:53], v[26:33], v[220:227], v[50:53], v246, v247 op_sel_hi:[0,0,0]
	v_mfma_scale_f32_16x16x128_f8f6f4 v[38:41], v[18:25], v[228:235], v[38:41], v246, v247 op_sel_hi:[0,0,0]
	v_mfma_scale_f32_16x16x128_f8f6f4 v[34:37], v[26:33], v[228:235], v[34:37], v246, v247 op_sel_hi:[0,0,0]
	s_setprio 2
	s_barrier
	s_add_u32 s24, s24, 0x100
	s_addc_u32 s25, s25, 0
	s_add_u32 s60, s60, 0x100
	s_addc_u32 s61, s61, 0
	s_cmp_ge_i32 s62, s46
	s_mov_b32 s26, s62
	s_cbranch_scc0 .LBB0_1042

; #define PG8_STAGE(bufoff, gbase, voff) do { _Pragma("unroll") for (int _i = 0; _i < 2; ++_i) \
;         __builtin_amdgcn_global_load_lds((const unsigned*)((const char*)(gbase) + (voff)[_i]), (PG8_LAS unsigned*)(lds + (bufoff) + ldsw + _i * 8192), 16, 0, 0); } while (0)
; #define PG8_WAIT_V(n) asm volatile("s_waitcnt vmcnt(" #n ")" ::: "memory")
; #define PG8_WAIT_L(n) asm volatile("s_waitcnt lgkmcnt(" #n ")" ::: "memory")
; #define PG8_BAR __builtin_amdgcn_s_barrier()
; #define PG8_SCHED __builtin_amdgcn_sched_barrier(0)
; template <class Epi, class Sched, bool ALIGN_EPI = false, bool SP2 = false, bool F8 = false>
; __device__ __forceinline__ void gemm_phase(PG8_LAS unsigned char* lds, const Gemm g, const Sched& S, const Epi& E, const int tidb  ) {
;     ...
;             const bool last = (t == nt - 2);
;             if constexpr (Epi::PREFETCH) { if (t == 0) E.prefetch(cur, wid, lane); }
;             const char* a1 = cA + (size_t)(t + 1) * kstep;
;             const char* a2 = last ? nA : cA + (size_t)(t + 2) * kstep; const char* b2 = last ? nB : cB + (size_t)(t + 2) * kstep;
;             const char* a3 = a2 + kstep; const char* b3 = b2 + kstep;
;             if (last && has_next) S.a_ready(nxt);
;             if constexpr (SP2) {
;             PG8_LDB(B0, 0, 0); PG8_LDB(B1, 0, 1); PG8_SCHED; PG8_LDA(At, 0, 0); PG8_STAGE(PG8_SA(1, 1), a1 + hstep, voffA);
;             PG8_WAIT_V(8); PG8_WAIT_L(0); PG8_BAR; PG8_MMA(0, 0, At, B0); PG8_MMA(0, 1, At, B1); PG8_BAR; PG8_SCHED;
;             PG8_LDA(At, 0, 1); PG8_STAGE(PG8_SB(0, 0), b2, voffB); PG8_STAGE(PG8_SB(0, 1), b2 + hstep, voffB); PG8_STAGE(PG8_SA(0, 0), a2, voffA);
;             PG8_WAIT_V(8); PG8_WAIT_L(0); PG8_BAR; PG8_MMA(1, 0, At, B0); PG8_MMA(1, 1, At, B1); PG8_BAR; PG8_SCHED;
.LBB0_1371:
	s_add_i32 s65, s24, 2
	s_add_u32 s67, s22, 0x80
	s_addc_u32 s25, s23, 0
	s_add_i32 s66, 0, 0x10000
	s_cmp_eq_u32 s57, s24
	s_cselect_b32 s25, s5, s25
	s_cselect_b32 s24, s4, s67
	v_add_u32_e32 v0, s66, v192
	s_cselect_b64 vcc, -1, 0
	s_add_i32 s67, 0, 0x14000
	ds_read_b128 v[18:21], v0
	ds_read_b128 v[22:25], v0 offset:1024
	ds_read_b128 v[26:29], v0 offset:2048
	ds_read_b128 v[30:33], v0 offset:3072
	v_add_u32_e32 v0, s67, v192
	ds_read_b128 v[2:5], v0
	ds_read_b128 v[6:9], v0 offset:1024
	ds_read_b128 v[10:13], v0 offset:2048
	ds_read_b128 v[14:17], v0 offset:3072
	v_cndmask_b32_e32 v189, v179, v177, vcc
	v_cndmask_b32_e32 v188, v178, v176, vcc
	v_lshl_add_u64 v[190:191], s[22:23], 0, v[172:173]
	s_add_i32 m0, s50, 0xc000
	ds_read_b128 v[180:183], v194
	ds_read_b128 v[184:187], v194 offset:1024
	ds_read_b128 v[204:207], v194 offset:2048
	ds_read_b128 v[208:211], v194 offset:3072
	ds_read_b128 v[212:215], v194 offset:4096
	ds_read_b128 v[216:219], v194 offset:5120
	ds_read_b128 v[220:223], v194 offset:6144
	ds_read_b128 v[224:227], v194 offset:7168
	global_load_lds_dwordx4 v[190:191], off
	v_lshl_add_u64 v[190:191], s[22:23], 0, v[174:175]
	s_add_i32 m0, s50, 0xe000
	s_nop 0
	global_load_lds_dwordx4 v[190:191], off
	s_waitcnt vmcnt(8)
	s_waitcnt lgkmcnt(0)
	s_barrier
	s_setprio 1
	s_waitcnt lgkmcnt(0)
	v_mfma_scale_f32_16x16x128_f8f6f4 v[154:157], v[18:25], v[180:187], v[154:157], v246, v253 op_sel_hi:[0,0,0]
	v_mfma_scale_f32_16x16x128_f8f6f4 v[150:153], v[26:33], v[180:187], v[150:153], v246, v253 op_sel_hi:[0,0,0]
	v_mfma_scale_f32_16x16x128_f8f6f4 v[142:145], v[18:25], v[204:211], v[142:145], v246, v253 op_sel_hi:[0,0,0]
	v_mfma_scale_f32_16x16x128_f8f6f4 v[134:137], v[26:33], v[204:211], v[134:137], v246, v253 op_sel_hi:[0,0,0]
	v_mfma_scale_f32_16x16x128_f8f6f4 v[126:129], v[18:25], v[212:219], v[126:129], v246, v253 op_sel_hi:[0,0,0]
	v_mfma_scale_f32_16x16x128_f8f6f4 v[118:121], v[26:33], v[212:219], v[118:121], v246, v253 op_sel_hi:[0,0,0]
	v_mfma_scale_f32_16x16x128_f8f6f4 v[110:113], v[18:25], v[220:227], v[110:113], v246, v253 op_sel_hi:[0,0,0]
	v_mfma_scale_f32_16x16x128_f8f6f4 v[102:105], v[26:33], v[220:227], v[102:105], v246, v253 op_sel_hi:[0,0,0]
	s_setprio 0
	s_setprio 1
	v_mfma_scale_f32_16x16x128_f8f6f4 v[158:161], v[2:9], v[180:187], v[158:161], v246, v253 op_sel_hi:[0,0,0]
	v_mfma_scale_f32_16x16x128_f8f6f4 v[146:149], v[10:17], v[180:187], v[146:149], v246, v253 op_sel_hi:[0,0,0]
	v_mfma_scale_f32_16x16x128_f8f6f4 v[138:141], v[2:9], v[204:211], v[138:141], v246, v253 op_sel_hi:[0,0,0]
	v_mfma_scale_f32_16x16x128_f8f6f4 v[130:133], v[10:17], v[204:211], v[130:133], v246, v253 op_sel_hi:[0,0,0]
	v_mfma_scale_f32_16x16x128_f8f6f4 v[122:125], v[2:9], v[212:219], v[122:125], v246, v253 op_sel_hi:[0,0,0]
	v_mfma_scale_f32_16x16x128_f8f6f4 v[114:117], v[10:17], v[212:219], v[114:117], v246, v253 op_sel_hi:[0,0,0]
	v_mfma_scale_f32_16x16x128_f8f6f4 v[106:109], v[2:9], v[220:227], v[106:109], v246, v253 op_sel_hi:[0,0,0]
	v_mfma_scale_f32_16x16x128_f8f6f4 v[98:101], v[10:17], v[220:227], v[98:101], v246, v253 op_sel_hi:[0,0,0]
	s_setprio 2
	s_barrier
	s_add_i32 s66, s66, s49
	v_lshl_add_u64 v[180:181], v[188:189], 0, v[166:167]
	s_mov_b32 m0, s66
	ds_read_b128 v[204:207], v194 offset:16384
	ds_read_b128 v[208:211], v194 offset:17408
	ds_read_b128 v[212:215], v194 offset:18432
	ds_read_b128 v[216:219], v194 offset:19456
	ds_read_b128 v[220:223], v194 offset:20480
	ds_read_b128 v[224:227], v194 offset:21504
	ds_read_b128 v[228:231], v194 offset:22528
	ds_read_b128 v[232:235], v194 offset:23552
	global_load_lds_dwordx4 v[180:181], off
	v_lshl_add_u64 v[182:183], v[188:189], 0, v[170:171]
	s_add_i32 m0, s66, 0x2000
	v_lshl_add_u64 v[186:187], v[188:189], 0, s[10:11]
	s_add_i32 s66, s67, s49
	global_load_lds_dwordx4 v[182:183], off
	v_lshl_add_u64 v[184:185], v[186:187], 0, v[166:167]
	s_mov_b32 m0, s66
	v_lshl_add_u64 v[186:187], v[186:187], 0, v[170:171]
	global_load_lds_dwordx4 v[184:185], off
	s_add_i32 m0, s66, 0x2000
	v_lshl_add_u64 v[188:189], s[24:25], 0, v[164:165]
	global_load_lds_dwordx4 v[186:187], off
	s_mov_b32 m0, s50
	v_lshl_add_u64 v[190:191], s[24:25], 0, v[168:169]
	global_load_lds_dwordx4 v[188:189], off
	s_mov_b32 m0, s51
	s_nop 0
	global_load_lds_dwordx4 v[190:191], off
	s_waitcnt vmcnt(8)
	s_waitcnt lgkmcnt(0)
	s_barrier
	s_setprio 1
	s_waitcnt lgkmcnt(0)
	v_mfma_scale_f32_16x16x128_f8f6f4 v[94:97], v[18:25], v[204:211], v[94:97], v246, v253 op_sel_hi:[0,0,0]
	v_mfma_scale_f32_16x16x128_f8f6f4 v[86:89], v[26:33], v[204:211], v[86:89], v246, v253 op_sel_hi:[0,0,0]
	v_mfma_scale_f32_16x16x128_f8f6f4 v[78:81], v[18:25], v[212:219], v[78:81], v246, v253 op_sel_hi:[0,0,0]
	v_mfma_scale_f32_16x16x128_f8f6f4 v[70:73], v[26:33], v[212:219], v[70:73], v246, v253 op_sel_hi:[0,0,0]
	v_mfma_scale_f32_16x16x128_f8f6f4 v[62:65], v[18:25], v[220:227], v[62:65], v246, v253 op_sel_hi:[0,0,0]
	v_mfma_scale_f32_16x16x128_f8f6f4 v[54:57], v[26:33], v[220:227], v[54:57], v246, v253 op_sel_hi:[0,0,0]
	v_mfma_scale_f32_16x16x128_f8f6f4 v[46:49], v[18:25], v[228:235], v[46:49], v246, v253 op_sel_hi:[0,0,0]
	v_mfma_scale_f32_16x16x128_f8f6f4 v[38:41], v[26:33], v[228:235], v[38:41], v246, v253 op_sel_hi:[0,0,0]
	s_setprio 0
	s_setprio 1
	v_mfma_scale_f32_16x16x128_f8f6f4 v[90:93], v[2:9], v[204:211], v[90:93], v246, v253 op_sel_hi:[0,0,0]
	v_mfma_scale_f32_16x16x128_f8f6f4 v[82:85], v[10:17], v[204:211], v[82:85], v246, v253 op_sel_hi:[0,0,0]
	v_mfma_scale_f32_16x16x128_f8f6f4 v[74:77], v[2:9], v[212:219], v[74:77], v246, v253 op_sel_hi:[0,0,0]
	v_mfma_scale_f32_16x16x128_f8f6f4 v[66:69], v[10:17], v[212:219], v[66:69], v246, v253 op_sel_hi:[0,0,0]
	v_mfma_scale_f32_16x16x128_f8f6f4 v[58:61], v[2:9], v[220:227], v[58:61], v246, v253 op_sel_hi:[0,0,0]
	v_mfma_scale_f32_16x16x128_f8f6f4 v[50:53], v[10:17], v[220:227], v[50:53], v246, v253 op_sel_hi:[0,0,0]
	v_mfma_scale_f32_16x16x128_f8f6f4 v[42:45], v[2:9], v[228:235], v[42:45], v246, v253 op_sel_hi:[0,0,0]
	v_mfma_scale_f32_16x16x128_f8f6f4 v[34:37], v[10:17], v[228:235], v[34:37], v246, v253 op_sel_hi:[0,0,0]
	s_setprio 2
	s_barrier
; #define PG8_STAGE(bufoff, gbase, voff) do { _Pragma("unroll") for (int _i = 0; _i < 2; ++_i) \
;         __builtin_amdgcn_global_load_lds((const unsigned*)((const char*)(gbase) + (voff)[_i]), (PG8_LAS unsigned*)(lds + (bufoff) + ldsw + _i * 8192), 16, 0, 0); } while (0)
; #define PG8_WAIT_V(n) asm volatile("s_waitcnt vmcnt(" #n ")" ::: "memory")
; #define PG8_WAIT_L(n) asm volatile("s_waitcnt lgkmcnt(" #n ")" ::: "memory")
; #define PG8_BAR __builtin_amdgcn_s_barrier()
; #define PG8_SCHED __builtin_amdgcn_sched_barrier(0)
; template <class Epi, class Sched, bool ALIGN_EPI = false, bool SP2 = false, bool F8 = false>
; __device__ __forceinline__ void gemm_phase(PG8_LAS unsigned char* lds, const Gemm g, const Sched& S, const Epi& E, const int tidb  ) {
;     ...
;             PG8_LDB(B0, 1, 0); PG8_LDB(B1, 1, 1); PG8_SCHED; PG8_LDA(At, 1, 0); PG8_STAGE(PG8_SA(0, 1), a2 + hstep, voffA);
;             PG8_WAIT_V(8); PG8_WAIT_L(0); PG8_BAR; PG8_MMA(0, 0, At, B0); PG8_MMA(0, 1, At, B1); PG8_BAR; PG8_SCHED;
;             PG8_LDA(At, 1, 1); PG8_STAGE(PG8_SB(1, 0), b3, voffB); PG8_STAGE(PG8_SB(1, 1), b3 + hstep, voffB); PG8_STAGE(PG8_SA(1, 0), a3, voffA);
;             PG8_WAIT_V(8); PG8_WAIT_L(0); PG8_BAR; PG8_MMA(1, 0, At, B0); PG8_MMA(1, 1, At, B1); PG8_BAR; PG8_SCHED;
	s_add_i32 s66, 0, 0x18000
	v_add_u32_e32 v0, s66, v192
	s_add_i32 s67, 0, 0x1c000
	ds_read_b128 v[2:5], v0
	ds_read_b128 v[6:9], v0 offset:1024
	ds_read_b128 v[10:13], v0 offset:2048
	ds_read_b128 v[14:17], v0 offset:3072
	v_add_u32_e32 v0, s67, v192
	ds_read_b128 v[18:21], v0
	ds_read_b128 v[22:25], v0 offset:1024
	ds_read_b128 v[26:29], v0 offset:2048
	ds_read_b128 v[30:33], v0 offset:3072
	s_add_u32 s24, s24, s10
	s_addc_u32 s25, s25, s11
	s_mov_b32 m0, s52
	v_lshl_add_u64 v[196:197], s[24:25], 0, v[164:165]
	ds_read_b128 v[204:207], v194 offset:32768
	ds_read_b128 v[208:211], v194 offset:33792
	ds_read_b128 v[212:215], v194 offset:34816
	ds_read_b128 v[216:219], v194 offset:35840
	ds_read_b128 v[220:223], v194 offset:36864
	ds_read_b128 v[224:227], v194 offset:37888
	ds_read_b128 v[228:231], v194 offset:38912
	ds_read_b128 v[232:235], v194 offset:39936
	global_load_lds_dwordx4 v[196:197], off
	v_lshl_add_u64 v[196:197], s[24:25], 0, v[168:169]
	s_mov_b32 m0, s53
	s_nop 0
	global_load_lds_dwordx4 v[196:197], off
	s_waitcnt vmcnt(8)
	s_waitcnt lgkmcnt(0)
	s_barrier
	s_setprio 1
	s_waitcnt lgkmcnt(0)
	v_mfma_scale_f32_16x16x128_f8f6f4 v[154:157], v[2:9], v[204:211], v[154:157], v246, v253 op_sel_hi:[0,0,0]
	v_mfma_scale_f32_16x16x128_f8f6f4 v[150:153], v[10:17], v[204:211], v[150:153], v246, v253 op_sel_hi:[0,0,0]
	v_mfma_scale_f32_16x16x128_f8f6f4 v[142:145], v[2:9], v[212:219], v[142:145], v246, v253 op_sel_hi:[0,0,0]
	v_mfma_scale_f32_16x16x128_f8f6f4 v[134:137], v[10:17], v[212:219], v[134:137], v246, v253 op_sel_hi:[0,0,0]
	v_mfma_scale_f32_16x16x128_f8f6f4 v[126:129], v[2:9], v[220:227], v[126:129], v246, v253 op_sel_hi:[0,0,0]
	v_mfma_scale_f32_16x16x128_f8f6f4 v[118:121], v[10:17], v[220:227], v[118:121], v246, v253 op_sel_hi:[0,0,0]
	v_mfma_scale_f32_16x16x128_f8f6f4 v[110:113], v[2:9], v[228:235], v[110:113], v246, v253 op_sel_hi:[0,0,0]
	v_mfma_scale_f32_16x16x128_f8f6f4 v[102:105], v[10:17], v[228:235], v[102:105], v246, v253 op_sel_hi:[0,0,0]
	s_setprio 0
	s_setprio 1
	v_mfma_scale_f32_16x16x128_f8f6f4 v[158:161], v[18:25], v[204:211], v[158:161], v246, v253 op_sel_hi:[0,0,0]
	v_mfma_scale_f32_16x16x128_f8f6f4 v[146:149], v[26:33], v[204:211], v[146:149], v246, v253 op_sel_hi:[0,0,0]
	v_mfma_scale_f32_16x16x128_f8f6f4 v[138:141], v[18:25], v[212:219], v[138:141], v246, v253 op_sel_hi:[0,0,0]
	v_mfma_scale_f32_16x16x128_f8f6f4 v[130:133], v[26:33], v[212:219], v[130:133], v246, v253 op_sel_hi:[0,0,0]
	v_mfma_scale_f32_16x16x128_f8f6f4 v[122:125], v[18:25], v[220:227], v[122:125], v246, v253 op_sel_hi:[0,0,0]
	v_mfma_scale_f32_16x16x128_f8f6f4 v[114:117], v[26:33], v[220:227], v[114:117], v246, v253 op_sel_hi:[0,0,0]
	v_mfma_scale_f32_16x16x128_f8f6f4 v[106:109], v[18:25], v[228:235], v[106:109], v246, v253 op_sel_hi:[0,0,0]
	v_mfma_scale_f32_16x16x128_f8f6f4 v[98:101], v[26:33], v[228:235], v[98:101], v246, v253 op_sel_hi:[0,0,0]
	s_setprio 2
	s_barrier
	s_add_i32 s24, s66, s49
	v_lshl_add_u64 v[180:181], v[180:181], 0, s[92:93]
	s_mov_b32 m0, s24
	ds_read_b128 v[204:207], v194 offset:49152
	ds_read_b128 v[208:211], v194 offset:50176
	ds_read_b128 v[212:215], v194 offset:51200
	ds_read_b128 v[216:219], v194 offset:52224
	ds_read_b128 v[220:223], v194 offset:53248
	ds_read_b128 v[224:227], v194 offset:54272
	ds_read_b128 v[228:231], v194 offset:55296
	ds_read_b128 v[232:235], v194 offset:56320
	global_load_lds_dwordx4 v[180:181], off
	v_lshl_add_u64 v[180:181], v[182:183], 0, s[92:93]
	s_add_i32 m0, s24, 0x2000
	s_add_i32 s24, s67, s49
	global_load_lds_dwordx4 v[180:181], off
	v_lshl_add_u64 v[180:181], v[184:185], 0, s[92:93]
	s_mov_b32 m0, s24
	s_nop 0
	global_load_lds_dwordx4 v[180:181], off
	v_lshl_add_u64 v[180:181], v[186:187], 0, s[92:93]
	s_add_i32 m0, s24, 0x2000
	s_nop 0
	global_load_lds_dwordx4 v[180:181], off
	v_lshl_add_u64 v[180:181], v[188:189], 0, s[92:93]
	s_mov_b32 m0, s54
	s_nop 0
	global_load_lds_dwordx4 v[180:181], off
	v_lshl_add_u64 v[180:181], v[190:191], 0, s[92:93]
	s_mov_b32 m0, s55
	s_nop 0
	global_load_lds_dwordx4 v[180:181], off
	s_waitcnt vmcnt(8)
	s_waitcnt lgkmcnt(0)
	s_barrier
	s_setprio 1
	s_waitcnt lgkmcnt(0)
	v_mfma_scale_f32_16x16x128_f8f6f4 v[94:97], v[2:9], v[204:211], v[94:97], v246, v253 op_sel_hi:[0,0,0]
	v_mfma_scale_f32_16x16x128_f8f6f4 v[86:89], v[10:17], v[204:211], v[86:89], v246, v253 op_sel_hi:[0,0,0]
	v_mfma_scale_f32_16x16x128_f8f6f4 v[78:81], v[2:9], v[212:219], v[78:81], v246, v253 op_sel_hi:[0,0,0]
	v_mfma_scale_f32_16x16x128_f8f6f4 v[70:73], v[10:17], v[212:219], v[70:73], v246, v253 op_sel_hi:[0,0,0]
	v_mfma_scale_f32_16x16x128_f8f6f4 v[62:65], v[2:9], v[220:227], v[62:65], v246, v253 op_sel_hi:[0,0,0]
	v_mfma_scale_f32_16x16x128_f8f6f4 v[54:57], v[10:17], v[220:227], v[54:57], v246, v253 op_sel_hi:[0,0,0]
	v_mfma_scale_f32_16x16x128_f8f6f4 v[46:49], v[2:9], v[228:235], v[46:49], v246, v253 op_sel_hi:[0,0,0]
	v_mfma_scale_f32_16x16x128_f8f6f4 v[38:41], v[10:17], v[228:235], v[38:41], v246, v253 op_sel_hi:[0,0,0]
	s_setprio 0
	s_setprio 1
	v_mfma_scale_f32_16x16x128_f8f6f4 v[90:93], v[18:25], v[204:211], v[90:93], v246, v253 op_sel_hi:[0,0,0]
	v_mfma_scale_f32_16x16x128_f8f6f4 v[82:85], v[26:33], v[204:211], v[82:85], v246, v253 op_sel_hi:[0,0,0]
	v_mfma_scale_f32_16x16x128_f8f6f4 v[74:77], v[18:25], v[212:219], v[74:77], v246, v253 op_sel_hi:[0,0,0]
	v_mfma_scale_f32_16x16x128_f8f6f4 v[66:69], v[26:33], v[212:219], v[66:69], v246, v253 op_sel_hi:[0,0,0]
	v_mfma_scale_f32_16x16x128_f8f6f4 v[58:61], v[18:25], v[220:227], v[58:61], v246, v253 op_sel_hi:[0,0,0]
	v_mfma_scale_f32_16x16x128_f8f6f4 v[50:53], v[26:33], v[220:227], v[50:53], v246, v253 op_sel_hi:[0,0,0]
	v_mfma_scale_f32_16x16x128_f8f6f4 v[42:45], v[18:25], v[228:235], v[42:45], v246, v253 op_sel_hi:[0,0,0]
	v_mfma_scale_f32_16x16x128_f8f6f4 v[34:37], v[26:33], v[228:235], v[34:37], v246, v253 op_sel_hi:[0,0,0]
	s_setprio 2
	s_barrier
	s_add_u32 s22, s22, 0x100
	s_addc_u32 s23, s23, 0
	v_lshl_add_u64 v[178:179], v[178:179], 0, s[84:85]
	s_cmp_ge_i32 s65, s56
	s_mov_b32 s24, s65
	s_cbranch_scc0 .LBB0_1371
	s_movk_i32 s67, 0x300

; #define PG8_STAGE(bufoff, gbase, voff) do { _Pragma("unroll") for (int _i = 0; _i < 2; ++_i) \
;         __builtin_amdgcn_global_load_lds((const unsigned*)((const char*)(gbase) + (voff)[_i]), (PG8_LAS unsigned*)(lds + (bufoff) + ldsw + _i * 8192), 16, 0, 0); } while (0)
; #define PG8_WAIT_V(n) asm volatile("s_waitcnt vmcnt(" #n ")" ::: "memory")
; #define PG8_WAIT_L(n) asm volatile("s_waitcnt lgkmcnt(" #n ")" ::: "memory")
; #define PG8_BAR __builtin_amdgcn_s_barrier()
; #define PG8_SCHED __builtin_amdgcn_sched_barrier(0)
; template <class Epi, class Sched, bool ALIGN_EPI = false, bool SP2 = false, bool F8 = false>
; __device__ __forceinline__ void gemm_phase(PG8_LAS unsigned char* lds, const Gemm g, const Sched& S, const Epi& E, const int tidb  ) {
;     ...
;             const bool last = (t == nt - 2);
;             if constexpr (Epi::PREFETCH) { if (t == 0) E.prefetch(cur, wid, lane); }
;             const char* a1 = cA + (size_t)(t + 1) * kstep;
;             const char* a2 = last ? nA : cA + (size_t)(t + 2) * kstep; const char* b2 = last ? nB : cB + (size_t)(t + 2) * kstep;
;             const char* a3 = a2 + kstep; const char* b3 = b2 + kstep;
;             if (last && has_next) S.a_ready(nxt);
;             if constexpr (SP2) {
;             PG8_LDB(B0, 0, 0); PG8_LDB(B1, 0, 1); PG8_SCHED; PG8_LDA(At, 0, 0); PG8_STAGE(PG8_SA(1, 1), a1 + hstep, voffA);
;             PG8_WAIT_V(8); PG8_WAIT_L(0); PG8_BAR; PG8_MMA(0, 0, At, B0); PG8_MMA(0, 1, At, B1); PG8_BAR; PG8_SCHED;
;             PG8_LDA(At, 0, 1); PG8_STAGE(PG8_SB(0, 0), b2, voffB); PG8_STAGE(PG8_SB(0, 1), b2 + hstep, voffB); PG8_STAGE(PG8_SA(0, 0), a2, voffA);
;             PG8_WAIT_V(8); PG8_WAIT_L(0); PG8_BAR; PG8_MMA(1, 0, At, B0); PG8_MMA(1, 1, At, B1); PG8_BAR; PG8_SCHED;
.LBB0_1452:
	ds_read_b128 v[6:9], v175 offset:3072
	ds_read_b128 v[2:5], v175 offset:2048
	ds_read_b128 v[182:185], v175 offset:1024
	ds_read_b128 v[178:181], v175
	ds_read_b128 v[190:193], v0 offset:3072
	ds_read_b128 v[186:189], v0 offset:2048
	ds_read_b128 v[208:211], v0 offset:1024
	ds_read_b128 v[204:207], v0
	s_add_u32 s54, s52, 0x80
	s_addc_u32 s55, s53, 0
	s_cmp_eq_u32 s66, s72
	s_cselect_b64 vcc, -1, 0
	s_cselect_b32 s55, s7, s55
	s_cselect_b32 s54, s6, s54
	v_cndmask_b32_e32 v161, v155, v153, vcc
	v_cndmask_b32_e32 v160, v154, v152, vcc
	s_mov_b32 m0, s35
	v_lshl_add_u64 v[156:157], s[52:53], 0, v[148:149]
	ds_read_b128 v[212:215], v174
	ds_read_b128 v[216:219], v174 offset:1024
	ds_read_b128 v[220:223], v174 offset:2048
	ds_read_b128 v[224:227], v174 offset:3072
	ds_read_b128 v[228:231], v174 offset:4096
	ds_read_b128 v[232:235], v174 offset:5120
	ds_read_b128 v[236:239], v174 offset:6144
	ds_read_b128 v[240:243], v174 offset:7168
	global_load_lds_dwordx4 v[156:157], off
	v_lshl_add_u64 v[156:157], s[52:53], 0, v[150:151]
	s_mov_b32 m0, s56
	s_nop 0
	global_load_lds_dwordx4 v[156:157], off
	s_waitcnt vmcnt(8)
	s_waitcnt lgkmcnt(0)
	s_barrier
	s_setprio 1
	s_waitcnt lgkmcnt(0)
	v_mfma_scale_f32_16x16x128_f8f6f4 v[134:137], v[204:211], v[212:219], v[134:137], v246, v247 op_sel_hi:[0,0,0]
	v_mfma_scale_f32_16x16x128_f8f6f4 v[130:133], v[186:193], v[212:219], v[130:133], v246, v247 op_sel_hi:[0,0,0]
	v_mfma_scale_f32_16x16x128_f8f6f4 v[118:121], v[204:211], v[220:227], v[118:121], v246, v247 op_sel_hi:[0,0,0]
	v_mfma_scale_f32_16x16x128_f8f6f4 v[114:117], v[186:193], v[220:227], v[114:117], v246, v247 op_sel_hi:[0,0,0]
	v_mfma_scale_f32_16x16x128_f8f6f4 v[102:105], v[204:211], v[228:235], v[102:105], v246, v247 op_sel_hi:[0,0,0]
	v_mfma_scale_f32_16x16x128_f8f6f4 v[98:101], v[186:193], v[228:235], v[98:101], v246, v247 op_sel_hi:[0,0,0]
	v_mfma_scale_f32_16x16x128_f8f6f4 v[86:89], v[204:211], v[236:243], v[86:89], v246, v247 op_sel_hi:[0,0,0]
	v_mfma_scale_f32_16x16x128_f8f6f4 v[82:85], v[186:193], v[236:243], v[82:85], v246, v247 op_sel_hi:[0,0,0]
	s_setprio 0
	s_setprio 1
	v_mfma_scale_f32_16x16x128_f8f6f4 v[126:129], v[178:185], v[212:219], v[126:129], v246, v247 op_sel_hi:[0,0,0]
	v_mfma_scale_f32_16x16x128_f8f6f4 v[122:125], v[2:9], v[212:219], v[122:125], v246, v247 op_sel_hi:[0,0,0]
	v_mfma_scale_f32_16x16x128_f8f6f4 v[110:113], v[178:185], v[220:227], v[110:113], v246, v247 op_sel_hi:[0,0,0]
	v_mfma_scale_f32_16x16x128_f8f6f4 v[106:109], v[2:9], v[220:227], v[106:109], v246, v247 op_sel_hi:[0,0,0]
	v_mfma_scale_f32_16x16x128_f8f6f4 v[94:97], v[178:185], v[228:235], v[94:97], v246, v247 op_sel_hi:[0,0,0]
	v_mfma_scale_f32_16x16x128_f8f6f4 v[90:93], v[2:9], v[228:235], v[90:93], v246, v247 op_sel_hi:[0,0,0]
	v_mfma_scale_f32_16x16x128_f8f6f4 v[78:81], v[178:185], v[236:243], v[78:81], v246, v247 op_sel_hi:[0,0,0]
	v_mfma_scale_f32_16x16x128_f8f6f4 v[70:73], v[2:9], v[236:243], v[70:73], v246, v247 op_sel_hi:[0,0,0]
	s_setprio 2
	s_barrier
	s_mov_b32 m0, s57
	v_lshl_add_u64 v[156:157], v[160:161], 0, v[140:141]
	ds_read_b128 v[212:215], v174 offset:16384
	ds_read_b128 v[216:219], v174 offset:17408
	ds_read_b128 v[220:223], v174 offset:18432
	ds_read_b128 v[224:227], v174 offset:19456
	ds_read_b128 v[228:231], v174 offset:20480
	ds_read_b128 v[232:235], v174 offset:21504
	ds_read_b128 v[236:239], v174 offset:22528
	ds_read_b128 v[240:243], v174 offset:23552
	global_load_lds_dwordx4 v[156:157], off
	v_lshl_add_u64 v[158:159], v[160:161], 0, v[144:145]
	s_mov_b32 m0, s68
	v_lshl_add_u64 v[164:165], v[160:161], 0, s[16:17]
	global_load_lds_dwordx4 v[158:159], off
	v_lshl_add_u64 v[160:161], v[164:165], 0, v[140:141]
	s_mov_b32 m0, s70
	v_lshl_add_u64 v[164:165], v[164:165], 0, v[144:145]
	global_load_lds_dwordx4 v[160:161], off
	s_mov_b32 m0, s71
	v_lshl_add_u64 v[166:167], s[54:55], 0, v[138:139]
	global_load_lds_dwordx4 v[164:165], off
	s_mov_b32 m0, s59
	v_lshl_add_u64 v[168:169], s[54:55], 0, v[142:143]
	global_load_lds_dwordx4 v[166:167], off
	s_mov_b32 m0, s60
	s_nop 0
	global_load_lds_dwordx4 v[168:169], off
	s_waitcnt vmcnt(8)
	s_waitcnt lgkmcnt(0)
	s_barrier
	s_setprio 1
	s_waitcnt lgkmcnt(0)
	v_mfma_scale_f32_16x16x128_f8f6f4 v[74:77], v[204:211], v[212:219], v[74:77], v246, v247 op_sel_hi:[0,0,0]
	v_mfma_scale_f32_16x16x128_f8f6f4 v[66:69], v[186:193], v[212:219], v[66:69], v246, v247 op_sel_hi:[0,0,0]
	v_mfma_scale_f32_16x16x128_f8f6f4 v[54:57], v[204:211], v[220:227], v[54:57], v246, v247 op_sel_hi:[0,0,0]
	v_mfma_scale_f32_16x16x128_f8f6f4 v[50:53], v[186:193], v[220:227], v[50:53], v246, v247 op_sel_hi:[0,0,0]
	v_mfma_scale_f32_16x16x128_f8f6f4 v[38:41], v[204:211], v[228:235], v[38:41], v246, v247 op_sel_hi:[0,0,0]
	v_mfma_scale_f32_16x16x128_f8f6f4 v[34:37], v[186:193], v[228:235], v[34:37], v246, v247 op_sel_hi:[0,0,0]
	v_mfma_scale_f32_16x16x128_f8f6f4 v[22:25], v[204:211], v[236:243], v[22:25], v246, v247 op_sel_hi:[0,0,0]
	v_mfma_scale_f32_16x16x128_f8f6f4 v[18:21], v[186:193], v[236:243], v[18:21], v246, v247 op_sel_hi:[0,0,0]
	s_setprio 0
	s_setprio 1
	v_mfma_scale_f32_16x16x128_f8f6f4 v[62:65], v[178:185], v[212:219], v[62:65], v246, v247 op_sel_hi:[0,0,0]
	v_mfma_scale_f32_16x16x128_f8f6f4 v[58:61], v[2:9], v[212:219], v[58:61], v246, v247 op_sel_hi:[0,0,0]
	v_mfma_scale_f32_16x16x128_f8f6f4 v[46:49], v[178:185], v[220:227], v[46:49], v246, v247 op_sel_hi:[0,0,0]
	v_mfma_scale_f32_16x16x128_f8f6f4 v[42:45], v[2:9], v[220:227], v[42:45], v246, v247 op_sel_hi:[0,0,0]
	v_mfma_scale_f32_16x16x128_f8f6f4 v[30:33], v[178:185], v[228:235], v[30:33], v246, v247 op_sel_hi:[0,0,0]
	v_mfma_scale_f32_16x16x128_f8f6f4 v[26:29], v[2:9], v[228:235], v[26:29], v246, v247 op_sel_hi:[0,0,0]
	v_mfma_scale_f32_16x16x128_f8f6f4 v[14:17], v[178:185], v[236:243], v[14:17], v246, v247 op_sel_hi:[0,0,0]
	v_mfma_scale_f32_16x16x128_f8f6f4 v[10:13], v[2:9], v[236:243], v[10:13], v246, v247 op_sel_hi:[0,0,0]
	s_setprio 2
	s_barrier
; #define PG8_STAGE(bufoff, gbase, voff) do { _Pragma("unroll") for (int _i = 0; _i < 2; ++_i) \
;         __builtin_amdgcn_global_load_lds((const unsigned*)((const char*)(gbase) + (voff)[_i]), (PG8_LAS unsigned*)(lds + (bufoff) + ldsw + _i * 8192), 16, 0, 0); } while (0)
; #define PG8_WAIT_V(n) asm volatile("s_waitcnt vmcnt(" #n ")" ::: "memory")
; #define PG8_WAIT_L(n) asm volatile("s_waitcnt lgkmcnt(" #n ")" ::: "memory")
; #define PG8_BAR __builtin_amdgcn_s_barrier()
; #define PG8_SCHED __builtin_amdgcn_sched_barrier(0)
; template <class Epi, class Sched, bool ALIGN_EPI = false, bool SP2 = false, bool F8 = false>
; __device__ __forceinline__ void gemm_phase(PG8_LAS unsigned char* lds, const Gemm g, const Sched& S, const Epi& E, const int tidb  ) {
;     ...
;             PG8_LDB(B0, 1, 0); PG8_LDB(B1, 1, 1); PG8_SCHED; PG8_LDA(At, 1, 0); PG8_STAGE(PG8_SA(0, 1), a2 + hstep, voffA);
;             PG8_WAIT_V(8); PG8_WAIT_L(0); PG8_BAR; PG8_MMA(0, 0, At, B0); PG8_MMA(0, 1, At, B1); PG8_BAR; PG8_SCHED;
;             PG8_LDA(At, 1, 1); PG8_STAGE(PG8_SB(1, 0), b3, voffB); PG8_STAGE(PG8_SB(1, 1), b3 + hstep, voffB); PG8_STAGE(PG8_SA(1, 0), a3, voffA);
;             PG8_WAIT_V(8); PG8_WAIT_L(0); PG8_BAR; PG8_MMA(1, 0, At, B0); PG8_MMA(1, 1, At, B1); PG8_BAR; PG8_SCHED;
	ds_read_b128 v[178:181], v176
	ds_read_b128 v[182:185], v176 offset:1024
	ds_read_b128 v[186:189], v176 offset:2048
	ds_read_b128 v[190:193], v176 offset:3072
	ds_read_b128 v[2:5], v177
	ds_read_b128 v[6:9], v177 offset:1024
	ds_read_b128 v[204:207], v177 offset:2048
	ds_read_b128 v[208:211], v177 offset:3072
	s_add_u32 s54, s54, s16
	s_addc_u32 s55, s55, s17
	s_mov_b32 m0, s61
	v_lshl_add_u64 v[194:195], s[54:55], 0, v[138:139]
	ds_read_b128 v[212:215], v174 offset:32768
	ds_read_b128 v[216:219], v174 offset:33792
	ds_read_b128 v[220:223], v174 offset:34816
	ds_read_b128 v[224:227], v174 offset:35840
	ds_read_b128 v[228:231], v174 offset:36864
	ds_read_b128 v[232:235], v174 offset:37888
	ds_read_b128 v[236:239], v174 offset:38912
	ds_read_b128 v[240:243], v174 offset:39936
	global_load_lds_dwordx4 v[194:195], off
	v_lshl_add_u64 v[194:195], s[54:55], 0, v[142:143]
	s_mov_b32 m0, s62
	s_nop 0
	global_load_lds_dwordx4 v[194:195], off
	s_waitcnt vmcnt(8)
	s_waitcnt lgkmcnt(0)
	s_barrier
	s_setprio 1
	s_waitcnt lgkmcnt(0)
	v_mfma_scale_f32_16x16x128_f8f6f4 v[134:137], v[178:185], v[212:219], v[134:137], v246, v247 op_sel_hi:[0,0,0]
	v_mfma_scale_f32_16x16x128_f8f6f4 v[130:133], v[186:193], v[212:219], v[130:133], v246, v247 op_sel_hi:[0,0,0]
	v_mfma_scale_f32_16x16x128_f8f6f4 v[118:121], v[178:185], v[220:227], v[118:121], v246, v247 op_sel_hi:[0,0,0]
	v_mfma_scale_f32_16x16x128_f8f6f4 v[114:117], v[186:193], v[220:227], v[114:117], v246, v247 op_sel_hi:[0,0,0]
	v_mfma_scale_f32_16x16x128_f8f6f4 v[102:105], v[178:185], v[228:235], v[102:105], v246, v247 op_sel_hi:[0,0,0]
	v_mfma_scale_f32_16x16x128_f8f6f4 v[98:101], v[186:193], v[228:235], v[98:101], v246, v247 op_sel_hi:[0,0,0]
	v_mfma_scale_f32_16x16x128_f8f6f4 v[86:89], v[178:185], v[236:243], v[86:89], v246, v247 op_sel_hi:[0,0,0]
	v_mfma_scale_f32_16x16x128_f8f6f4 v[82:85], v[186:193], v[236:243], v[82:85], v246, v247 op_sel_hi:[0,0,0]
	s_setprio 0
	s_setprio 1
	v_mfma_scale_f32_16x16x128_f8f6f4 v[126:129], v[2:9], v[212:219], v[126:129], v246, v247 op_sel_hi:[0,0,0]
	v_mfma_scale_f32_16x16x128_f8f6f4 v[122:125], v[204:211], v[212:219], v[122:125], v246, v247 op_sel_hi:[0,0,0]
	v_mfma_scale_f32_16x16x128_f8f6f4 v[110:113], v[2:9], v[220:227], v[110:113], v246, v247 op_sel_hi:[0,0,0]
	v_mfma_scale_f32_16x16x128_f8f6f4 v[106:109], v[204:211], v[220:227], v[106:109], v246, v247 op_sel_hi:[0,0,0]
	v_mfma_scale_f32_16x16x128_f8f6f4 v[94:97], v[2:9], v[228:235], v[94:97], v246, v247 op_sel_hi:[0,0,0]
	v_mfma_scale_f32_16x16x128_f8f6f4 v[90:93], v[204:211], v[228:235], v[90:93], v246, v247 op_sel_hi:[0,0,0]
	v_mfma_scale_f32_16x16x128_f8f6f4 v[78:81], v[2:9], v[236:243], v[78:81], v246, v247 op_sel_hi:[0,0,0]
	v_mfma_scale_f32_16x16x128_f8f6f4 v[70:73], v[204:211], v[236:243], v[70:73], v246, v247 op_sel_hi:[0,0,0]
	s_setprio 2
	s_barrier
	s_mov_b32 m0, s91
	v_lshl_add_u64 v[156:157], v[156:157], 0, s[92:93]
	ds_read_b128 v[212:215], v174 offset:49152
	ds_read_b128 v[216:219], v174 offset:50176
	ds_read_b128 v[220:223], v174 offset:51200
	ds_read_b128 v[224:227], v174 offset:52224
	ds_read_b128 v[228:231], v174 offset:53248
	ds_read_b128 v[232:235], v174 offset:54272
	ds_read_b128 v[236:239], v174 offset:55296
	ds_read_b128 v[240:243], v174 offset:56320
	global_load_lds_dwordx4 v[156:157], off
	v_lshl_add_u64 v[156:157], v[158:159], 0, s[92:93]
	s_mov_b32 m0, s94
	s_nop 0
	global_load_lds_dwordx4 v[156:157], off
	v_lshl_add_u64 v[156:157], v[160:161], 0, s[92:93]
	s_mov_b32 m0, s95
	s_nop 0
	global_load_lds_dwordx4 v[156:157], off
	v_lshl_add_u64 v[156:157], v[164:165], 0, s[92:93]
	s_mov_b32 m0, s97
	s_nop 0
	global_load_lds_dwordx4 v[156:157], off
	v_lshl_add_u64 v[156:157], v[166:167], 0, s[92:93]
	s_mov_b32 m0, s63
	s_nop 0
	global_load_lds_dwordx4 v[156:157], off
	v_lshl_add_u64 v[156:157], v[168:169], 0, s[92:93]
	s_mov_b32 m0, s65
	s_nop 0
	global_load_lds_dwordx4 v[156:157], off
	s_waitcnt vmcnt(8)
	s_waitcnt lgkmcnt(0)
	s_barrier
	s_setprio 1
	s_waitcnt lgkmcnt(0)
	v_mfma_scale_f32_16x16x128_f8f6f4 v[74:77], v[178:185], v[212:219], v[74:77], v246, v247 op_sel_hi:[0,0,0]
	v_mfma_scale_f32_16x16x128_f8f6f4 v[66:69], v[186:193], v[212:219], v[66:69], v246, v247 op_sel_hi:[0,0,0]
	v_mfma_scale_f32_16x16x128_f8f6f4 v[54:57], v[178:185], v[220:227], v[54:57], v246, v247 op_sel_hi:[0,0,0]
	v_mfma_scale_f32_16x16x128_f8f6f4 v[50:53], v[186:193], v[220:227], v[50:53], v246, v247 op_sel_hi:[0,0,0]
	v_mfma_scale_f32_16x16x128_f8f6f4 v[38:41], v[178:185], v[228:235], v[38:41], v246, v247 op_sel_hi:[0,0,0]
	v_mfma_scale_f32_16x16x128_f8f6f4 v[34:37], v[186:193], v[228:235], v[34:37], v246, v247 op_sel_hi:[0,0,0]
	v_mfma_scale_f32_16x16x128_f8f6f4 v[22:25], v[178:185], v[236:243], v[22:25], v246, v247 op_sel_hi:[0,0,0]
	v_mfma_scale_f32_16x16x128_f8f6f4 v[18:21], v[186:193], v[236:243], v[18:21], v246, v247 op_sel_hi:[0,0,0]
	s_setprio 0
	s_setprio 1
	v_mfma_scale_f32_16x16x128_f8f6f4 v[62:65], v[2:9], v[212:219], v[62:65], v246, v247 op_sel_hi:[0,0,0]
	v_mfma_scale_f32_16x16x128_f8f6f4 v[58:61], v[204:211], v[212:219], v[58:61], v246, v247 op_sel_hi:[0,0,0]
	v_mfma_scale_f32_16x16x128_f8f6f4 v[46:49], v[2:9], v[220:227], v[46:49], v246, v247 op_sel_hi:[0,0,0]
	v_mfma_scale_f32_16x16x128_f8f6f4 v[42:45], v[204:211], v[220:227], v[42:45], v246, v247 op_sel_hi:[0,0,0]
	v_mfma_scale_f32_16x16x128_f8f6f4 v[30:33], v[2:9], v[228:235], v[30:33], v246, v247 op_sel_hi:[0,0,0]
	v_mfma_scale_f32_16x16x128_f8f6f4 v[26:29], v[204:211], v[228:235], v[26:29], v246, v247 op_sel_hi:[0,0,0]
	v_mfma_scale_f32_16x16x128_f8f6f4 v[14:17], v[2:9], v[236:243], v[14:17], v246, v247 op_sel_hi:[0,0,0]
	v_mfma_scale_f32_16x16x128_f8f6f4 v[10:13], v[204:211], v[236:243], v[10:13], v246, v247 op_sel_hi:[0,0,0]
	s_setprio 2
	s_barrier
	s_add_i32 s54, s72, 2
	s_add_u32 s52, s52, 0x100
	s_addc_u32 s53, s53, 0
	v_lshl_add_u64 v[154:155], v[154:155], 0, s[10:11]
	s_cmp_ge_i32 s72, s66
	s_mov_b32 s72, s54
	s_cbranch_scc0 .LBB0_1452

; #define PG8_STAGE(bufoff, gbase, voff) do { _Pragma("unroll") for (int _i = 0; _i < 2; ++_i) \
;         __builtin_amdgcn_global_load_lds((const unsigned*)((const char*)(gbase) + (voff)[_i]), (PG8_LAS unsigned*)(lds + (bufoff) + ldsw + _i * 8192), 16, 0, 0); } while (0)
; #define PG8_WAIT_V(n) asm volatile("s_waitcnt vmcnt(" #n ")" ::: "memory")
; #define PG8_WAIT_L(n) asm volatile("s_waitcnt lgkmcnt(" #n ")" ::: "memory")
; #define PG8_BAR __builtin_amdgcn_s_barrier()
; #define PG8_SCHED __builtin_amdgcn_sched_barrier(0)
; template <class Epi, class Sched, bool ALIGN_EPI = false, bool SP2 = false, bool F8 = false>
; __device__ __forceinline__ void gemm_phase(PG8_LAS unsigned char* lds, const Gemm g, const Sched& S, const Epi& E, const int tidb  ) {
;     ...
;             const bool last = (t == nt - 2);
;             if constexpr (Epi::PREFETCH) { if (t == 0) E.prefetch(cur, wid, lane); }
;             const char* a1 = cA + (size_t)(t + 1) * kstep;
;             const char* a2 = last ? nA : cA + (size_t)(t + 2) * kstep; const char* b2 = last ? nB : cB + (size_t)(t + 2) * kstep;
;             const char* a3 = a2 + kstep; const char* b3 = b2 + kstep;
;             if (last && has_next) S.a_ready(nxt);
;             if constexpr (SP2) {
;             PG8_LDB(B0, 0, 0); PG8_LDB(B1, 0, 1); PG8_SCHED; PG8_LDA(At, 0, 0); PG8_STAGE(PG8_SA(1, 1), a1 + hstep, voffA);
;             PG8_WAIT_V(8); PG8_WAIT_L(0); PG8_BAR; PG8_MMA(0, 0, At, B0); PG8_MMA(0, 1, At, B1); PG8_BAR; PG8_SCHED;
;             PG8_LDA(At, 0, 1); PG8_STAGE(PG8_SB(0, 0), b2, voffB); PG8_STAGE(PG8_SB(0, 1), b2 + hstep, voffB); PG8_STAGE(PG8_SA(0, 0), a2, voffA);
;             PG8_WAIT_V(8); PG8_WAIT_L(0); PG8_BAR; PG8_MMA(1, 0, At, B0); PG8_MMA(1, 1, At, B1); PG8_BAR; PG8_SCHED;
.LBB0_1705:
	s_add_i32 s60, s28, 2
	s_add_u32 s61, s26, 0x80
	s_addc_u32 s29, s27, 0
	s_add_i32 s65, 0, 0x10000
	s_cmp_eq_u32 s51, s28
	s_cselect_b32 s29, s5, s29
	s_cselect_b32 s28, s4, s61
	v_add_u32_e32 v148, s65, v151
	s_cselect_b32 s63, s25, s59
	s_cselect_b32 s62, s24, s58
	s_add_i32 s61, 0, 0x14000
	ds_read_b128 v[140:143], v148
	ds_read_b128 v[144:147], v148 offset:1024
	ds_read_b128 v[158:161], v148 offset:2048
	ds_read_b128 v[164:167], v148 offset:3072
	v_add_u32_e32 v148, s61, v151
	ds_read_b128 v[168:171], v148
	ds_read_b128 v[172:175], v148 offset:1024
	ds_read_b128 v[176:179], v148 offset:2048
	ds_read_b128 v[180:183], v148 offset:3072
	v_lshl_add_u64 v[148:149], s[26:27], 0, v[136:137]
	s_add_i32 m0, s41, 0xc000
	ds_read_b128 v[184:187], v156
	ds_read_b128 v[188:191], v156 offset:1024
	ds_read_b128 v[192:195], v156 offset:2048
	ds_read_b128 v[204:207], v156 offset:3072
	ds_read_b128 v[208:211], v156 offset:4096
	ds_read_b128 v[212:215], v156 offset:5120
	ds_read_b128 v[216:219], v156 offset:6144
	ds_read_b128 v[220:223], v156 offset:7168
	global_load_lds_dwordx4 v[148:149], off
	v_lshl_add_u64 v[148:149], s[26:27], 0, v[138:139]
	s_add_i32 m0, s41, 0xe000
	s_nop 0
	global_load_lds_dwordx4 v[148:149], off
	s_waitcnt vmcnt(8)
	s_waitcnt lgkmcnt(0)
	s_barrier
	s_setprio 1
	s_waitcnt lgkmcnt(0)
	v_mfma_f32_16x16x32_bf16 v[122:125], v[140:143], v[184:187], v[122:125]
	v_mfma_f32_16x16x32_bf16 v[118:121], v[158:161], v[184:187], v[118:121]
	v_mfma_f32_16x16x32_bf16 v[110:113], v[140:143], v[192:195], v[110:113]
	v_mfma_f32_16x16x32_bf16 v[102:105], v[158:161], v[192:195], v[102:105]
	v_mfma_f32_16x16x32_bf16 v[94:97], v[140:143], v[208:211], v[94:97]
	v_mfma_f32_16x16x32_bf16 v[86:89], v[158:161], v[208:211], v[86:89]
	v_mfma_f32_16x16x32_bf16 v[78:81], v[140:143], v[216:219], v[78:81]
	v_mfma_f32_16x16x32_bf16 v[70:73], v[158:161], v[216:219], v[70:73]
	v_mfma_f32_16x16x32_bf16 v[122:125], v[144:147], v[188:191], v[122:125]
	v_mfma_f32_16x16x32_bf16 v[118:121], v[164:167], v[188:191], v[118:121]
	v_mfma_f32_16x16x32_bf16 v[110:113], v[144:147], v[204:207], v[110:113]
	v_mfma_f32_16x16x32_bf16 v[102:105], v[164:167], v[204:207], v[102:105]
	v_mfma_f32_16x16x32_bf16 v[94:97], v[144:147], v[212:215], v[94:97]
	v_mfma_f32_16x16x32_bf16 v[86:89], v[164:167], v[212:215], v[86:89]
	v_mfma_f32_16x16x32_bf16 v[78:81], v[144:147], v[220:223], v[78:81]
	v_mfma_f32_16x16x32_bf16 v[70:73], v[164:167], v[220:223], v[70:73]
	s_setprio 0
	s_setprio 1
	v_mfma_f32_16x16x32_bf16 v[126:129], v[168:171], v[184:187], v[126:129]
	v_mfma_f32_16x16x32_bf16 v[114:117], v[176:179], v[184:187], v[114:117]
	v_mfma_f32_16x16x32_bf16 v[106:109], v[168:171], v[192:195], v[106:109]
	v_mfma_f32_16x16x32_bf16 v[98:101], v[176:179], v[192:195], v[98:101]
	v_mfma_f32_16x16x32_bf16 v[90:93], v[168:171], v[208:211], v[90:93]
	v_mfma_f32_16x16x32_bf16 v[82:85], v[176:179], v[208:211], v[82:85]
	v_mfma_f32_16x16x32_bf16 v[74:77], v[168:171], v[216:219], v[74:77]
	v_mfma_f32_16x16x32_bf16 v[66:69], v[176:179], v[216:219], v[66:69]
	v_mfma_f32_16x16x32_bf16 v[126:129], v[172:175], v[188:191], v[126:129]
	v_mfma_f32_16x16x32_bf16 v[114:117], v[180:183], v[188:191], v[114:117]
	v_mfma_f32_16x16x32_bf16 v[106:109], v[172:175], v[204:207], v[106:109]
	v_mfma_f32_16x16x32_bf16 v[98:101], v[180:183], v[204:207], v[98:101]
	v_mfma_f32_16x16x32_bf16 v[90:93], v[172:175], v[212:215], v[90:93]
	v_mfma_f32_16x16x32_bf16 v[82:85], v[180:183], v[212:215], v[82:85]
	v_mfma_f32_16x16x32_bf16 v[74:77], v[172:175], v[220:223], v[74:77]
	v_mfma_f32_16x16x32_bf16 v[66:69], v[180:183], v[220:223], v[66:69]
	s_setprio 2
	s_barrier
	s_add_i32 s65, s65, s0
	v_lshl_add_u64 v[148:149], s[62:63], 0, v[0:1]
	s_mov_b32 m0, s65
	ds_read_b128 v[184:187], v156 offset:16384
	ds_read_b128 v[188:191], v156 offset:17408
	ds_read_b128 v[192:195], v156 offset:18432
	ds_read_b128 v[204:207], v156 offset:19456
	ds_read_b128 v[208:211], v156 offset:20480
	ds_read_b128 v[212:215], v156 offset:21504
	ds_read_b128 v[216:219], v156 offset:22528
	ds_read_b128 v[220:223], v156 offset:23552
	global_load_lds_dwordx4 v[148:149], off
	s_add_i32 m0, s65, 0x2000
	v_lshl_add_u64 v[196:197], s[62:63], 0, v[130:131]
	s_add_u32 s62, s62, s6
	s_addc_u32 s63, s63, s7
	s_add_i32 s61, s61, s0
	global_load_lds_dwordx4 v[196:197], off
	v_lshl_add_u64 v[198:199], s[62:63], 0, v[0:1]
	s_mov_b32 m0, s61
	v_lshl_add_u64 v[200:201], s[62:63], 0, v[130:131]
	global_load_lds_dwordx4 v[198:199], off
	s_add_i32 m0, s61, 0x2000
	v_lshl_add_u64 v[224:225], s[28:29], 0, v[134:135]
	global_load_lds_dwordx4 v[200:201], off
	s_mov_b32 m0, s41
	v_lshl_add_u64 v[226:227], s[28:29], 0, v[132:133]
	global_load_lds_dwordx4 v[224:225], off
	s_mov_b32 m0, s43
	s_nop 0
	global_load_lds_dwordx4 v[226:227], off
	s_waitcnt vmcnt(8)
	s_waitcnt lgkmcnt(0)
	s_barrier
; #define PG8_STAGE(bufoff, gbase, voff) do { _Pragma("unroll") for (int _i = 0; _i < 2; ++_i) \
;         __builtin_amdgcn_global_load_lds((const unsigned*)((const char*)(gbase) + (voff)[_i]), (PG8_LAS unsigned*)(lds + (bufoff) + ldsw + _i * 8192), 16, 0, 0); } while (0)
; #define PG8_WAIT_V(n) asm volatile("s_waitcnt vmcnt(" #n ")" ::: "memory")
; #define PG8_WAIT_L(n) asm volatile("s_waitcnt lgkmcnt(" #n ")" ::: "memory")
; #define PG8_BAR __builtin_amdgcn_s_barrier()
; #define PG8_SCHED __builtin_amdgcn_sched_barrier(0)
; template <class Epi, class Sched, bool ALIGN_EPI = false, bool SP2 = false, bool F8 = false>
; __device__ __forceinline__ void gemm_phase(PG8_LAS unsigned char* lds, const Gemm g, const Sched& S, const Epi& E, const int tidb  ) {
;     ...
;             PG8_WAIT_V(8); PG8_WAIT_L(0); PG8_BAR; PG8_MMA(1, 0, At, B0); PG8_MMA(1, 1, At, B1); PG8_BAR; PG8_SCHED;
;             PG8_LDB(B0, 1, 0); PG8_LDB(B1, 1, 1); PG8_SCHED; PG8_LDA(At, 1, 0); PG8_STAGE(PG8_SA(0, 1), a2 + hstep, voffA);
;             PG8_WAIT_V(8); PG8_WAIT_L(0); PG8_BAR; PG8_MMA(0, 0, At, B0); PG8_MMA(0, 1, At, B1); PG8_BAR; PG8_SCHED;
	s_setprio 1
	s_waitcnt lgkmcnt(0)
	v_mfma_f32_16x16x32_bf16 v[62:65], v[140:143], v[184:187], v[62:65]
	v_mfma_f32_16x16x32_bf16 v[54:57], v[158:161], v[184:187], v[54:57]
	v_mfma_f32_16x16x32_bf16 v[46:49], v[140:143], v[192:195], v[46:49]
	v_mfma_f32_16x16x32_bf16 v[38:41], v[158:161], v[192:195], v[38:41]
	v_mfma_f32_16x16x32_bf16 v[30:33], v[140:143], v[208:211], v[30:33]
	v_mfma_f32_16x16x32_bf16 v[22:25], v[158:161], v[208:211], v[22:25]
	v_mfma_f32_16x16x32_bf16 v[14:17], v[140:143], v[216:219], v[14:17]
	v_mfma_f32_16x16x32_bf16 v[6:9], v[158:161], v[216:219], v[6:9]
	v_mfma_f32_16x16x32_bf16 v[62:65], v[144:147], v[188:191], v[62:65]
	v_mfma_f32_16x16x32_bf16 v[54:57], v[164:167], v[188:191], v[54:57]
	v_mfma_f32_16x16x32_bf16 v[46:49], v[144:147], v[204:207], v[46:49]
	v_mfma_f32_16x16x32_bf16 v[38:41], v[164:167], v[204:207], v[38:41]
	v_mfma_f32_16x16x32_bf16 v[30:33], v[144:147], v[212:215], v[30:33]
	v_mfma_f32_16x16x32_bf16 v[22:25], v[164:167], v[212:215], v[22:25]
	v_mfma_f32_16x16x32_bf16 v[14:17], v[144:147], v[220:223], v[14:17]
	v_mfma_f32_16x16x32_bf16 v[6:9], v[164:167], v[220:223], v[6:9]
	s_setprio 0
	s_setprio 1
	v_mfma_f32_16x16x32_bf16 v[58:61], v[168:171], v[184:187], v[58:61]
	v_mfma_f32_16x16x32_bf16 v[50:53], v[176:179], v[184:187], v[50:53]
	v_mfma_f32_16x16x32_bf16 v[42:45], v[168:171], v[192:195], v[42:45]
	v_mfma_f32_16x16x32_bf16 v[34:37], v[176:179], v[192:195], v[34:37]
	v_mfma_f32_16x16x32_bf16 v[26:29], v[168:171], v[208:211], v[26:29]
	v_mfma_f32_16x16x32_bf16 v[18:21], v[176:179], v[208:211], v[18:21]
	v_mfma_f32_16x16x32_bf16 v[10:13], v[168:171], v[216:219], v[10:13]
	v_mfma_f32_16x16x32_bf16 v[2:5], v[176:179], v[216:219], v[2:5]
	v_mfma_f32_16x16x32_bf16 v[58:61], v[172:175], v[188:191], v[58:61]
	v_mfma_f32_16x16x32_bf16 v[50:53], v[180:183], v[188:191], v[50:53]
	v_mfma_f32_16x16x32_bf16 v[42:45], v[172:175], v[204:207], v[42:45]
	v_mfma_f32_16x16x32_bf16 v[34:37], v[180:183], v[204:207], v[34:37]
	v_mfma_f32_16x16x32_bf16 v[26:29], v[172:175], v[212:215], v[26:29]
	v_mfma_f32_16x16x32_bf16 v[18:21], v[180:183], v[212:215], v[18:21]
	v_mfma_f32_16x16x32_bf16 v[10:13], v[172:175], v[220:223], v[10:13]
	v_mfma_f32_16x16x32_bf16 v[2:5], v[180:183], v[220:223], v[2:5]
	s_setprio 2
	s_barrier
	s_add_i32 s61, 0, 0x18000
	v_add_u32_e32 v157, s61, v151
	s_add_i32 s62, 0, 0x1c000
	ds_read_b128 v[140:143], v157
	ds_read_b128 v[144:147], v157 offset:1024
	ds_read_b128 v[158:161], v157 offset:2048
	ds_read_b128 v[164:167], v157 offset:3072
	v_add_u32_e32 v157, s62, v151
	ds_read_b128 v[168:171], v157
	ds_read_b128 v[172:175], v157 offset:1024
	ds_read_b128 v[176:179], v157 offset:2048
	ds_read_b128 v[180:183], v157 offset:3072
	s_add_u32 s28, s28, s6
	s_addc_u32 s29, s29, s7
	s_mov_b32 m0, s45
	v_lshl_add_u64 v[228:229], s[28:29], 0, v[134:135]
	ds_read_b128 v[184:187], v156 offset:32768
	ds_read_b128 v[188:191], v156 offset:33792
	ds_read_b128 v[192:195], v156 offset:34816
	ds_read_b128 v[204:207], v156 offset:35840
	ds_read_b128 v[208:211], v156 offset:36864
	ds_read_b128 v[212:215], v156 offset:37888
	ds_read_b128 v[216:219], v156 offset:38912
	ds_read_b128 v[220:223], v156 offset:39936
	global_load_lds_dwordx4 v[228:229], off
	v_lshl_add_u64 v[228:229], s[28:29], 0, v[132:133]
	s_mov_b32 m0, s46
	s_nop 0
	global_load_lds_dwordx4 v[228:229], off
	s_waitcnt vmcnt(8)
	s_waitcnt lgkmcnt(0)
	s_barrier
	s_setprio 1
	s_waitcnt lgkmcnt(0)
	v_mfma_f32_16x16x32_bf16 v[122:125], v[140:143], v[184:187], v[122:125]
	v_mfma_f32_16x16x32_bf16 v[118:121], v[158:161], v[184:187], v[118:121]
	v_mfma_f32_16x16x32_bf16 v[110:113], v[140:143], v[192:195], v[110:113]
	v_mfma_f32_16x16x32_bf16 v[102:105], v[158:161], v[192:195], v[102:105]
	v_mfma_f32_16x16x32_bf16 v[94:97], v[140:143], v[208:211], v[94:97]
	v_mfma_f32_16x16x32_bf16 v[86:89], v[158:161], v[208:211], v[86:89]
	v_mfma_f32_16x16x32_bf16 v[78:81], v[140:143], v[216:219], v[78:81]
	v_mfma_f32_16x16x32_bf16 v[70:73], v[158:161], v[216:219], v[70:73]
	v_mfma_f32_16x16x32_bf16 v[122:125], v[144:147], v[188:191], v[122:125]
	v_mfma_f32_16x16x32_bf16 v[118:121], v[164:167], v[188:191], v[118:121]
	v_mfma_f32_16x16x32_bf16 v[110:113], v[144:147], v[204:207], v[110:113]
	v_mfma_f32_16x16x32_bf16 v[102:105], v[164:167], v[204:207], v[102:105]
	v_mfma_f32_16x16x32_bf16 v[94:97], v[144:147], v[212:215], v[94:97]
	v_mfma_f32_16x16x32_bf16 v[86:89], v[164:167], v[212:215], v[86:89]
	v_mfma_f32_16x16x32_bf16 v[78:81], v[144:147], v[220:223], v[78:81]
	v_mfma_f32_16x16x32_bf16 v[70:73], v[164:167], v[220:223], v[70:73]
	s_setprio 0
	s_setprio 1
	v_mfma_f32_16x16x32_bf16 v[126:129], v[168:171], v[184:187], v[126:129]
	v_mfma_f32_16x16x32_bf16 v[114:117], v[176:179], v[184:187], v[114:117]
	v_mfma_f32_16x16x32_bf16 v[106:109], v[168:171], v[192:195], v[106:109]
	v_mfma_f32_16x16x32_bf16 v[98:101], v[176:179], v[192:195], v[98:101]
	v_mfma_f32_16x16x32_bf16 v[90:93], v[168:171], v[208:211], v[90:93]
	v_mfma_f32_16x16x32_bf16 v[82:85], v[176:179], v[208:211], v[82:85]
	v_mfma_f32_16x16x32_bf16 v[74:77], v[168:171], v[216:219], v[74:77]
	v_mfma_f32_16x16x32_bf16 v[66:69], v[176:179], v[216:219], v[66:69]
	v_mfma_f32_16x16x32_bf16 v[126:129], v[172:175], v[188:191], v[126:129]
	v_mfma_f32_16x16x32_bf16 v[114:117], v[180:183], v[188:191], v[114:117]
	v_mfma_f32_16x16x32_bf16 v[106:109], v[172:175], v[204:207], v[106:109]
	v_mfma_f32_16x16x32_bf16 v[98:101], v[180:183], v[204:207], v[98:101]
	v_mfma_f32_16x16x32_bf16 v[90:93], v[172:175], v[212:215], v[90:93]
	v_mfma_f32_16x16x32_bf16 v[82:85], v[180:183], v[212:215], v[82:85]
	v_mfma_f32_16x16x32_bf16 v[74:77], v[172:175], v[220:223], v[74:77]
	v_mfma_f32_16x16x32_bf16 v[66:69], v[180:183], v[220:223], v[66:69]
	s_setprio 2
	s_barrier
; #define PG8_STAGE(bufoff, gbase, voff) do { _Pragma("unroll") for (int _i = 0; _i < 2; ++_i) \
;         __builtin_amdgcn_global_load_lds((const unsigned*)((const char*)(gbase) + (voff)[_i]), (PG8_LAS unsigned*)(lds + (bufoff) + ldsw + _i * 8192), 16, 0, 0); } while (0)
; #define PG8_WAIT_V(n) asm volatile("s_waitcnt vmcnt(" #n ")" ::: "memory")
; #define PG8_WAIT_L(n) asm volatile("s_waitcnt lgkmcnt(" #n ")" ::: "memory")
; #define PG8_BAR __builtin_amdgcn_s_barrier()
; #define PG8_SCHED __builtin_amdgcn_sched_barrier(0)
; template <class Epi, class Sched, bool ALIGN_EPI = false, bool SP2 = false, bool F8 = false>
; __device__ __forceinline__ void gemm_phase(PG8_LAS unsigned char* lds, const Gemm g, const Sched& S, const Epi& E, const int tidb  ) {
;     ...
;             PG8_LDA(At, 1, 1); PG8_STAGE(PG8_SB(1, 0), b3, voffB); PG8_STAGE(PG8_SB(1, 1), b3 + hstep, voffB); PG8_STAGE(PG8_SA(1, 0), a3, voffA);
;             PG8_WAIT_V(8); PG8_WAIT_L(0); PG8_BAR; PG8_MMA(1, 0, At, B0); PG8_MMA(1, 1, At, B1); PG8_BAR; PG8_SCHED;
	s_add_i32 s28, s61, s0
	v_lshl_add_u64 v[148:149], v[148:149], 0, s[92:93]
	s_mov_b32 m0, s28
	ds_read_b128 v[184:187], v156 offset:49152
	ds_read_b128 v[188:191], v156 offset:50176
	ds_read_b128 v[192:195], v156 offset:51200
	ds_read_b128 v[204:207], v156 offset:52224
	ds_read_b128 v[208:211], v156 offset:53248
	ds_read_b128 v[212:215], v156 offset:54272
	ds_read_b128 v[216:219], v156 offset:55296
	ds_read_b128 v[220:223], v156 offset:56320
	global_load_lds_dwordx4 v[148:149], off
	v_lshl_add_u64 v[148:149], v[196:197], 0, s[92:93]
	s_add_i32 m0, s28, 0x2000
	s_add_i32 s28, s62, s0
	global_load_lds_dwordx4 v[148:149], off
	v_lshl_add_u64 v[148:149], v[198:199], 0, s[92:93]
	s_mov_b32 m0, s28
	s_nop 0
	global_load_lds_dwordx4 v[148:149], off
	v_lshl_add_u64 v[148:149], v[200:201], 0, s[92:93]
	s_add_i32 m0, s28, 0x2000
	s_nop 0
	global_load_lds_dwordx4 v[148:149], off
	v_lshl_add_u64 v[148:149], v[224:225], 0, s[92:93]
	s_mov_b32 m0, s47
	s_nop 0
	global_load_lds_dwordx4 v[148:149], off
	v_lshl_add_u64 v[148:149], v[226:227], 0, s[92:93]
	s_mov_b32 m0, s48
	s_nop 0
	global_load_lds_dwordx4 v[148:149], off
	s_waitcnt vmcnt(8)
	s_waitcnt lgkmcnt(0)
	s_barrier
	s_setprio 1
	s_waitcnt lgkmcnt(0)
	v_mfma_f32_16x16x32_bf16 v[62:65], v[140:143], v[184:187], v[62:65]
	v_mfma_f32_16x16x32_bf16 v[54:57], v[158:161], v[184:187], v[54:57]
	v_mfma_f32_16x16x32_bf16 v[46:49], v[140:143], v[192:195], v[46:49]
	v_mfma_f32_16x16x32_bf16 v[38:41], v[158:161], v[192:195], v[38:41]
	v_mfma_f32_16x16x32_bf16 v[30:33], v[140:143], v[208:211], v[30:33]
	v_mfma_f32_16x16x32_bf16 v[22:25], v[158:161], v[208:211], v[22:25]
	v_mfma_f32_16x16x32_bf16 v[14:17], v[140:143], v[216:219], v[14:17]
	v_mfma_f32_16x16x32_bf16 v[6:9], v[158:161], v[216:219], v[6:9]
	v_mfma_f32_16x16x32_bf16 v[62:65], v[144:147], v[188:191], v[62:65]
	v_mfma_f32_16x16x32_bf16 v[54:57], v[164:167], v[188:191], v[54:57]
	v_mfma_f32_16x16x32_bf16 v[46:49], v[144:147], v[204:207], v[46:49]
	v_mfma_f32_16x16x32_bf16 v[38:41], v[164:167], v[204:207], v[38:41]
	v_mfma_f32_16x16x32_bf16 v[30:33], v[144:147], v[212:215], v[30:33]
	v_mfma_f32_16x16x32_bf16 v[22:25], v[164:167], v[212:215], v[22:25]
	v_mfma_f32_16x16x32_bf16 v[14:17], v[144:147], v[220:223], v[14:17]
	v_mfma_f32_16x16x32_bf16 v[6:9], v[164:167], v[220:223], v[6:9]
	s_setprio 0
	s_setprio 1
	v_mfma_f32_16x16x32_bf16 v[58:61], v[168:171], v[184:187], v[58:61]
	v_mfma_f32_16x16x32_bf16 v[50:53], v[176:179], v[184:187], v[50:53]
	v_mfma_f32_16x16x32_bf16 v[42:45], v[168:171], v[192:195], v[42:45]
	v_mfma_f32_16x16x32_bf16 v[34:37], v[176:179], v[192:195], v[34:37]
	v_mfma_f32_16x16x32_bf16 v[26:29], v[168:171], v[208:211], v[26:29]
	v_mfma_f32_16x16x32_bf16 v[18:21], v[176:179], v[208:211], v[18:21]
	v_mfma_f32_16x16x32_bf16 v[10:13], v[168:171], v[216:219], v[10:13]
	v_mfma_f32_16x16x32_bf16 v[2:5], v[176:179], v[216:219], v[2:5]
	v_mfma_f32_16x16x32_bf16 v[58:61], v[172:175], v[188:191], v[58:61]
	v_mfma_f32_16x16x32_bf16 v[50:53], v[180:183], v[188:191], v[50:53]
	v_mfma_f32_16x16x32_bf16 v[42:45], v[172:175], v[204:207], v[42:45]
	v_mfma_f32_16x16x32_bf16 v[34:37], v[180:183], v[204:207], v[34:37]
	v_mfma_f32_16x16x32_bf16 v[26:29], v[172:175], v[212:215], v[26:29]
	v_mfma_f32_16x16x32_bf16 v[18:21], v[180:183], v[212:215], v[18:21]
	v_mfma_f32_16x16x32_bf16 v[10:13], v[172:175], v[220:223], v[10:13]
	v_mfma_f32_16x16x32_bf16 v[2:5], v[180:183], v[220:223], v[2:5]
	s_setprio 2
	s_barrier
	s_add_u32 s26, s26, 0x100
	s_addc_u32 s27, s27, 0
	s_add_u32 s58, s58, 0x100
	s_addc_u32 s59, s59, 0
	s_cmp_ge_i32 s60, s49
	s_mov_b32 s28, s60
	s_cbranch_scc0 .LBB0_1705

; #define PG8_STAGE(bufoff, gbase, voff) do { _Pragma("unroll") for (int _i = 0; _i < 2; ++_i) \
;         __builtin_amdgcn_global_load_lds((const unsigned*)((const char*)(gbase) + (voff)[_i]), (PG8_LAS unsigned*)(lds + (bufoff) + ldsw + _i * 8192), 16, 0, 0); } while (0)
; #define PG8_WAIT_V(n) asm volatile("s_waitcnt vmcnt(" #n ")" ::: "memory")
; #define PG8_WAIT_L(n) asm volatile("s_waitcnt lgkmcnt(" #n ")" ::: "memory")
; #define PG8_BAR __builtin_amdgcn_s_barrier()
; #define PG8_SCHED __builtin_amdgcn_sched_barrier(0)
; template <class Epi, class Sched, bool ALIGN_EPI = false, bool SP2 = false, bool F8 = false>
; __device__ __forceinline__ void gemm_phase(PG8_LAS unsigned char* lds, const Gemm g, const Sched& S, const Epi& E, const int tidb  ) {
;     ...
;             const bool last = (t == nt - 2);
;             if constexpr (Epi::PREFETCH) { if (t == 0) E.prefetch(cur, wid, lane); }
;             const char* a1 = cA + (size_t)(t + 1) * kstep;
;             const char* a2 = last ? nA : cA + (size_t)(t + 2) * kstep; const char* b2 = last ? nB : cB + (size_t)(t + 2) * kstep;
;             const char* a3 = a2 + kstep; const char* b3 = b2 + kstep;
;             if (last && has_next) S.a_ready(nxt);
;             if constexpr (SP2) {
;             PG8_LDB(B0, 0, 0); PG8_LDB(B1, 0, 1); PG8_SCHED; PG8_LDA(At, 0, 0); PG8_STAGE(PG8_SA(1, 1), a1 + hstep, voffA);
;             PG8_WAIT_V(8); PG8_WAIT_L(0); PG8_BAR; PG8_MMA(0, 0, At, B0); PG8_MMA(0, 1, At, B1); PG8_BAR; PG8_SCHED;
;             PG8_LDA(At, 0, 1); PG8_STAGE(PG8_SB(0, 0), b2, voffB); PG8_STAGE(PG8_SB(0, 1), b2 + hstep, voffB); PG8_STAGE(PG8_SA(0, 0), a2, voffA);
;             PG8_WAIT_V(8); PG8_WAIT_L(0); PG8_BAR; PG8_MMA(1, 0, At, B0); PG8_MMA(1, 1, At, B1); PG8_BAR; PG8_SCHED;
.LBB0_1728:
	s_add_i32 s60, s26, 2
	s_add_u32 s28, s24, 0x80
	s_addc_u32 s27, s25, 0
	s_add_i32 s61, 0, 0x10000
	s_cmp_eq_u32 s51, s26
	s_cselect_b32 s27, s5, s27
	s_cselect_b32 s26, s4, s28
	s_cselect_b32 s29, s23, s59
	s_cselect_b32 s28, s22, s58
	s_add_i32 s62, 0, 0x14000
	v_add_u32_e32 v2, s61, v186
	v_add_u32_e32 v14, s62, v186
	ds_read_b128 v[18:21], v2
	ds_read_b128 v[22:25], v2 offset:1024
	ds_read_b128 v[26:29], v2 offset:2048
	ds_read_b128 v[30:33], v2 offset:3072
	ds_read_b128 v[2:5], v14
	ds_read_b128 v[6:9], v14 offset:1024
	ds_read_b128 v[10:13], v14 offset:2048
	ds_read_b128 v[14:17], v14 offset:3072
	v_lshl_add_u64 v[182:183], s[24:25], 0, v[170:171]
	s_add_i32 m0, s41, 0xc000
	ds_read_b128 v[174:177], v191
	ds_read_b128 v[178:181], v191 offset:1024
	ds_read_b128 v[204:207], v191 offset:2048
	ds_read_b128 v[208:211], v191 offset:3072
	ds_read_b128 v[212:215], v191 offset:4096
	ds_read_b128 v[216:219], v191 offset:5120
	ds_read_b128 v[220:223], v191 offset:6144
	ds_read_b128 v[224:227], v191 offset:7168
	global_load_lds_dwordx4 v[182:183], off
	v_lshl_add_u64 v[182:183], s[24:25], 0, v[172:173]
	s_add_i32 m0, s41, 0xe000
	s_nop 0
	global_load_lds_dwordx4 v[182:183], off
	s_waitcnt vmcnt(8)
	s_waitcnt lgkmcnt(0)
	s_barrier
	s_setprio 1
	s_waitcnt lgkmcnt(0)
	v_mfma_scale_f32_16x16x128_f8f6f4 v[154:157], v[18:25], v[174:181], v[154:157], v246, v247 op_sel_hi:[0,0,0]
	v_mfma_scale_f32_16x16x128_f8f6f4 v[150:153], v[26:33], v[174:181], v[150:153], v246, v247 op_sel_hi:[0,0,0]
	v_mfma_scale_f32_16x16x128_f8f6f4 v[142:145], v[18:25], v[204:211], v[142:145], v246, v247 op_sel_hi:[0,0,0]
	v_mfma_scale_f32_16x16x128_f8f6f4 v[134:137], v[26:33], v[204:211], v[134:137], v246, v247 op_sel_hi:[0,0,0]
	v_mfma_scale_f32_16x16x128_f8f6f4 v[126:129], v[18:25], v[212:219], v[126:129], v246, v247 op_sel_hi:[0,0,0]
	v_mfma_scale_f32_16x16x128_f8f6f4 v[118:121], v[26:33], v[212:219], v[118:121], v246, v247 op_sel_hi:[0,0,0]
	v_mfma_scale_f32_16x16x128_f8f6f4 v[110:113], v[18:25], v[220:227], v[110:113], v246, v247 op_sel_hi:[0,0,0]
	v_mfma_scale_f32_16x16x128_f8f6f4 v[102:105], v[26:33], v[220:227], v[102:105], v246, v247 op_sel_hi:[0,0,0]
	s_setprio 0
	s_setprio 1
	v_mfma_scale_f32_16x16x128_f8f6f4 v[158:161], v[2:9], v[174:181], v[158:161], v246, v247 op_sel_hi:[0,0,0]
	v_mfma_scale_f32_16x16x128_f8f6f4 v[146:149], v[10:17], v[174:181], v[146:149], v246, v247 op_sel_hi:[0,0,0]
	v_mfma_scale_f32_16x16x128_f8f6f4 v[138:141], v[2:9], v[204:211], v[138:141], v246, v247 op_sel_hi:[0,0,0]
	v_mfma_scale_f32_16x16x128_f8f6f4 v[130:133], v[10:17], v[204:211], v[130:133], v246, v247 op_sel_hi:[0,0,0]
	v_mfma_scale_f32_16x16x128_f8f6f4 v[122:125], v[2:9], v[212:219], v[122:125], v246, v247 op_sel_hi:[0,0,0]
	v_mfma_scale_f32_16x16x128_f8f6f4 v[114:117], v[10:17], v[212:219], v[114:117], v246, v247 op_sel_hi:[0,0,0]
	v_mfma_scale_f32_16x16x128_f8f6f4 v[106:109], v[2:9], v[220:227], v[106:109], v246, v247 op_sel_hi:[0,0,0]
	v_mfma_scale_f32_16x16x128_f8f6f4 v[98:101], v[10:17], v[220:227], v[98:101], v246, v247 op_sel_hi:[0,0,0]
	s_setprio 2
	s_barrier
	s_add_i32 s61, s61, s36
	v_lshl_add_u64 v[174:175], s[28:29], 0, v[0:1]
	s_mov_b32 m0, s61
	ds_read_b128 v[204:207], v191 offset:16384
	ds_read_b128 v[208:211], v191 offset:17408
	ds_read_b128 v[212:215], v191 offset:18432
	ds_read_b128 v[216:219], v191 offset:19456
	ds_read_b128 v[220:223], v191 offset:20480
	ds_read_b128 v[224:227], v191 offset:21504
	ds_read_b128 v[228:231], v191 offset:22528
	ds_read_b128 v[232:235], v191 offset:23552
	global_load_lds_dwordx4 v[174:175], off
	s_add_i32 m0, s61, 0x2000
	v_lshl_add_u64 v[176:177], s[28:29], 0, v[164:165]
	s_add_u32 s28, s28, s6
	s_addc_u32 s29, s29, s7
	s_add_i32 s61, s62, s36
	global_load_lds_dwordx4 v[176:177], off
	v_lshl_add_u64 v[178:179], s[28:29], 0, v[0:1]
	s_mov_b32 m0, s61
	v_lshl_add_u64 v[180:181], s[28:29], 0, v[164:165]
	global_load_lds_dwordx4 v[178:179], off
	s_add_i32 m0, s61, 0x2000
	v_lshl_add_u64 v[182:183], s[26:27], 0, v[168:169]
	global_load_lds_dwordx4 v[180:181], off
	s_mov_b32 m0, s41
	v_lshl_add_u64 v[184:185], s[26:27], 0, v[166:167]
	global_load_lds_dwordx4 v[182:183], off
	s_mov_b32 m0, s43
	s_nop 0
	global_load_lds_dwordx4 v[184:185], off
	s_waitcnt vmcnt(8)
	s_waitcnt lgkmcnt(0)
	s_barrier
	s_setprio 1
	s_waitcnt lgkmcnt(0)
	v_mfma_scale_f32_16x16x128_f8f6f4 v[94:97], v[18:25], v[204:211], v[94:97], v246, v247 op_sel_hi:[0,0,0]
	v_mfma_scale_f32_16x16x128_f8f6f4 v[86:89], v[26:33], v[204:211], v[86:89], v246, v247 op_sel_hi:[0,0,0]
	v_mfma_scale_f32_16x16x128_f8f6f4 v[78:81], v[18:25], v[212:219], v[78:81], v246, v247 op_sel_hi:[0,0,0]
	v_mfma_scale_f32_16x16x128_f8f6f4 v[70:73], v[26:33], v[212:219], v[70:73], v246, v247 op_sel_hi:[0,0,0]
	v_mfma_scale_f32_16x16x128_f8f6f4 v[62:65], v[18:25], v[220:227], v[62:65], v246, v247 op_sel_hi:[0,0,0]
	v_mfma_scale_f32_16x16x128_f8f6f4 v[54:57], v[26:33], v[220:227], v[54:57], v246, v247 op_sel_hi:[0,0,0]
	v_mfma_scale_f32_16x16x128_f8f6f4 v[46:49], v[18:25], v[228:235], v[46:49], v246, v247 op_sel_hi:[0,0,0]
	v_mfma_scale_f32_16x16x128_f8f6f4 v[38:41], v[26:33], v[228:235], v[38:41], v246, v247 op_sel_hi:[0,0,0]
	s_setprio 0
	s_setprio 1
	v_mfma_scale_f32_16x16x128_f8f6f4 v[90:93], v[2:9], v[204:211], v[90:93], v246, v247 op_sel_hi:[0,0,0]
	v_mfma_scale_f32_16x16x128_f8f6f4 v[82:85], v[10:17], v[204:211], v[82:85], v246, v247 op_sel_hi:[0,0,0]
	v_mfma_scale_f32_16x16x128_f8f6f4 v[74:77], v[2:9], v[212:219], v[74:77], v246, v247 op_sel_hi:[0,0,0]
	v_mfma_scale_f32_16x16x128_f8f6f4 v[66:69], v[10:17], v[212:219], v[66:69], v246, v247 op_sel_hi:[0,0,0]
	v_mfma_scale_f32_16x16x128_f8f6f4 v[58:61], v[2:9], v[220:227], v[58:61], v246, v247 op_sel_hi:[0,0,0]
	v_mfma_scale_f32_16x16x128_f8f6f4 v[50:53], v[10:17], v[220:227], v[50:53], v246, v247 op_sel_hi:[0,0,0]
	v_mfma_scale_f32_16x16x128_f8f6f4 v[42:45], v[2:9], v[228:235], v[42:45], v246, v247 op_sel_hi:[0,0,0]
	v_mfma_scale_f32_16x16x128_f8f6f4 v[34:37], v[10:17], v[228:235], v[34:37], v246, v247 op_sel_hi:[0,0,0]
	s_setprio 2
	s_barrier
; #define PG8_STAGE(bufoff, gbase, voff) do { _Pragma("unroll") for (int _i = 0; _i < 2; ++_i) \
;         __builtin_amdgcn_global_load_lds((const unsigned*)((const char*)(gbase) + (voff)[_i]), (PG8_LAS unsigned*)(lds + (bufoff) + ldsw + _i * 8192), 16, 0, 0); } while (0)
; #define PG8_WAIT_V(n) asm volatile("s_waitcnt vmcnt(" #n ")" ::: "memory")
; #define PG8_WAIT_L(n) asm volatile("s_waitcnt lgkmcnt(" #n ")" ::: "memory")
; #define PG8_BAR __builtin_amdgcn_s_barrier()
; #define PG8_SCHED __builtin_amdgcn_sched_barrier(0)
; template <class Epi, class Sched, bool ALIGN_EPI = false, bool SP2 = false, bool F8 = false>
; __device__ __forceinline__ void gemm_phase(PG8_LAS unsigned char* lds, const Gemm g, const Sched& S, const Epi& E, const int tidb  ) {
;     ...
;             PG8_LDB(B0, 1, 0); PG8_LDB(B1, 1, 1); PG8_SCHED; PG8_LDA(At, 1, 0); PG8_STAGE(PG8_SA(0, 1), a2 + hstep, voffA);
;             PG8_WAIT_V(8); PG8_WAIT_L(0); PG8_BAR; PG8_MMA(0, 0, At, B0); PG8_MMA(0, 1, At, B1); PG8_BAR; PG8_SCHED;
;             PG8_LDA(At, 1, 1); PG8_STAGE(PG8_SB(1, 0), b3, voffB); PG8_STAGE(PG8_SB(1, 1), b3 + hstep, voffB); PG8_STAGE(PG8_SA(1, 0), a3, voffA);
;             PG8_WAIT_V(8); PG8_WAIT_L(0); PG8_BAR; PG8_MMA(1, 0, At, B0); PG8_MMA(1, 1, At, B1); PG8_BAR; PG8_SCHED;
	s_add_i32 s28, 0, 0x18000
	s_add_i32 s29, 0, 0x1c000
	v_add_u32_e32 v14, s28, v186
	v_add_u32_e32 v30, s29, v186
	ds_read_b128 v[2:5], v14
	ds_read_b128 v[6:9], v14 offset:1024
	ds_read_b128 v[10:13], v14 offset:2048
	ds_read_b128 v[14:17], v14 offset:3072
	ds_read_b128 v[18:21], v30
	ds_read_b128 v[22:25], v30 offset:1024
	ds_read_b128 v[26:29], v30 offset:2048
	ds_read_b128 v[30:33], v30 offset:3072
	s_add_u32 s26, s26, s6
	s_addc_u32 s27, s27, s7
	s_mov_b32 m0, s45
	v_lshl_add_u64 v[192:193], s[26:27], 0, v[168:169]
	ds_read_b128 v[204:207], v191 offset:32768
	ds_read_b128 v[208:211], v191 offset:33792
	ds_read_b128 v[212:215], v191 offset:34816
	ds_read_b128 v[216:219], v191 offset:35840
	ds_read_b128 v[220:223], v191 offset:36864
	ds_read_b128 v[224:227], v191 offset:37888
	ds_read_b128 v[228:231], v191 offset:38912
	ds_read_b128 v[232:235], v191 offset:39936
	global_load_lds_dwordx4 v[192:193], off
	v_lshl_add_u64 v[192:193], s[26:27], 0, v[166:167]
	s_mov_b32 m0, s46
	s_nop 0
	global_load_lds_dwordx4 v[192:193], off
	s_waitcnt vmcnt(8)
	s_waitcnt lgkmcnt(0)
	s_barrier
	s_setprio 1
	s_waitcnt lgkmcnt(0)
	v_mfma_scale_f32_16x16x128_f8f6f4 v[154:157], v[2:9], v[204:211], v[154:157], v246, v247 op_sel_hi:[0,0,0]
	v_mfma_scale_f32_16x16x128_f8f6f4 v[150:153], v[10:17], v[204:211], v[150:153], v246, v247 op_sel_hi:[0,0,0]
	v_mfma_scale_f32_16x16x128_f8f6f4 v[142:145], v[2:9], v[212:219], v[142:145], v246, v247 op_sel_hi:[0,0,0]
	v_mfma_scale_f32_16x16x128_f8f6f4 v[134:137], v[10:17], v[212:219], v[134:137], v246, v247 op_sel_hi:[0,0,0]
	v_mfma_scale_f32_16x16x128_f8f6f4 v[126:129], v[2:9], v[220:227], v[126:129], v246, v247 op_sel_hi:[0,0,0]
	v_mfma_scale_f32_16x16x128_f8f6f4 v[118:121], v[10:17], v[220:227], v[118:121], v246, v247 op_sel_hi:[0,0,0]
	v_mfma_scale_f32_16x16x128_f8f6f4 v[110:113], v[2:9], v[228:235], v[110:113], v246, v247 op_sel_hi:[0,0,0]
	v_mfma_scale_f32_16x16x128_f8f6f4 v[102:105], v[10:17], v[228:235], v[102:105], v246, v247 op_sel_hi:[0,0,0]
	s_setprio 0
	s_setprio 1
	v_mfma_scale_f32_16x16x128_f8f6f4 v[158:161], v[18:25], v[204:211], v[158:161], v246, v247 op_sel_hi:[0,0,0]
	v_mfma_scale_f32_16x16x128_f8f6f4 v[146:149], v[26:33], v[204:211], v[146:149], v246, v247 op_sel_hi:[0,0,0]
	v_mfma_scale_f32_16x16x128_f8f6f4 v[138:141], v[18:25], v[212:219], v[138:141], v246, v247 op_sel_hi:[0,0,0]
	v_mfma_scale_f32_16x16x128_f8f6f4 v[130:133], v[26:33], v[212:219], v[130:133], v246, v247 op_sel_hi:[0,0,0]
	v_mfma_scale_f32_16x16x128_f8f6f4 v[122:125], v[18:25], v[220:227], v[122:125], v246, v247 op_sel_hi:[0,0,0]
	v_mfma_scale_f32_16x16x128_f8f6f4 v[114:117], v[26:33], v[220:227], v[114:117], v246, v247 op_sel_hi:[0,0,0]
	v_mfma_scale_f32_16x16x128_f8f6f4 v[106:109], v[18:25], v[228:235], v[106:109], v246, v247 op_sel_hi:[0,0,0]
	v_mfma_scale_f32_16x16x128_f8f6f4 v[98:101], v[26:33], v[228:235], v[98:101], v246, v247 op_sel_hi:[0,0,0]
	s_setprio 2
	s_barrier
	s_add_i32 s26, s28, s36
	v_lshl_add_u64 v[174:175], v[174:175], 0, s[92:93]
	s_mov_b32 m0, s26
	ds_read_b128 v[204:207], v191 offset:49152
	ds_read_b128 v[208:211], v191 offset:50176
	ds_read_b128 v[212:215], v191 offset:51200
	ds_read_b128 v[216:219], v191 offset:52224
	ds_read_b128 v[220:223], v191 offset:53248
	ds_read_b128 v[224:227], v191 offset:54272
	ds_read_b128 v[228:231], v191 offset:55296
	ds_read_b128 v[232:235], v191 offset:56320
	global_load_lds_dwordx4 v[174:175], off
	v_lshl_add_u64 v[174:175], v[176:177], 0, s[92:93]
	s_add_i32 m0, s26, 0x2000
	s_add_i32 s26, s29, s36
	global_load_lds_dwordx4 v[174:175], off
	v_lshl_add_u64 v[174:175], v[178:179], 0, s[92:93]
	s_mov_b32 m0, s26
	s_nop 0
	global_load_lds_dwordx4 v[174:175], off
	v_lshl_add_u64 v[174:175], v[180:181], 0, s[92:93]
	s_add_i32 m0, s26, 0x2000
	s_nop 0
	global_load_lds_dwordx4 v[174:175], off
	v_lshl_add_u64 v[174:175], v[182:183], 0, s[92:93]
	s_mov_b32 m0, s47
	s_nop 0
	global_load_lds_dwordx4 v[174:175], off
	v_lshl_add_u64 v[174:175], v[184:185], 0, s[92:93]
	s_mov_b32 m0, s48
	s_nop 0
	global_load_lds_dwordx4 v[174:175], off
	s_waitcnt vmcnt(8)
	s_waitcnt lgkmcnt(0)
	s_barrier
	s_setprio 1
	s_waitcnt lgkmcnt(0)
	v_mfma_scale_f32_16x16x128_f8f6f4 v[94:97], v[2:9], v[204:211], v[94:97], v246, v247 op_sel_hi:[0,0,0]
	v_mfma_scale_f32_16x16x128_f8f6f4 v[86:89], v[10:17], v[204:211], v[86:89], v246, v247 op_sel_hi:[0,0,0]
	v_mfma_scale_f32_16x16x128_f8f6f4 v[78:81], v[2:9], v[212:219], v[78:81], v246, v247 op_sel_hi:[0,0,0]
	v_mfma_scale_f32_16x16x128_f8f6f4 v[70:73], v[10:17], v[212:219], v[70:73], v246, v247 op_sel_hi:[0,0,0]
	v_mfma_scale_f32_16x16x128_f8f6f4 v[62:65], v[2:9], v[220:227], v[62:65], v246, v247 op_sel_hi:[0,0,0]
	v_mfma_scale_f32_16x16x128_f8f6f4 v[54:57], v[10:17], v[220:227], v[54:57], v246, v247 op_sel_hi:[0,0,0]
	v_mfma_scale_f32_16x16x128_f8f6f4 v[46:49], v[2:9], v[228:235], v[46:49], v246, v247 op_sel_hi:[0,0,0]
	v_mfma_scale_f32_16x16x128_f8f6f4 v[38:41], v[10:17], v[228:235], v[38:41], v246, v247 op_sel_hi:[0,0,0]
	s_setprio 0
	s_setprio 1
	v_mfma_scale_f32_16x16x128_f8f6f4 v[90:93], v[18:25], v[204:211], v[90:93], v246, v247 op_sel_hi:[0,0,0]
	v_mfma_scale_f32_16x16x128_f8f6f4 v[82:85], v[26:33], v[204:211], v[82:85], v246, v247 op_sel_hi:[0,0,0]
	v_mfma_scale_f32_16x16x128_f8f6f4 v[74:77], v[18:25], v[212:219], v[74:77], v246, v247 op_sel_hi:[0,0,0]
	v_mfma_scale_f32_16x16x128_f8f6f4 v[66:69], v[26:33], v[212:219], v[66:69], v246, v247 op_sel_hi:[0,0,0]
	v_mfma_scale_f32_16x16x128_f8f6f4 v[58:61], v[18:25], v[220:227], v[58:61], v246, v247 op_sel_hi:[0,0,0]
	v_mfma_scale_f32_16x16x128_f8f6f4 v[50:53], v[26:33], v[220:227], v[50:53], v246, v247 op_sel_hi:[0,0,0]
	v_mfma_scale_f32_16x16x128_f8f6f4 v[42:45], v[18:25], v[228:235], v[42:45], v246, v247 op_sel_hi:[0,0,0]
	v_mfma_scale_f32_16x16x128_f8f6f4 v[34:37], v[26:33], v[228:235], v[34:37], v246, v247 op_sel_hi:[0,0,0]
	s_setprio 2
	s_barrier
	s_add_u32 s24, s24, 0x100
	s_addc_u32 s25, s25, 0
	s_add_u32 s58, s58, 0x100
	s_addc_u32 s59, s59, 0
	s_cmp_ge_i32 s60, s49
	s_mov_b32 s26, s60
	s_cbranch_scc0 .LBB0_1728

; #define PG8_STAGE(bufoff, gbase, voff) do { _Pragma("unroll") for (int _i = 0; _i < 2; ++_i) \
;         __builtin_amdgcn_global_load_lds((const unsigned*)((const char*)(gbase) + (voff)[_i]), (PG8_LAS unsigned*)(lds + (bufoff) + ldsw + _i * 8192), 16, 0, 0); } while (0)
; #define PG8_WAIT_V(n) asm volatile("s_waitcnt vmcnt(" #n ")" ::: "memory")
; #define PG8_WAIT_L(n) asm volatile("s_waitcnt lgkmcnt(" #n ")" ::: "memory")
; #define PG8_BAR __builtin_amdgcn_s_barrier()
; #define PG8_SCHED __builtin_amdgcn_sched_barrier(0)
; template <class Epi, class Sched, bool ALIGN_EPI = false, bool SP2 = false, bool F8 = false>
; __device__ __forceinline__ void gemm_phase(PG8_LAS unsigned char* lds, const Gemm g, const Sched& S, const Epi& E, const int tidb  ) {
;     ...
;             const bool last = (t == nt - 2);
;             if constexpr (Epi::PREFETCH) { if (t == 0) E.prefetch(cur, wid, lane); }
;             const char* a1 = cA + (size_t)(t + 1) * kstep;
;             const char* a2 = last ? nA : cA + (size_t)(t + 2) * kstep; const char* b2 = last ? nB : cB + (size_t)(t + 2) * kstep;
;             const char* a3 = a2 + kstep; const char* b3 = b2 + kstep;
;             if (last && has_next) S.a_ready(nxt);
;             if constexpr (SP2) {
;             PG8_LDB(B0, 0, 0); PG8_LDB(B1, 0, 1); PG8_SCHED; PG8_LDA(At, 0, 0); PG8_STAGE(PG8_SA(1, 1), a1 + hstep, voffA);
;             PG8_WAIT_V(8); PG8_WAIT_L(0); PG8_BAR; PG8_MMA(0, 0, At, B0); PG8_MMA(0, 1, At, B1); PG8_BAR; PG8_SCHED;
;             PG8_LDA(At, 0, 1); PG8_STAGE(PG8_SB(0, 0), b2, voffB); PG8_STAGE(PG8_SB(0, 1), b2 + hstep, voffB); PG8_STAGE(PG8_SA(0, 0), a2, voffA);
;             PG8_WAIT_V(8); PG8_WAIT_L(0); PG8_BAR; PG8_MMA(1, 0, At, B0); PG8_MMA(1, 1, At, B1); PG8_BAR; PG8_SCHED;
.LBB0_1807:
	s_add_i32 s65, s30, 2
	s_add_u32 s66, s28, 0x80
	s_addc_u32 s31, s29, 0
	s_add_i32 s68, 0, 0x10000
	s_cmp_eq_u32 s47, s30
	s_cselect_b32 s31, s7, s31
	s_cselect_b32 s30, s6, s66
	s_cselect_b32 s67, s27, s63
	s_cselect_b32 s66, s26, s62
	s_add_i32 s70, 0, 0x14000
	v_add_u32_e32 v142, s68, v192
	v_add_u32_e32 v170, s70, v192
	ds_read_b128 v[122:125], v142
	ds_read_b128 v[126:129], v142 offset:1024
	ds_read_b128 v[138:141], v142 offset:2048
	ds_read_b128 v[142:145], v142 offset:3072
	ds_read_b128 v[146:149], v170
	ds_read_b128 v[150:153], v170 offset:1024
	ds_read_b128 v[154:157], v170 offset:2048
	ds_read_b128 v[170:173], v170 offset:3072
	v_lshl_add_u64 v[190:191], s[28:29], 0, v[166:167]
	s_add_i32 m0, s1, 0xc000
	ds_read_b128 v[174:177], v194
	ds_read_b128 v[178:181], v194 offset:1024
	ds_read_b128 v[182:185], v194 offset:2048
	ds_read_b128 v[186:189], v194 offset:3072
	ds_read_b128 v[204:207], v194 offset:4096
	ds_read_b128 v[208:211], v194 offset:5120
	ds_read_b128 v[212:215], v194 offset:6144
	ds_read_b128 v[216:219], v194 offset:7168
	global_load_lds_dwordx4 v[190:191], off
	v_lshl_add_u64 v[190:191], s[28:29], 0, v[168:169]
	s_add_i32 m0, s1, 0xe000
	s_nop 0
	global_load_lds_dwordx4 v[190:191], off
	s_waitcnt vmcnt(8)
	s_waitcnt lgkmcnt(0)
	s_barrier
	s_setprio 1
	s_waitcnt lgkmcnt(0)
	v_mfma_f32_16x16x32_bf16 v[134:137], v[122:125], v[174:177], v[134:137]
	v_mfma_f32_16x16x32_bf16 v[130:133], v[138:141], v[174:177], v[130:133]
	v_mfma_f32_16x16x32_bf16 v[110:113], v[122:125], v[182:185], v[110:113]
	v_mfma_f32_16x16x32_bf16 v[106:109], v[138:141], v[182:185], v[106:109]
	v_mfma_f32_16x16x32_bf16 v[94:97], v[122:125], v[204:207], v[94:97]
	v_mfma_f32_16x16x32_bf16 v[90:93], v[138:141], v[204:207], v[90:93]
	v_mfma_f32_16x16x32_bf16 v[78:81], v[122:125], v[212:215], v[78:81]
	v_mfma_f32_16x16x32_bf16 v[74:77], v[138:141], v[212:215], v[74:77]
	v_mfma_f32_16x16x32_bf16 v[134:137], v[126:129], v[178:181], v[134:137]
	v_mfma_f32_16x16x32_bf16 v[130:133], v[142:145], v[178:181], v[130:133]
	v_mfma_f32_16x16x32_bf16 v[110:113], v[126:129], v[186:189], v[110:113]
	v_mfma_f32_16x16x32_bf16 v[106:109], v[142:145], v[186:189], v[106:109]
	v_mfma_f32_16x16x32_bf16 v[94:97], v[126:129], v[208:211], v[94:97]
	v_mfma_f32_16x16x32_bf16 v[90:93], v[142:145], v[208:211], v[90:93]
	v_mfma_f32_16x16x32_bf16 v[78:81], v[126:129], v[216:219], v[78:81]
	v_mfma_f32_16x16x32_bf16 v[74:77], v[142:145], v[216:219], v[74:77]
	s_setprio 0
	s_setprio 1
	v_mfma_f32_16x16x32_bf16 v[118:121], v[146:149], v[174:177], v[118:121]
	v_mfma_f32_16x16x32_bf16 v[114:117], v[154:157], v[174:177], v[114:117]
	v_mfma_f32_16x16x32_bf16 v[102:105], v[146:149], v[182:185], v[102:105]
	v_mfma_f32_16x16x32_bf16 v[98:101], v[154:157], v[182:185], v[98:101]
	v_mfma_f32_16x16x32_bf16 v[86:89], v[146:149], v[204:207], v[86:89]
	v_mfma_f32_16x16x32_bf16 v[82:85], v[154:157], v[204:207], v[82:85]
	v_mfma_f32_16x16x32_bf16 v[70:73], v[146:149], v[212:215], v[70:73]
	v_mfma_f32_16x16x32_bf16 v[66:69], v[154:157], v[212:215], v[66:69]
	v_mfma_f32_16x16x32_bf16 v[118:121], v[150:153], v[178:181], v[118:121]
	v_mfma_f32_16x16x32_bf16 v[114:117], v[170:173], v[178:181], v[114:117]
	v_mfma_f32_16x16x32_bf16 v[102:105], v[150:153], v[186:189], v[102:105]
	v_mfma_f32_16x16x32_bf16 v[98:101], v[170:173], v[186:189], v[98:101]
	v_mfma_f32_16x16x32_bf16 v[86:89], v[150:153], v[208:211], v[86:89]
	v_mfma_f32_16x16x32_bf16 v[82:85], v[170:173], v[208:211], v[82:85]
	v_mfma_f32_16x16x32_bf16 v[70:73], v[150:153], v[216:219], v[70:73]
	v_mfma_f32_16x16x32_bf16 v[66:69], v[170:173], v[216:219], v[66:69]
	s_setprio 2
	s_barrier
	s_add_i32 s68, s68, s0
	v_lshl_add_u64 v[190:191], s[66:67], 0, v[0:1]
	s_mov_b32 m0, s68
	ds_read_b128 v[174:177], v194 offset:16384
	ds_read_b128 v[178:181], v194 offset:17408
	ds_read_b128 v[182:185], v194 offset:18432
	ds_read_b128 v[186:189], v194 offset:19456
	ds_read_b128 v[204:207], v194 offset:20480
	ds_read_b128 v[208:211], v194 offset:21504
	ds_read_b128 v[212:215], v194 offset:22528
	ds_read_b128 v[216:219], v194 offset:23552
	global_load_lds_dwordx4 v[190:191], off
	s_add_i32 m0, s68, 0x2000
	v_lshl_add_u64 v[196:197], s[66:67], 0, v[164:165]
	s_add_u32 s66, s66, s12
	s_addc_u32 s67, s67, s13
	s_add_i32 s68, s70, s0
	global_load_lds_dwordx4 v[196:197], off
	v_lshl_add_u64 v[198:199], s[66:67], 0, v[0:1]
	s_mov_b32 m0, s68
	v_lshl_add_u64 v[200:201], s[66:67], 0, v[164:165]
	global_load_lds_dwordx4 v[198:199], off
	s_add_i32 m0, s68, 0x2000
	v_lshl_add_u64 v[220:221], s[30:31], 0, v[158:159]
	global_load_lds_dwordx4 v[200:201], off
	s_mov_b32 m0, s1
	v_lshl_add_u64 v[222:223], s[30:31], 0, v[160:161]
	global_load_lds_dwordx4 v[220:221], off
	s_mov_b32 m0, s36
	s_nop 0
	global_load_lds_dwordx4 v[222:223], off
	s_waitcnt vmcnt(8)
	s_waitcnt lgkmcnt(0)
	s_barrier
; #define PG8_STAGE(bufoff, gbase, voff) do { _Pragma("unroll") for (int _i = 0; _i < 2; ++_i) \
;         __builtin_amdgcn_global_load_lds((const unsigned*)((const char*)(gbase) + (voff)[_i]), (PG8_LAS unsigned*)(lds + (bufoff) + ldsw + _i * 8192), 16, 0, 0); } while (0)
; #define PG8_WAIT_V(n) asm volatile("s_waitcnt vmcnt(" #n ")" ::: "memory")
; #define PG8_WAIT_L(n) asm volatile("s_waitcnt lgkmcnt(" #n ")" ::: "memory")
; #define PG8_BAR __builtin_amdgcn_s_barrier()
; #define PG8_SCHED __builtin_amdgcn_sched_barrier(0)
; template <class Epi, class Sched, bool ALIGN_EPI = false, bool SP2 = false, bool F8 = false>
; __device__ __forceinline__ void gemm_phase(PG8_LAS unsigned char* lds, const Gemm g, const Sched& S, const Epi& E, const int tidb  ) {
;     ...
;             PG8_WAIT_V(8); PG8_WAIT_L(0); PG8_BAR; PG8_MMA(1, 0, At, B0); PG8_MMA(1, 1, At, B1); PG8_BAR; PG8_SCHED;
;             PG8_LDB(B0, 1, 0); PG8_LDB(B1, 1, 1); PG8_SCHED; PG8_LDA(At, 1, 0); PG8_STAGE(PG8_SA(0, 1), a2 + hstep, voffA);
;             PG8_WAIT_V(8); PG8_WAIT_L(0); PG8_BAR; PG8_MMA(0, 0, At, B0); PG8_MMA(0, 1, At, B1); PG8_BAR; PG8_SCHED;
	s_setprio 1
	s_waitcnt lgkmcnt(0)
	v_mfma_f32_16x16x32_bf16 v[62:65], v[122:125], v[174:177], v[62:65]
	v_mfma_f32_16x16x32_bf16 v[58:61], v[138:141], v[174:177], v[58:61]
	v_mfma_f32_16x16x32_bf16 v[46:49], v[122:125], v[182:185], v[46:49]
	v_mfma_f32_16x16x32_bf16 v[42:45], v[138:141], v[182:185], v[42:45]
	v_mfma_f32_16x16x32_bf16 v[30:33], v[122:125], v[204:207], v[30:33]
	v_mfma_f32_16x16x32_bf16 v[26:29], v[138:141], v[204:207], v[26:29]
	v_mfma_f32_16x16x32_bf16 v[14:17], v[122:125], v[212:215], v[14:17]
	v_mfma_f32_16x16x32_bf16 v[10:13], v[138:141], v[212:215], v[10:13]
	v_mfma_f32_16x16x32_bf16 v[62:65], v[126:129], v[178:181], v[62:65]
	v_mfma_f32_16x16x32_bf16 v[58:61], v[142:145], v[178:181], v[58:61]
	v_mfma_f32_16x16x32_bf16 v[46:49], v[126:129], v[186:189], v[46:49]
	v_mfma_f32_16x16x32_bf16 v[42:45], v[142:145], v[186:189], v[42:45]
	v_mfma_f32_16x16x32_bf16 v[30:33], v[126:129], v[208:211], v[30:33]
	v_mfma_f32_16x16x32_bf16 v[26:29], v[142:145], v[208:211], v[26:29]
	v_mfma_f32_16x16x32_bf16 v[14:17], v[126:129], v[216:219], v[14:17]
	v_mfma_f32_16x16x32_bf16 v[10:13], v[142:145], v[216:219], v[10:13]
	s_setprio 0
	s_setprio 1
	v_mfma_f32_16x16x32_bf16 v[54:57], v[146:149], v[174:177], v[54:57]
	v_mfma_f32_16x16x32_bf16 v[50:53], v[154:157], v[174:177], v[50:53]
	v_mfma_f32_16x16x32_bf16 v[38:41], v[146:149], v[182:185], v[38:41]
	v_mfma_f32_16x16x32_bf16 v[34:37], v[154:157], v[182:185], v[34:37]
	v_mfma_f32_16x16x32_bf16 v[22:25], v[146:149], v[204:207], v[22:25]
	v_mfma_f32_16x16x32_bf16 v[18:21], v[154:157], v[204:207], v[18:21]
	v_mfma_f32_16x16x32_bf16 v[6:9], v[146:149], v[212:215], v[6:9]
	v_mfma_f32_16x16x32_bf16 v[2:5], v[154:157], v[212:215], v[2:5]
	v_mfma_f32_16x16x32_bf16 v[54:57], v[150:153], v[178:181], v[54:57]
	v_mfma_f32_16x16x32_bf16 v[50:53], v[170:173], v[178:181], v[50:53]
	v_mfma_f32_16x16x32_bf16 v[38:41], v[150:153], v[186:189], v[38:41]
	v_mfma_f32_16x16x32_bf16 v[34:37], v[170:173], v[186:189], v[34:37]
	v_mfma_f32_16x16x32_bf16 v[22:25], v[150:153], v[208:211], v[22:25]
	v_mfma_f32_16x16x32_bf16 v[18:21], v[170:173], v[208:211], v[18:21]
	v_mfma_f32_16x16x32_bf16 v[6:9], v[150:153], v[216:219], v[6:9]
	v_mfma_f32_16x16x32_bf16 v[2:5], v[170:173], v[216:219], v[2:5]
	s_setprio 2
	s_barrier
	s_add_i32 s66, 0, 0x18000
	s_add_i32 s67, 0, 0x1c000
	v_add_u32_e32 v142, s66, v192
	v_add_u32_e32 v170, s67, v192
	ds_read_b128 v[122:125], v142
	ds_read_b128 v[126:129], v142 offset:1024
	ds_read_b128 v[138:141], v142 offset:2048
	ds_read_b128 v[142:145], v142 offset:3072
	ds_read_b128 v[146:149], v170
	ds_read_b128 v[150:153], v170 offset:1024
	ds_read_b128 v[154:157], v170 offset:2048
	ds_read_b128 v[170:173], v170 offset:3072
	s_add_u32 s30, s30, s12
	s_addc_u32 s31, s31, s13
	s_mov_b32 m0, s37
	v_lshl_add_u64 v[224:225], s[30:31], 0, v[158:159]
	ds_read_b128 v[174:177], v194 offset:32768
	ds_read_b128 v[178:181], v194 offset:33792
	ds_read_b128 v[182:185], v194 offset:34816
	ds_read_b128 v[186:189], v194 offset:35840
	ds_read_b128 v[204:207], v194 offset:36864
	ds_read_b128 v[208:211], v194 offset:37888
	ds_read_b128 v[212:215], v194 offset:38912
	ds_read_b128 v[216:219], v194 offset:39936
	global_load_lds_dwordx4 v[224:225], off
	v_lshl_add_u64 v[224:225], s[30:31], 0, v[160:161]
	s_mov_b32 m0, s41
	s_nop 0
	global_load_lds_dwordx4 v[224:225], off
	s_waitcnt vmcnt(8)
	s_waitcnt lgkmcnt(0)
	s_barrier
	s_setprio 1
	s_waitcnt lgkmcnt(0)
	v_mfma_f32_16x16x32_bf16 v[134:137], v[122:125], v[174:177], v[134:137]
	v_mfma_f32_16x16x32_bf16 v[130:133], v[138:141], v[174:177], v[130:133]
	v_mfma_f32_16x16x32_bf16 v[110:113], v[122:125], v[182:185], v[110:113]
	v_mfma_f32_16x16x32_bf16 v[106:109], v[138:141], v[182:185], v[106:109]
	v_mfma_f32_16x16x32_bf16 v[94:97], v[122:125], v[204:207], v[94:97]
	v_mfma_f32_16x16x32_bf16 v[90:93], v[138:141], v[204:207], v[90:93]
	v_mfma_f32_16x16x32_bf16 v[78:81], v[122:125], v[212:215], v[78:81]
	v_mfma_f32_16x16x32_bf16 v[74:77], v[138:141], v[212:215], v[74:77]
	v_mfma_f32_16x16x32_bf16 v[134:137], v[126:129], v[178:181], v[134:137]
	v_mfma_f32_16x16x32_bf16 v[130:133], v[142:145], v[178:181], v[130:133]
	v_mfma_f32_16x16x32_bf16 v[110:113], v[126:129], v[186:189], v[110:113]
	v_mfma_f32_16x16x32_bf16 v[106:109], v[142:145], v[186:189], v[106:109]
	v_mfma_f32_16x16x32_bf16 v[94:97], v[126:129], v[208:211], v[94:97]
	v_mfma_f32_16x16x32_bf16 v[90:93], v[142:145], v[208:211], v[90:93]
	v_mfma_f32_16x16x32_bf16 v[78:81], v[126:129], v[216:219], v[78:81]
	v_mfma_f32_16x16x32_bf16 v[74:77], v[142:145], v[216:219], v[74:77]
	s_setprio 0
	s_setprio 1
	v_mfma_f32_16x16x32_bf16 v[118:121], v[146:149], v[174:177], v[118:121]
	v_mfma_f32_16x16x32_bf16 v[114:117], v[154:157], v[174:177], v[114:117]
	v_mfma_f32_16x16x32_bf16 v[102:105], v[146:149], v[182:185], v[102:105]
	v_mfma_f32_16x16x32_bf16 v[98:101], v[154:157], v[182:185], v[98:101]
	v_mfma_f32_16x16x32_bf16 v[86:89], v[146:149], v[204:207], v[86:89]
	v_mfma_f32_16x16x32_bf16 v[82:85], v[154:157], v[204:207], v[82:85]
	v_mfma_f32_16x16x32_bf16 v[70:73], v[146:149], v[212:215], v[70:73]
	v_mfma_f32_16x16x32_bf16 v[66:69], v[154:157], v[212:215], v[66:69]
	v_mfma_f32_16x16x32_bf16 v[118:121], v[150:153], v[178:181], v[118:121]
	v_mfma_f32_16x16x32_bf16 v[114:117], v[170:173], v[178:181], v[114:117]
	v_mfma_f32_16x16x32_bf16 v[102:105], v[150:153], v[186:189], v[102:105]
	v_mfma_f32_16x16x32_bf16 v[98:101], v[170:173], v[186:189], v[98:101]
	v_mfma_f32_16x16x32_bf16 v[86:89], v[150:153], v[208:211], v[86:89]
	v_mfma_f32_16x16x32_bf16 v[82:85], v[170:173], v[208:211], v[82:85]
	v_mfma_f32_16x16x32_bf16 v[70:73], v[150:153], v[216:219], v[70:73]
	v_mfma_f32_16x16x32_bf16 v[66:69], v[170:173], v[216:219], v[66:69]
	s_setprio 2
	s_barrier
; #define PG8_STAGE(bufoff, gbase, voff) do { _Pragma("unroll") for (int _i = 0; _i < 2; ++_i) \
;         __builtin_amdgcn_global_load_lds((const unsigned*)((const char*)(gbase) + (voff)[_i]), (PG8_LAS unsigned*)(lds + (bufoff) + ldsw + _i * 8192), 16, 0, 0); } while (0)
; #define PG8_WAIT_V(n) asm volatile("s_waitcnt vmcnt(" #n ")" ::: "memory")
; #define PG8_WAIT_L(n) asm volatile("s_waitcnt lgkmcnt(" #n ")" ::: "memory")
; #define PG8_BAR __builtin_amdgcn_s_barrier()
; #define PG8_SCHED __builtin_amdgcn_sched_barrier(0)
; template <class Epi, class Sched, bool ALIGN_EPI = false, bool SP2 = false, bool F8 = false>
; __device__ __forceinline__ void gemm_phase(PG8_LAS unsigned char* lds, const Gemm g, const Sched& S, const Epi& E, const int tidb  ) {
;     ...
;             PG8_LDA(At, 1, 1); PG8_STAGE(PG8_SB(1, 0), b3, voffB); PG8_STAGE(PG8_SB(1, 1), b3 + hstep, voffB); PG8_STAGE(PG8_SA(1, 0), a3, voffA);
;             PG8_WAIT_V(8); PG8_WAIT_L(0); PG8_BAR; PG8_MMA(1, 0, At, B0); PG8_MMA(1, 1, At, B1); PG8_BAR; PG8_SCHED;
	s_add_i32 s30, s66, s0
	v_lshl_add_u64 v[190:191], v[190:191], 0, s[92:93]
	s_mov_b32 m0, s30
	ds_read_b128 v[174:177], v194 offset:49152
	ds_read_b128 v[178:181], v194 offset:50176
	ds_read_b128 v[182:185], v194 offset:51200
	ds_read_b128 v[186:189], v194 offset:52224
	ds_read_b128 v[204:207], v194 offset:53248
	ds_read_b128 v[208:211], v194 offset:54272
	ds_read_b128 v[212:215], v194 offset:55296
	ds_read_b128 v[216:219], v194 offset:56320
	global_load_lds_dwordx4 v[190:191], off
	v_lshl_add_u64 v[190:191], v[196:197], 0, s[92:93]
	s_add_i32 m0, s30, 0x2000
	s_add_i32 s30, s67, s0
	global_load_lds_dwordx4 v[190:191], off
	v_lshl_add_u64 v[190:191], v[198:199], 0, s[92:93]
	s_mov_b32 m0, s30
	s_nop 0
	global_load_lds_dwordx4 v[190:191], off
	v_lshl_add_u64 v[190:191], v[200:201], 0, s[92:93]
	s_add_i32 m0, s30, 0x2000
	s_nop 0
	global_load_lds_dwordx4 v[190:191], off
	v_lshl_add_u64 v[190:191], v[220:221], 0, s[92:93]
	s_mov_b32 m0, s43
	s_nop 0
	global_load_lds_dwordx4 v[190:191], off
	v_lshl_add_u64 v[190:191], v[222:223], 0, s[92:93]
	s_mov_b32 m0, s45
	s_nop 0
	global_load_lds_dwordx4 v[190:191], off
	s_waitcnt vmcnt(8)
	s_waitcnt lgkmcnt(0)
	s_barrier
	s_setprio 1
	s_waitcnt lgkmcnt(0)
	v_mfma_f32_16x16x32_bf16 v[62:65], v[122:125], v[174:177], v[62:65]
	v_mfma_f32_16x16x32_bf16 v[58:61], v[138:141], v[174:177], v[58:61]
	v_mfma_f32_16x16x32_bf16 v[46:49], v[122:125], v[182:185], v[46:49]
	v_mfma_f32_16x16x32_bf16 v[42:45], v[138:141], v[182:185], v[42:45]
	v_mfma_f32_16x16x32_bf16 v[30:33], v[122:125], v[204:207], v[30:33]
	v_mfma_f32_16x16x32_bf16 v[26:29], v[138:141], v[204:207], v[26:29]
	v_mfma_f32_16x16x32_bf16 v[14:17], v[122:125], v[212:215], v[14:17]
	v_mfma_f32_16x16x32_bf16 v[10:13], v[138:141], v[212:215], v[10:13]
	v_mfma_f32_16x16x32_bf16 v[62:65], v[126:129], v[178:181], v[62:65]
	v_mfma_f32_16x16x32_bf16 v[58:61], v[142:145], v[178:181], v[58:61]
	v_mfma_f32_16x16x32_bf16 v[46:49], v[126:129], v[186:189], v[46:49]
	v_mfma_f32_16x16x32_bf16 v[42:45], v[142:145], v[186:189], v[42:45]
	v_mfma_f32_16x16x32_bf16 v[30:33], v[126:129], v[208:211], v[30:33]
	v_mfma_f32_16x16x32_bf16 v[26:29], v[142:145], v[208:211], v[26:29]
	v_mfma_f32_16x16x32_bf16 v[14:17], v[126:129], v[216:219], v[14:17]
	v_mfma_f32_16x16x32_bf16 v[10:13], v[142:145], v[216:219], v[10:13]
	s_setprio 0
	s_setprio 1
	v_mfma_f32_16x16x32_bf16 v[54:57], v[146:149], v[174:177], v[54:57]
	v_mfma_f32_16x16x32_bf16 v[50:53], v[154:157], v[174:177], v[50:53]
	v_mfma_f32_16x16x32_bf16 v[38:41], v[146:149], v[182:185], v[38:41]
	v_mfma_f32_16x16x32_bf16 v[34:37], v[154:157], v[182:185], v[34:37]
	v_mfma_f32_16x16x32_bf16 v[22:25], v[146:149], v[204:207], v[22:25]
	v_mfma_f32_16x16x32_bf16 v[18:21], v[154:157], v[204:207], v[18:21]
	v_mfma_f32_16x16x32_bf16 v[6:9], v[146:149], v[212:215], v[6:9]
	v_mfma_f32_16x16x32_bf16 v[2:5], v[154:157], v[212:215], v[2:5]
	v_mfma_f32_16x16x32_bf16 v[54:57], v[150:153], v[178:181], v[54:57]
	v_mfma_f32_16x16x32_bf16 v[50:53], v[170:173], v[178:181], v[50:53]
	v_mfma_f32_16x16x32_bf16 v[38:41], v[150:153], v[186:189], v[38:41]
	v_mfma_f32_16x16x32_bf16 v[34:37], v[170:173], v[186:189], v[34:37]
	v_mfma_f32_16x16x32_bf16 v[22:25], v[150:153], v[208:211], v[22:25]
	v_mfma_f32_16x16x32_bf16 v[18:21], v[170:173], v[208:211], v[18:21]
	v_mfma_f32_16x16x32_bf16 v[6:9], v[150:153], v[216:219], v[6:9]
	v_mfma_f32_16x16x32_bf16 v[2:5], v[170:173], v[216:219], v[2:5]
	s_setprio 2
	s_barrier
	s_add_u32 s28, s28, 0x100
	s_addc_u32 s29, s29, 0
	s_add_u32 s62, s62, 0x100
	s_addc_u32 s63, s63, 0
	s_cmp_ge_i32 s65, s46
	s_mov_b32 s30, s65
	s_cbranch_scc0 .LBB0_1807
	s_movk_i32 s67, 0x300

; #define PG8_STAGE(bufoff, gbase, voff) do { _Pragma("unroll") for (int _i = 0; _i < 2; ++_i) \
;         __builtin_amdgcn_global_load_lds((const unsigned*)((const char*)(gbase) + (voff)[_i]), (PG8_LAS unsigned*)(lds + (bufoff) + ldsw + _i * 8192), 16, 0, 0); } while (0)
; #define PG8_WAIT_V(n) asm volatile("s_waitcnt vmcnt(" #n ")" ::: "memory")
; #define PG8_WAIT_L(n) asm volatile("s_waitcnt lgkmcnt(" #n ")" ::: "memory")
; #define PG8_BAR __builtin_amdgcn_s_barrier()
; #define PG8_SCHED __builtin_amdgcn_sched_barrier(0)
; template <class Epi, class Sched, bool ALIGN_EPI = false, bool SP2 = false, bool F8 = false>
; __device__ __forceinline__ void gemm_phase(PG8_LAS unsigned char* lds, const Gemm g, const Sched& S, const Epi& E, const int tidb  ) {
;     ...
;             const bool last = (t == nt - 2);
;             if constexpr (Epi::PREFETCH) { if (t == 0) E.prefetch(cur, wid, lane); }
;             const char* a1 = cA + (size_t)(t + 1) * kstep;
;             const char* a2 = last ? nA : cA + (size_t)(t + 2) * kstep; const char* b2 = last ? nB : cB + (size_t)(t + 2) * kstep;
;             const char* a3 = a2 + kstep; const char* b3 = b2 + kstep;
;             if (last && has_next) S.a_ready(nxt);
;             if constexpr (SP2) {
;             PG8_LDB(B0, 0, 0); PG8_LDB(B1, 0, 1); PG8_SCHED; PG8_LDA(At, 0, 0); PG8_STAGE(PG8_SA(1, 1), a1 + hstep, voffA);
;             PG8_WAIT_V(8); PG8_WAIT_L(0); PG8_BAR; PG8_MMA(0, 0, At, B0); PG8_MMA(0, 1, At, B1); PG8_BAR; PG8_SCHED;
;             PG8_LDA(At, 0, 1); PG8_STAGE(PG8_SB(0, 0), b2, voffB); PG8_STAGE(PG8_SB(0, 1), b2 + hstep, voffB); PG8_STAGE(PG8_SA(0, 0), a2, voffA);
;             PG8_WAIT_V(8); PG8_WAIT_L(0); PG8_BAR; PG8_MMA(1, 0, At, B0); PG8_MMA(1, 1, At, B1); PG8_BAR; PG8_SCHED;
.LBB0_1857:
	s_add_i32 s65, s28, 2
	s_add_u32 s30, s26, 0x80
	s_addc_u32 s29, s27, 0
	s_add_i32 s66, 0, 0x10000
	s_cmp_eq_u32 s47, s28
	s_cselect_b32 s29, s7, s29
	s_cselect_b32 s28, s6, s30
	s_cselect_b32 s31, s11, s63
	s_cselect_b32 s30, s10, s62
	s_add_i32 s67, 0, 0x14000
	v_add_u32_e32 v2, s66, v192
	v_add_u32_e32 v14, s67, v192
	ds_read_b128 v[18:21], v2
	ds_read_b128 v[22:25], v2 offset:1024
	ds_read_b128 v[26:29], v2 offset:2048
	ds_read_b128 v[30:33], v2 offset:3072
	ds_read_b128 v[2:5], v14
	ds_read_b128 v[6:9], v14 offset:1024
	ds_read_b128 v[10:13], v14 offset:2048
	ds_read_b128 v[14:17], v14 offset:3072
	v_lshl_add_u64 v[190:191], s[26:27], 0, v[170:171]
	s_add_i32 m0, s1, 0xc000
	ds_read_b128 v[174:177], v194
	ds_read_b128 v[178:181], v194 offset:1024
	ds_read_b128 v[182:185], v194 offset:2048
	ds_read_b128 v[186:189], v194 offset:3072
	ds_read_b128 v[204:207], v194 offset:4096
	ds_read_b128 v[208:211], v194 offset:5120
	ds_read_b128 v[212:215], v194 offset:6144
	ds_read_b128 v[216:219], v194 offset:7168
	global_load_lds_dwordx4 v[190:191], off
	v_lshl_add_u64 v[190:191], s[26:27], 0, v[172:173]
	s_add_i32 m0, s1, 0xe000
	s_nop 0
	global_load_lds_dwordx4 v[190:191], off
	s_waitcnt vmcnt(8)
	s_waitcnt lgkmcnt(0)
	s_barrier
	s_setprio 1
	s_waitcnt lgkmcnt(0)
	v_mfma_scale_f32_16x16x128_f8f6f4 v[158:161], v[18:25], v[174:181], v[158:161], v246, v247 op_sel_hi:[0,0,0]
	v_mfma_scale_f32_16x16x128_f8f6f4 v[154:157], v[26:33], v[174:181], v[154:157], v246, v247 op_sel_hi:[0,0,0]
	v_mfma_scale_f32_16x16x128_f8f6f4 v[142:145], v[18:25], v[182:189], v[142:145], v246, v247 op_sel_hi:[0,0,0]
	v_mfma_scale_f32_16x16x128_f8f6f4 v[138:141], v[26:33], v[182:189], v[138:141], v246, v247 op_sel_hi:[0,0,0]
	v_mfma_scale_f32_16x16x128_f8f6f4 v[126:129], v[18:25], v[204:211], v[126:129], v246, v247 op_sel_hi:[0,0,0]
	v_mfma_scale_f32_16x16x128_f8f6f4 v[122:125], v[26:33], v[204:211], v[122:125], v246, v247 op_sel_hi:[0,0,0]
	v_mfma_scale_f32_16x16x128_f8f6f4 v[110:113], v[18:25], v[212:219], v[110:113], v246, v247 op_sel_hi:[0,0,0]
	v_mfma_scale_f32_16x16x128_f8f6f4 v[106:109], v[26:33], v[212:219], v[106:109], v246, v247 op_sel_hi:[0,0,0]
	s_setprio 0
	s_setprio 1
	v_mfma_scale_f32_16x16x128_f8f6f4 v[150:153], v[2:9], v[174:181], v[150:153], v246, v247 op_sel_hi:[0,0,0]
	v_mfma_scale_f32_16x16x128_f8f6f4 v[146:149], v[10:17], v[174:181], v[146:149], v246, v247 op_sel_hi:[0,0,0]
	v_mfma_scale_f32_16x16x128_f8f6f4 v[134:137], v[2:9], v[182:189], v[134:137], v246, v247 op_sel_hi:[0,0,0]
	v_mfma_scale_f32_16x16x128_f8f6f4 v[130:133], v[10:17], v[182:189], v[130:133], v246, v247 op_sel_hi:[0,0,0]
	v_mfma_scale_f32_16x16x128_f8f6f4 v[118:121], v[2:9], v[204:211], v[118:121], v246, v247 op_sel_hi:[0,0,0]
	v_mfma_scale_f32_16x16x128_f8f6f4 v[114:117], v[10:17], v[204:211], v[114:117], v246, v247 op_sel_hi:[0,0,0]
	v_mfma_scale_f32_16x16x128_f8f6f4 v[102:105], v[2:9], v[212:219], v[102:105], v246, v247 op_sel_hi:[0,0,0]
	v_mfma_scale_f32_16x16x128_f8f6f4 v[98:101], v[10:17], v[212:219], v[98:101], v246, v247 op_sel_hi:[0,0,0]
	s_setprio 2
	s_barrier
	s_add_i32 s66, s66, s0
	v_lshl_add_u64 v[174:175], s[30:31], 0, v[0:1]
	s_mov_b32 m0, s66
	ds_read_b128 v[204:207], v194 offset:16384
	ds_read_b128 v[208:211], v194 offset:17408
	ds_read_b128 v[212:215], v194 offset:18432
	ds_read_b128 v[216:219], v194 offset:19456
	ds_read_b128 v[220:223], v194 offset:20480
	ds_read_b128 v[224:227], v194 offset:21504
	ds_read_b128 v[228:231], v194 offset:22528
	ds_read_b128 v[232:235], v194 offset:23552
	global_load_lds_dwordx4 v[174:175], off
	s_add_i32 m0, s66, 0x2000
	v_lshl_add_u64 v[176:177], s[30:31], 0, v[168:169]
	s_add_u32 s30, s30, s12
	s_addc_u32 s31, s31, s13
	s_add_i32 s66, s67, s0
	global_load_lds_dwordx4 v[176:177], off
	v_lshl_add_u64 v[178:179], s[30:31], 0, v[0:1]
	s_mov_b32 m0, s66
	v_lshl_add_u64 v[180:181], s[30:31], 0, v[168:169]
	global_load_lds_dwordx4 v[178:179], off
	s_add_i32 m0, s66, 0x2000
	v_lshl_add_u64 v[182:183], s[28:29], 0, v[164:165]
	global_load_lds_dwordx4 v[180:181], off
	s_mov_b32 m0, s1
	v_lshl_add_u64 v[184:185], s[28:29], 0, v[166:167]
	global_load_lds_dwordx4 v[182:183], off
	s_mov_b32 m0, s36
	s_nop 0
	global_load_lds_dwordx4 v[184:185], off
	s_waitcnt vmcnt(8)
	s_waitcnt lgkmcnt(0)
	s_barrier
	s_setprio 1
	s_waitcnt lgkmcnt(0)
	v_mfma_scale_f32_16x16x128_f8f6f4 v[94:97], v[18:25], v[204:211], v[94:97], v246, v247 op_sel_hi:[0,0,0]
	v_mfma_scale_f32_16x16x128_f8f6f4 v[90:93], v[26:33], v[204:211], v[90:93], v246, v247 op_sel_hi:[0,0,0]
	v_mfma_scale_f32_16x16x128_f8f6f4 v[78:81], v[18:25], v[212:219], v[78:81], v246, v247 op_sel_hi:[0,0,0]
	v_mfma_scale_f32_16x16x128_f8f6f4 v[74:77], v[26:33], v[212:219], v[74:77], v246, v247 op_sel_hi:[0,0,0]
	v_mfma_scale_f32_16x16x128_f8f6f4 v[62:65], v[18:25], v[220:227], v[62:65], v246, v247 op_sel_hi:[0,0,0]
	v_mfma_scale_f32_16x16x128_f8f6f4 v[58:61], v[26:33], v[220:227], v[58:61], v246, v247 op_sel_hi:[0,0,0]
	v_mfma_scale_f32_16x16x128_f8f6f4 v[46:49], v[18:25], v[228:235], v[46:49], v246, v247 op_sel_hi:[0,0,0]
	v_mfma_scale_f32_16x16x128_f8f6f4 v[42:45], v[26:33], v[228:235], v[42:45], v246, v247 op_sel_hi:[0,0,0]
	s_setprio 0
	s_setprio 1
	v_mfma_scale_f32_16x16x128_f8f6f4 v[86:89], v[2:9], v[204:211], v[86:89], v246, v247 op_sel_hi:[0,0,0]
	v_mfma_scale_f32_16x16x128_f8f6f4 v[82:85], v[10:17], v[204:211], v[82:85], v246, v247 op_sel_hi:[0,0,0]
	v_mfma_scale_f32_16x16x128_f8f6f4 v[70:73], v[2:9], v[212:219], v[70:73], v246, v247 op_sel_hi:[0,0,0]
	v_mfma_scale_f32_16x16x128_f8f6f4 v[66:69], v[10:17], v[212:219], v[66:69], v246, v247 op_sel_hi:[0,0,0]
	v_mfma_scale_f32_16x16x128_f8f6f4 v[54:57], v[2:9], v[220:227], v[54:57], v246, v247 op_sel_hi:[0,0,0]
	v_mfma_scale_f32_16x16x128_f8f6f4 v[50:53], v[10:17], v[220:227], v[50:53], v246, v247 op_sel_hi:[0,0,0]
	v_mfma_scale_f32_16x16x128_f8f6f4 v[38:41], v[2:9], v[228:235], v[38:41], v246, v247 op_sel_hi:[0,0,0]
	v_mfma_scale_f32_16x16x128_f8f6f4 v[34:37], v[10:17], v[228:235], v[34:37], v246, v247 op_sel_hi:[0,0,0]
	s_setprio 2
	s_barrier
; #define PG8_STAGE(bufoff, gbase, voff) do { _Pragma("unroll") for (int _i = 0; _i < 2; ++_i) \
;         __builtin_amdgcn_global_load_lds((const unsigned*)((const char*)(gbase) + (voff)[_i]), (PG8_LAS unsigned*)(lds + (bufoff) + ldsw + _i * 8192), 16, 0, 0); } while (0)
; #define PG8_WAIT_V(n) asm volatile("s_waitcnt vmcnt(" #n ")" ::: "memory")
; #define PG8_WAIT_L(n) asm volatile("s_waitcnt lgkmcnt(" #n ")" ::: "memory")
; #define PG8_BAR __builtin_amdgcn_s_barrier()
; #define PG8_SCHED __builtin_amdgcn_sched_barrier(0)
; template <class Epi, class Sched, bool ALIGN_EPI = false, bool SP2 = false, bool F8 = false>
; __device__ __forceinline__ void gemm_phase(PG8_LAS unsigned char* lds, const Gemm g, const Sched& S, const Epi& E, const int tidb  ) {
;     ...
;             PG8_LDB(B0, 1, 0); PG8_LDB(B1, 1, 1); PG8_SCHED; PG8_LDA(At, 1, 0); PG8_STAGE(PG8_SA(0, 1), a2 + hstep, voffA);
;             PG8_WAIT_V(8); PG8_WAIT_L(0); PG8_BAR; PG8_MMA(0, 0, At, B0); PG8_MMA(0, 1, At, B1); PG8_BAR; PG8_SCHED;
;             PG8_LDA(At, 1, 1); PG8_STAGE(PG8_SB(1, 0), b3, voffB); PG8_STAGE(PG8_SB(1, 1), b3 + hstep, voffB); PG8_STAGE(PG8_SA(1, 0), a3, voffA);
;             PG8_WAIT_V(8); PG8_WAIT_L(0); PG8_BAR; PG8_MMA(1, 0, At, B0); PG8_MMA(1, 1, At, B1); PG8_BAR; PG8_SCHED;
	s_add_i32 s30, 0, 0x18000
	s_add_i32 s31, 0, 0x1c000
	v_add_u32_e32 v14, s30, v192
	v_add_u32_e32 v30, s31, v192
	ds_read_b128 v[2:5], v14
	ds_read_b128 v[6:9], v14 offset:1024
	ds_read_b128 v[10:13], v14 offset:2048
	ds_read_b128 v[14:17], v14 offset:3072
	ds_read_b128 v[18:21], v30
	ds_read_b128 v[22:25], v30 offset:1024
	ds_read_b128 v[26:29], v30 offset:2048
	ds_read_b128 v[30:33], v30 offset:3072
	s_add_u32 s28, s28, s12
	s_addc_u32 s29, s29, s13
	s_mov_b32 m0, s37
	v_lshl_add_u64 v[186:187], s[28:29], 0, v[164:165]
	ds_read_b128 v[204:207], v194 offset:32768
	ds_read_b128 v[208:211], v194 offset:33792
	ds_read_b128 v[212:215], v194 offset:34816
	ds_read_b128 v[216:219], v194 offset:35840
	ds_read_b128 v[220:223], v194 offset:36864
	ds_read_b128 v[224:227], v194 offset:37888
	ds_read_b128 v[228:231], v194 offset:38912
	ds_read_b128 v[232:235], v194 offset:39936
	global_load_lds_dwordx4 v[186:187], off
	v_lshl_add_u64 v[186:187], s[28:29], 0, v[166:167]
	s_mov_b32 m0, s41
	s_nop 0
	global_load_lds_dwordx4 v[186:187], off
	s_waitcnt vmcnt(8)
	s_waitcnt lgkmcnt(0)
	s_barrier
	s_setprio 1
	s_waitcnt lgkmcnt(0)
	v_mfma_scale_f32_16x16x128_f8f6f4 v[158:161], v[2:9], v[204:211], v[158:161], v246, v247 op_sel_hi:[0,0,0]
	v_mfma_scale_f32_16x16x128_f8f6f4 v[154:157], v[10:17], v[204:211], v[154:157], v246, v247 op_sel_hi:[0,0,0]
	v_mfma_scale_f32_16x16x128_f8f6f4 v[142:145], v[2:9], v[212:219], v[142:145], v246, v247 op_sel_hi:[0,0,0]
	v_mfma_scale_f32_16x16x128_f8f6f4 v[138:141], v[10:17], v[212:219], v[138:141], v246, v247 op_sel_hi:[0,0,0]
	v_mfma_scale_f32_16x16x128_f8f6f4 v[126:129], v[2:9], v[220:227], v[126:129], v246, v247 op_sel_hi:[0,0,0]
	v_mfma_scale_f32_16x16x128_f8f6f4 v[122:125], v[10:17], v[220:227], v[122:125], v246, v247 op_sel_hi:[0,0,0]
	v_mfma_scale_f32_16x16x128_f8f6f4 v[110:113], v[2:9], v[228:235], v[110:113], v246, v247 op_sel_hi:[0,0,0]
	v_mfma_scale_f32_16x16x128_f8f6f4 v[106:109], v[10:17], v[228:235], v[106:109], v246, v247 op_sel_hi:[0,0,0]
	s_setprio 0
	s_setprio 1
	v_mfma_scale_f32_16x16x128_f8f6f4 v[150:153], v[18:25], v[204:211], v[150:153], v246, v247 op_sel_hi:[0,0,0]
	v_mfma_scale_f32_16x16x128_f8f6f4 v[146:149], v[26:33], v[204:211], v[146:149], v246, v247 op_sel_hi:[0,0,0]
	v_mfma_scale_f32_16x16x128_f8f6f4 v[134:137], v[18:25], v[212:219], v[134:137], v246, v247 op_sel_hi:[0,0,0]
	v_mfma_scale_f32_16x16x128_f8f6f4 v[130:133], v[26:33], v[212:219], v[130:133], v246, v247 op_sel_hi:[0,0,0]
	v_mfma_scale_f32_16x16x128_f8f6f4 v[118:121], v[18:25], v[220:227], v[118:121], v246, v247 op_sel_hi:[0,0,0]
	v_mfma_scale_f32_16x16x128_f8f6f4 v[114:117], v[26:33], v[220:227], v[114:117], v246, v247 op_sel_hi:[0,0,0]
	v_mfma_scale_f32_16x16x128_f8f6f4 v[102:105], v[18:25], v[228:235], v[102:105], v246, v247 op_sel_hi:[0,0,0]
	v_mfma_scale_f32_16x16x128_f8f6f4 v[98:101], v[26:33], v[228:235], v[98:101], v246, v247 op_sel_hi:[0,0,0]
	s_setprio 2
	s_barrier
	s_add_i32 s28, s30, s0
	v_lshl_add_u64 v[174:175], v[174:175], 0, s[92:93]
	s_mov_b32 m0, s28
	ds_read_b128 v[204:207], v194 offset:49152
	ds_read_b128 v[208:211], v194 offset:50176
	ds_read_b128 v[212:215], v194 offset:51200
	ds_read_b128 v[216:219], v194 offset:52224
	ds_read_b128 v[220:223], v194 offset:53248
	ds_read_b128 v[224:227], v194 offset:54272
	ds_read_b128 v[228:231], v194 offset:55296
	ds_read_b128 v[232:235], v194 offset:56320
	global_load_lds_dwordx4 v[174:175], off
	v_lshl_add_u64 v[174:175], v[176:177], 0, s[92:93]
	s_add_i32 m0, s28, 0x2000
	s_add_i32 s28, s31, s0
	global_load_lds_dwordx4 v[174:175], off
	v_lshl_add_u64 v[174:175], v[178:179], 0, s[92:93]
	s_mov_b32 m0, s28
	s_nop 0
	global_load_lds_dwordx4 v[174:175], off
	v_lshl_add_u64 v[174:175], v[180:181], 0, s[92:93]
	s_add_i32 m0, s28, 0x2000
	s_nop 0
	global_load_lds_dwordx4 v[174:175], off
	v_lshl_add_u64 v[174:175], v[182:183], 0, s[92:93]
	s_mov_b32 m0, s43
	s_nop 0
	global_load_lds_dwordx4 v[174:175], off
	v_lshl_add_u64 v[174:175], v[184:185], 0, s[92:93]
	s_mov_b32 m0, s45
	s_nop 0
	global_load_lds_dwordx4 v[174:175], off
	s_waitcnt vmcnt(8)
	s_waitcnt lgkmcnt(0)
	s_barrier
	s_setprio 1
	s_waitcnt lgkmcnt(0)
	v_mfma_scale_f32_16x16x128_f8f6f4 v[94:97], v[2:9], v[204:211], v[94:97], v246, v247 op_sel_hi:[0,0,0]
	v_mfma_scale_f32_16x16x128_f8f6f4 v[90:93], v[10:17], v[204:211], v[90:93], v246, v247 op_sel_hi:[0,0,0]
	v_mfma_scale_f32_16x16x128_f8f6f4 v[78:81], v[2:9], v[212:219], v[78:81], v246, v247 op_sel_hi:[0,0,0]
	v_mfma_scale_f32_16x16x128_f8f6f4 v[74:77], v[10:17], v[212:219], v[74:77], v246, v247 op_sel_hi:[0,0,0]
	v_mfma_scale_f32_16x16x128_f8f6f4 v[62:65], v[2:9], v[220:227], v[62:65], v246, v247 op_sel_hi:[0,0,0]
	v_mfma_scale_f32_16x16x128_f8f6f4 v[58:61], v[10:17], v[220:227], v[58:61], v246, v247 op_sel_hi:[0,0,0]
	v_mfma_scale_f32_16x16x128_f8f6f4 v[46:49], v[2:9], v[228:235], v[46:49], v246, v247 op_sel_hi:[0,0,0]
	v_mfma_scale_f32_16x16x128_f8f6f4 v[42:45], v[10:17], v[228:235], v[42:45], v246, v247 op_sel_hi:[0,0,0]
	s_setprio 0
	s_setprio 1
	v_mfma_scale_f32_16x16x128_f8f6f4 v[86:89], v[18:25], v[204:211], v[86:89], v246, v247 op_sel_hi:[0,0,0]
	v_mfma_scale_f32_16x16x128_f8f6f4 v[82:85], v[26:33], v[204:211], v[82:85], v246, v247 op_sel_hi:[0,0,0]
	v_mfma_scale_f32_16x16x128_f8f6f4 v[70:73], v[18:25], v[212:219], v[70:73], v246, v247 op_sel_hi:[0,0,0]
	v_mfma_scale_f32_16x16x128_f8f6f4 v[66:69], v[26:33], v[212:219], v[66:69], v246, v247 op_sel_hi:[0,0,0]
	v_mfma_scale_f32_16x16x128_f8f6f4 v[54:57], v[18:25], v[220:227], v[54:57], v246, v247 op_sel_hi:[0,0,0]
	v_mfma_scale_f32_16x16x128_f8f6f4 v[50:53], v[26:33], v[220:227], v[50:53], v246, v247 op_sel_hi:[0,0,0]
	v_mfma_scale_f32_16x16x128_f8f6f4 v[38:41], v[18:25], v[228:235], v[38:41], v246, v247 op_sel_hi:[0,0,0]
	v_mfma_scale_f32_16x16x128_f8f6f4 v[34:37], v[26:33], v[228:235], v[34:37], v246, v247 op_sel_hi:[0,0,0]
	s_setprio 2
	s_barrier
	s_add_u32 s26, s26, 0x100
	s_addc_u32 s27, s27, 0
	s_add_u32 s62, s62, 0x100
	s_addc_u32 s63, s63, 0
	s_cmp_ge_i32 s65, s46
	s_mov_b32 s28, s65
	s_cbranch_scc0 .LBB0_1857
	s_movk_i32 s67, 0x300
